# dead-instruction sweep: 52 redundant lgkmcnt(0) waits after the K-loop barriers and 78 dead zero-inits before fp8 pack pairs in the VALU-bound epilogues removed
# speedup vs baseline: 1.0027x; 1.0027x over previous
; #define PG8_STAGE(bufoff, gbase, voff) do { _Pragma("unroll") for (int _i = 0; _i < 2; ++_i) \
;         __builtin_amdgcn_global_load_lds((const unsigned*)((const char*)(gbase) + (voff)[_i]), (PG8_LAS unsigned*)(lds + (bufoff) + ldsw + _i * 8192), 16, 0, 0); } while (0)
; #define PG8_WAIT_V(n) asm volatile("s_waitcnt vmcnt(" #n ")" ::: "memory")
; #define PG8_WAIT_L(n) asm volatile("s_waitcnt lgkmcnt(" #n ")" ::: "memory")
; #define PG8_BAR __builtin_amdgcn_s_barrier()
; #define PG8_SCHED __builtin_amdgcn_sched_barrier(0)
; template <class Epi, class Sched, bool ALIGN_EPI = false, bool SP2 = false, bool FP8 = false, bool PEEL = false>
; __device__ __forceinline__ void gemm_phase(PG8_LAS unsigned char* lds, const Gemm g, const Sched& S, const Epi& E, const int wid) {
;     ...
;         const char* nA = has_next ? (const char*)g.A + (size_t)nxt.pm * tstep + nxt.koff : cA; const char* nB = has_next ? (const char*)g.Bt + (size_t)nxt.pn * tstep + nxt.koff : cB;
;         if constexpr (SP2 && PEEL) {
;         {
;             const int t = 0;
;             const bool last = (t == nt - 2);
;             const char* a1 = cA + (size_t)(t + 1) * kstep;
;             const char* a2 = last ? nA : cA + (size_t)(t + 2) * kstep; const char* b2 = last ? nB : cB + (size_t)(t + 2) * kstep;
;             const char* a3 = a2 + kstep; const char* b3 = b2 + kstep;
;             if (last && has_next) S.a_ready(nxt);
;             PG8_LDB(B0, 0, 0); PG8_LDB(B1, 0, 1); PG8_SCHED; PG8_LDA(At, 0, 0); PG8_STAGE(PG8_SA(1, 1), a1 + hstep, voffA);
;             PG8_WAIT_V(8); PG8_WAIT_L(0); PG8_BAR; PG8_MMAZ(0, 0, At, B0); PG8_MMAZ(0, 1, At, B1); PG8_BAR; PG8_SCHED;
;             PG8_LDA(At, 0, 1); PG8_STAGE(PG8_SB(0, 0), b2, voffB); PG8_STAGE(PG8_SB(0, 1), b2 + hstep, voffB); PG8_STAGE(PG8_SA(0, 0), a2, voffA);
;             PG8_WAIT_V(8); PG8_WAIT_L(0); PG8_BAR; PG8_MMAZ(1, 0, At, B0); PG8_MMAZ(1, 1, At, B1); PG8_BAR; PG8_SCHED;
.LBB0_236:
	s_ashr_i32 s23, s22, 31
	s_lshl_b64 s[24:25], s[22:23], 19
	s_add_u32 s24, s34, s24
	ds_read_b128 v[0:3], v153
	ds_read_b128 v[4:7], v153 offset:1024
	ds_read_b128 v[8:11], v153 offset:2048
	ds_read_b128 v[12:15], v153 offset:3072
	ds_read_b128 v[16:19], v154
	ds_read_b128 v[20:23], v154 offset:1024
	ds_read_b128 v[24:27], v154 offset:2048
	ds_read_b128 v[28:31], v154 offset:3072
	s_addc_u32 s25, s35, s25
	s_ashr_i32 s21, s20, 31
	s_lshl_b64 s[26:27], s[20:21], 19
	s_add_u32 s26, s42, s26
	s_addc_u32 s27, s43, s27
	s_and_b64 s[40:41], s[10:11], exec
	s_cselect_b32 s13, s25, s37
	s_cselect_b32 s21, s24, s36
	s_cselect_b32 s23, s27, s31
	s_cselect_b32 s60, s26, s30
	s_add_u32 s40, s36, 0x40080
	s_addc_u32 s41, s37, 0
	s_add_i32 s61, s44, 0xc000
	v_lshl_add_u64 v[64:65], s[40:41], 0, v[128:129]
	s_mov_b32 m0, s61
	s_add_i32 s62, s44, 0xe000
	ds_read_b128 v[32:35], v155
	ds_read_b128 v[36:39], v155 offset:1024
	ds_read_b128 v[40:43], v155 offset:2048
	ds_read_b128 v[44:47], v155 offset:3072
	ds_read_b128 v[48:51], v155 offset:4096
	ds_read_b128 v[52:55], v155 offset:5120
	ds_read_b128 v[56:59], v155 offset:6144
	ds_read_b128 v[60:63], v155 offset:7168
	global_load_lds_dwordx4 v[64:65], off
	v_lshl_add_u64 v[64:65], s[40:41], 0, v[132:133]
	s_mov_b32 m0, s62
	s_nop 0
	global_load_lds_dwordx4 v[64:65], off
	s_waitcnt vmcnt(8)
	s_waitcnt lgkmcnt(0)
	s_barrier
	s_setprio 1
	v_mfma_f32_16x16x32_bf16 v[88:91], v[0:3], v[56:59], 0
	v_mfma_f32_16x16x32_bf16 v[64:67], v[0:3], v[32:35], 0
	v_mfma_f32_16x16x32_bf16 v[68:71], v[8:11], v[32:35], 0
	v_mfma_f32_16x16x32_bf16 v[72:75], v[0:3], v[40:43], 0
	v_mfma_f32_16x16x32_bf16 v[76:79], v[8:11], v[40:43], 0
	v_mfma_f32_16x16x32_bf16 v[80:83], v[0:3], v[48:51], 0
	v_mfma_f32_16x16x32_bf16 v[84:87], v[8:11], v[48:51], 0
	v_mfma_f32_16x16x32_bf16 v[96:99], v[4:7], v[60:63], v[88:91]
	v_mfma_f32_16x16x32_bf16 v[88:91], v[8:11], v[56:59], 0
	v_mfma_f32_16x16x32_bf16 v[64:67], v[4:7], v[36:39], v[64:67]
	v_mfma_f32_16x16x32_bf16 v[68:71], v[12:15], v[36:39], v[68:71]
	v_mfma_f32_16x16x32_bf16 v[72:75], v[4:7], v[44:47], v[72:75]
	v_mfma_f32_16x16x32_bf16 v[76:79], v[12:15], v[44:47], v[76:79]
	v_mfma_f32_16x16x32_bf16 v[80:83], v[4:7], v[52:55], v[80:83]
	v_mfma_f32_16x16x32_bf16 v[84:87], v[12:15], v[52:55], v[84:87]
	v_mfma_f32_16x16x32_bf16 v[100:103], v[12:15], v[60:63], v[88:91]
	s_setprio 0
	s_setprio 1
	v_mfma_f32_16x16x32_bf16 v[88:91], v[16:19], v[32:35], 0
	v_mfma_f32_16x16x32_bf16 v[32:35], v[24:27], v[32:35], 0
	v_mfma_f32_16x16x32_bf16 v[112:115], v[20:23], v[36:39], v[88:91]
	v_mfma_f32_16x16x32_bf16 v[32:35], v[28:31], v[36:39], v[32:35]
	v_mfma_f32_16x16x32_bf16 v[36:39], v[16:19], v[40:43], 0
	v_mfma_f32_16x16x32_bf16 v[40:43], v[24:27], v[40:43], 0
	v_mfma_f32_16x16x32_bf16 v[36:39], v[20:23], v[44:47], v[36:39]
	v_mfma_f32_16x16x32_bf16 v[40:43], v[28:31], v[44:47], v[40:43]
	v_mfma_f32_16x16x32_bf16 v[44:47], v[16:19], v[48:51], 0
	v_mfma_f32_16x16x32_bf16 v[48:51], v[24:27], v[48:51], 0
	v_mfma_f32_16x16x32_bf16 v[44:47], v[20:23], v[52:55], v[44:47]
	v_mfma_f32_16x16x32_bf16 v[48:51], v[28:31], v[52:55], v[48:51]
	v_mfma_f32_16x16x32_bf16 v[52:55], v[16:19], v[56:59], 0
	v_mfma_f32_16x16x32_bf16 v[56:59], v[24:27], v[56:59], 0
	v_mfma_f32_16x16x32_bf16 v[52:55], v[20:23], v[60:63], v[52:55]
	v_mfma_f32_16x16x32_bf16 v[56:59], v[28:31], v[60:63], v[56:59]
	s_setprio 0
	s_barrier
	s_add_i32 s63, s56, s3
	v_lshl_add_u64 v[250:251], s[30:31], 0, v[130:131]
	s_add_i32 s64, s63, 0x2000
	v_lshl_add_u64 v[144:145], v[250:251], 0, s[16:17]
	s_mov_b32 m0, s63
	v_lshl_add_u64 v[252:253], s[30:31], 0, v[134:135]
	s_add_u32 s40, s30, 0x40100
	ds_read_b128 v[60:63], v155 offset:16384
	ds_read_b128 v[88:91], v155 offset:17408
	ds_read_b128 v[92:95], v155 offset:18432
	ds_read_b128 v[104:107], v155 offset:19456
	ds_read_b128 v[108:111], v155 offset:20480
	ds_read_b128 v[116:119], v155 offset:21504
	ds_read_b128 v[120:123], v155 offset:22528
	ds_read_b128 v[124:127], v155 offset:23552
	global_load_lds_dwordx4 v[144:145], off
	v_lshl_add_u64 v[144:145], v[252:253], 0, s[16:17]
	s_mov_b32 m0, s64
	s_addc_u32 s41, s31, 0
	s_add_i32 s65, s57, s3
	global_load_lds_dwordx4 v[144:145], off
	v_lshl_add_u64 v[144:145], s[40:41], 0, v[130:131]
	s_mov_b32 m0, s65
	s_add_i32 s66, s65, 0x2000
	global_load_lds_dwordx4 v[144:145], off
	v_lshl_add_u64 v[144:145], s[40:41], 0, v[134:135]
	s_mov_b32 m0, s66
	v_lshl_add_u64 v[140:141], s[36:37], 0, v[128:129]
	global_load_lds_dwordx4 v[144:145], off
	v_lshl_add_u64 v[144:145], v[140:141], 0, s[16:17]
	s_mov_b32 m0, s44
	v_lshl_add_u64 v[142:143], s[36:37], 0, v[132:133]
	global_load_lds_dwordx4 v[144:145], off
	v_lshl_add_u64 v[144:145], v[142:143], 0, s[16:17]
	s_mov_b32 m0, s45
	s_nop 0
	global_load_lds_dwordx4 v[144:145], off
	s_waitcnt vmcnt(8)
	s_waitcnt lgkmcnt(0)
	s_barrier
; #define PG8_STAGE(bufoff, gbase, voff) do { _Pragma("unroll") for (int _i = 0; _i < 2; ++_i) \
;         __builtin_amdgcn_global_load_lds((const unsigned*)((const char*)(gbase) + (voff)[_i]), (PG8_LAS unsigned*)(lds + (bufoff) + ldsw + _i * 8192), 16, 0, 0); } while (0)
; #define PG8_WAIT_V(n) asm volatile("s_waitcnt vmcnt(" #n ")" ::: "memory")
; #define PG8_WAIT_L(n) asm volatile("s_waitcnt lgkmcnt(" #n ")" ::: "memory")
; #define PG8_BAR __builtin_amdgcn_s_barrier()
; #define PG8_SCHED __builtin_amdgcn_sched_barrier(0)
; template <class Epi, class Sched, bool ALIGN_EPI = false, bool SP2 = false, bool FP8 = false, bool PEEL = false>
; __device__ __forceinline__ void gemm_phase(PG8_LAS unsigned char* lds, const Gemm g, const Sched& S, const Epi& E, const int wid) {
;     ...
;             PG8_WAIT_V(8); PG8_WAIT_L(0); PG8_BAR; PG8_MMAZ(1, 0, At, B0); PG8_MMAZ(1, 1, At, B1); PG8_BAR; PG8_SCHED;
;             PG8_LDB(B0, 1, 0); PG8_LDB(B1, 1, 1); PG8_SCHED; PG8_LDA(At, 1, 0); PG8_STAGE(PG8_SA(0, 1), a2 + hstep, voffA);
;             PG8_WAIT_V(8); PG8_WAIT_L(0); PG8_BAR; PG8_MMA(0, 0, At, B0); PG8_MMA(0, 1, At, B1); PG8_BAR; PG8_SCHED;
	s_setprio 1
	v_mfma_f32_16x16x32_bf16 v[144:147], v[0:3], v[60:63], 0
	v_mfma_f32_16x16x32_bf16 v[162:165], v[0:3], v[92:95], 0
	v_mfma_f32_16x16x32_bf16 v[170:173], v[0:3], v[108:111], 0
	v_mfma_f32_16x16x32_bf16 v[0:3], v[0:3], v[120:123], 0
	v_mfma_f32_16x16x32_bf16 v[146:149], v[4:7], v[88:91], v[144:147]
	v_mfma_f32_16x16x32_bf16 v[162:165], v[4:7], v[104:107], v[162:165]
	v_mfma_f32_16x16x32_bf16 v[170:173], v[4:7], v[116:119], v[170:173]
	v_mfma_f32_16x16x32_bf16 v[0:3], v[4:7], v[124:127], v[0:3]
	v_mfma_f32_16x16x32_bf16 v[4:7], v[8:11], v[120:123], 0
	v_mfma_f32_16x16x32_bf16 v[158:161], v[8:11], v[60:63], 0
	v_mfma_f32_16x16x32_bf16 v[166:169], v[8:11], v[92:95], 0
	v_mfma_f32_16x16x32_bf16 v[174:177], v[8:11], v[108:111], 0
	v_mfma_f32_16x16x32_bf16 v[4:7], v[12:15], v[124:127], v[4:7]
	v_mfma_f32_16x16x32_bf16 v[158:161], v[12:15], v[88:91], v[158:161]
	v_mfma_f32_16x16x32_bf16 v[166:169], v[12:15], v[104:107], v[166:169]
	v_mfma_f32_16x16x32_bf16 v[174:177], v[12:15], v[116:119], v[174:177]
	s_setprio 0
	s_setprio 1
	v_mfma_f32_16x16x32_bf16 v[8:11], v[16:19], v[60:63], 0
	v_mfma_f32_16x16x32_bf16 v[178:181], v[20:23], v[88:91], v[8:11]
	v_mfma_f32_16x16x32_bf16 v[8:11], v[24:27], v[60:63], 0
	v_mfma_f32_16x16x32_bf16 v[182:185], v[28:31], v[88:91], v[8:11]
	v_mfma_f32_16x16x32_bf16 v[8:11], v[16:19], v[92:95], 0
	v_mfma_f32_16x16x32_bf16 v[186:189], v[20:23], v[104:107], v[8:11]
	v_mfma_f32_16x16x32_bf16 v[8:11], v[24:27], v[92:95], 0
	v_mfma_f32_16x16x32_bf16 v[190:193], v[28:31], v[104:107], v[8:11]
	v_mfma_f32_16x16x32_bf16 v[8:11], v[16:19], v[108:111], 0
	v_mfma_f32_16x16x32_bf16 v[194:197], v[20:23], v[116:119], v[8:11]
	v_mfma_f32_16x16x32_bf16 v[8:11], v[24:27], v[108:111], 0
	v_mfma_f32_16x16x32_bf16 v[198:201], v[28:31], v[116:119], v[8:11]
	v_mfma_f32_16x16x32_bf16 v[8:11], v[16:19], v[120:123], 0
	v_mfma_f32_16x16x32_bf16 v[202:205], v[20:23], v[124:127], v[8:11]
	v_mfma_f32_16x16x32_bf16 v[8:11], v[24:27], v[120:123], 0
	v_mfma_f32_16x16x32_bf16 v[206:209], v[28:31], v[124:127], v[8:11]
	s_setprio 0
	s_barrier
	s_add_i32 s67, 0, 0x18000
	s_add_i32 s84, 0, 0x1c000
	v_add_u32_e32 v144, s67, v151
	v_add_u32_e32 v145, s84, v151
	s_nop 0
	ds_read_b128 v[8:11], v144
	ds_read_b128 v[12:15], v144 offset:1024
	ds_read_b128 v[16:19], v144 offset:2048
	ds_read_b128 v[20:23], v144 offset:3072
	ds_read_b128 v[210:213], v145
	ds_read_b128 v[214:217], v145 offset:1024
	ds_read_b128 v[218:221], v145 offset:2048
	ds_read_b128 v[222:225], v145 offset:3072
	s_add_u32 s40, s36, 0x40100
	s_addc_u32 s41, s37, 0
	s_mov_b32 m0, s46
	v_lshl_add_u64 v[88:89], s[40:41], 0, v[128:129]
	ds_read_b128 v[24:27], v155 offset:32768
	ds_read_b128 v[28:31], v155 offset:33792
	ds_read_b128 v[60:63], v155 offset:34816
	ds_read_b128 v[226:229], v155 offset:35840
	ds_read_b128 v[230:233], v155 offset:36864
	ds_read_b128 v[234:237], v155 offset:37888
	ds_read_b128 v[238:241], v155 offset:38912
	ds_read_b128 v[242:245], v155 offset:39936
	global_load_lds_dwordx4 v[88:89], off
	v_lshl_add_u64 v[88:89], s[40:41], 0, v[132:133]
	s_mov_b32 m0, s47
	s_nop 0
	global_load_lds_dwordx4 v[88:89], off
	s_waitcnt vmcnt(8)
	s_waitcnt lgkmcnt(0)
	s_barrier
	s_setprio 1
	v_mfma_f32_16x16x32_bf16 v[64:67], v[8:11], v[24:27], v[64:67]
	v_mfma_f32_16x16x32_bf16 v[124:127], v[12:15], v[28:31], v[64:67]
	v_mfma_f32_16x16x32_bf16 v[64:67], v[16:19], v[24:27], v[68:71]
	v_mfma_f32_16x16x32_bf16 v[120:123], v[20:23], v[28:31], v[64:67]
	v_mfma_f32_16x16x32_bf16 v[64:67], v[8:11], v[60:63], v[72:75]
	v_mfma_f32_16x16x32_bf16 v[108:111], v[12:15], v[226:229], v[64:67]
	v_mfma_f32_16x16x32_bf16 v[64:67], v[16:19], v[60:63], v[76:79]
	v_mfma_f32_16x16x32_bf16 v[104:107], v[20:23], v[226:229], v[64:67]
	v_mfma_f32_16x16x32_bf16 v[64:67], v[8:11], v[230:233], v[80:83]
	v_mfma_f32_16x16x32_bf16 v[92:95], v[12:15], v[234:237], v[64:67]
	v_mfma_f32_16x16x32_bf16 v[64:67], v[16:19], v[230:233], v[84:87]
	v_mfma_f32_16x16x32_bf16 v[88:91], v[20:23], v[234:237], v[64:67]
	v_mfma_f32_16x16x32_bf16 v[64:67], v[8:11], v[238:241], v[96:99]
	v_mfma_f32_16x16x32_bf16 v[76:79], v[12:15], v[242:245], v[64:67]
	v_mfma_f32_16x16x32_bf16 v[64:67], v[16:19], v[238:241], v[100:103]
	v_mfma_f32_16x16x32_bf16 v[72:75], v[20:23], v[242:245], v[64:67]
	s_setprio 0
	s_setprio 1
	v_mfma_f32_16x16x32_bf16 v[64:67], v[210:213], v[24:27], v[112:115]
	v_mfma_f32_16x16x32_bf16 v[24:27], v[218:221], v[24:27], v[32:35]
	v_mfma_f32_16x16x32_bf16 v[112:115], v[222:225], v[28:31], v[24:27]
	v_mfma_f32_16x16x32_bf16 v[24:27], v[210:213], v[60:63], v[36:39]
	v_mfma_f32_16x16x32_bf16 v[100:103], v[214:217], v[226:229], v[24:27]
	v_mfma_f32_16x16x32_bf16 v[24:27], v[218:221], v[60:63], v[40:43]
	v_mfma_f32_16x16x32_bf16 v[96:99], v[222:225], v[226:229], v[24:27]
	v_mfma_f32_16x16x32_bf16 v[24:27], v[210:213], v[230:233], v[44:47]
	v_mfma_f32_16x16x32_bf16 v[84:87], v[214:217], v[234:237], v[24:27]
	v_mfma_f32_16x16x32_bf16 v[24:27], v[218:221], v[230:233], v[48:51]
	v_mfma_f32_16x16x32_bf16 v[80:83], v[222:225], v[234:237], v[24:27]
	v_mfma_f32_16x16x32_bf16 v[24:27], v[210:213], v[238:241], v[52:55]
	v_mfma_f32_16x16x32_bf16 v[68:71], v[214:217], v[242:245], v[24:27]
	v_mfma_f32_16x16x32_bf16 v[24:27], v[218:221], v[238:241], v[56:59]
	v_mfma_f32_16x16x32_bf16 v[116:119], v[214:217], v[28:31], v[64:67]
	v_mfma_f32_16x16x32_bf16 v[64:67], v[222:225], v[242:245], v[24:27]
	s_setprio 0
	s_barrier
; #define PG8_STAGE(bufoff, gbase, voff) do { _Pragma("unroll") for (int _i = 0; _i < 2; ++_i) \
;         __builtin_amdgcn_global_load_lds((const unsigned*)((const char*)(gbase) + (voff)[_i]), (PG8_LAS unsigned*)(lds + (bufoff) + ldsw + _i * 8192), 16, 0, 0); } while (0)
; #define PG8_WAIT_V(n) asm volatile("s_waitcnt vmcnt(" #n ")" ::: "memory")
; #define PG8_WAIT_L(n) asm volatile("s_waitcnt lgkmcnt(" #n ")" ::: "memory")
; #define PG8_BAR __builtin_amdgcn_s_barrier()
; #define PG8_SCHED __builtin_amdgcn_sched_barrier(0)
; template <class Epi, class Sched, bool ALIGN_EPI = false, bool SP2 = false, bool FP8 = false, bool PEEL = false>
; __device__ __forceinline__ void gemm_phase(PG8_LAS unsigned char* lds, const Gemm g, const Sched& S, const Epi& E, const int wid) {
;     ...
;             PG8_LDA(At, 1, 1); PG8_STAGE(PG8_SB(1, 0), b3, voffB); PG8_STAGE(PG8_SB(1, 1), b3 + hstep, voffB); PG8_STAGE(PG8_SA(1, 0), a3, voffA);
;             PG8_WAIT_V(8); PG8_WAIT_L(0); PG8_BAR; PG8_MMA(1, 0, At, B0); PG8_MMA(1, 1, At, B1); PG8_BAR; PG8_SCHED;
;         }
; #pragma unroll 1
;         for (int t = 2; t < nt; t += 2) {
;             const bool last = (t == nt - 2);
;             const char* a1 = cA + (size_t)(t + 1) * kstep;
;             const char* a2 = last ? nA : cA + (size_t)(t + 2) * kstep; const char* b2 = last ? nB : cB + (size_t)(t + 2) * kstep;
;             const char* a3 = a2 + kstep; const char* b3 = b2 + kstep;
;             if (last && has_next) S.a_ready(nxt);
;             PG8_LDB(B0, 0, 0); PG8_LDB(B1, 0, 1); PG8_SCHED; PG8_LDA(At, 0, 0); PG8_STAGE(PG8_SA(1, 1), a1 + hstep, voffA);
	s_add_i32 s67, s67, s3
	s_add_i32 s75, s67, 0x2000
	s_nop 1
	v_lshl_add_u64 v[24:25], v[250:251], 0, s[18:19]
	s_mov_b32 m0, s67
	s_add_u32 s40, s30, 0x40180
	ds_read_b128 v[32:35], v155 offset:49152
	ds_read_b128 v[36:39], v155 offset:50176
	ds_read_b128 v[226:229], v155 offset:51200
	ds_read_b128 v[230:233], v155 offset:52224
	ds_read_b128 v[234:237], v155 offset:53248
	ds_read_b128 v[238:241], v155 offset:54272
	ds_read_b128 v[242:245], v155 offset:55296
	ds_read_b128 v[246:249], v155 offset:56320
	global_load_lds_dwordx4 v[24:25], off
	v_lshl_add_u64 v[24:25], v[252:253], 0, s[18:19]
	s_mov_b32 m0, s75
	s_addc_u32 s41, s31, 0
	s_add_i32 s84, s84, s3
	global_load_lds_dwordx4 v[24:25], off
	v_lshl_add_u64 v[24:25], s[40:41], 0, v[130:131]
	s_mov_b32 m0, s84
	s_add_i32 s85, s84, 0x2000
	global_load_lds_dwordx4 v[24:25], off
	v_lshl_add_u64 v[24:25], s[40:41], 0, v[134:135]
	s_mov_b32 m0, s85
	s_nop 0
	global_load_lds_dwordx4 v[24:25], off
	v_lshl_add_u64 v[24:25], v[140:141], 0, s[18:19]
	s_mov_b32 m0, s54
	s_nop 0
	global_load_lds_dwordx4 v[24:25], off
	v_lshl_add_u64 v[24:25], v[142:143], 0, s[18:19]
	s_mov_b32 m0, s55
	s_nop 0
	global_load_lds_dwordx4 v[24:25], off
	s_waitcnt vmcnt(8)
	s_waitcnt lgkmcnt(0)
	s_barrier
	s_setprio 1
	v_mfma_f32_16x16x32_bf16 v[24:27], v[8:11], v[32:35], v[146:149]
	v_mfma_f32_16x16x32_bf16 v[60:63], v[12:15], v[36:39], v[24:27]
	v_mfma_f32_16x16x32_bf16 v[24:27], v[16:19], v[32:35], v[158:161]
	v_mfma_f32_16x16x32_bf16 v[56:59], v[20:23], v[36:39], v[24:27]
	v_mfma_f32_16x16x32_bf16 v[24:27], v[8:11], v[226:229], v[162:165]
	v_mfma_f32_16x16x32_bf16 v[44:47], v[12:15], v[230:233], v[24:27]
	v_mfma_f32_16x16x32_bf16 v[24:27], v[16:19], v[226:229], v[166:169]
	v_mfma_f32_16x16x32_bf16 v[40:43], v[20:23], v[230:233], v[24:27]
	v_mfma_f32_16x16x32_bf16 v[24:27], v[8:11], v[234:237], v[170:173]
	v_mfma_f32_16x16x32_bf16 v[0:3], v[8:11], v[242:245], v[0:3]
	v_mfma_f32_16x16x32_bf16 v[28:31], v[12:15], v[238:241], v[24:27]
	v_mfma_f32_16x16x32_bf16 v[24:27], v[16:19], v[234:237], v[174:177]
	v_mfma_f32_16x16x32_bf16 v[12:15], v[12:15], v[246:249], v[0:3]
	v_mfma_f32_16x16x32_bf16 v[0:3], v[16:19], v[242:245], v[4:7]
	v_mfma_f32_16x16x32_bf16 v[24:27], v[20:23], v[238:241], v[24:27]
	v_mfma_f32_16x16x32_bf16 v[8:11], v[20:23], v[246:249], v[0:3]
	s_setprio 0
	s_setprio 1
	v_mfma_f32_16x16x32_bf16 v[0:3], v[210:213], v[32:35], v[178:181]
	v_mfma_f32_16x16x32_bf16 v[52:55], v[214:217], v[36:39], v[0:3]
	v_mfma_f32_16x16x32_bf16 v[0:3], v[218:221], v[32:35], v[182:185]
	v_mfma_f32_16x16x32_bf16 v[48:51], v[222:225], v[36:39], v[0:3]
	v_mfma_f32_16x16x32_bf16 v[0:3], v[210:213], v[226:229], v[186:189]
	v_mfma_f32_16x16x32_bf16 v[36:39], v[214:217], v[230:233], v[0:3]
	v_mfma_f32_16x16x32_bf16 v[0:3], v[218:221], v[226:229], v[190:193]
	v_mfma_f32_16x16x32_bf16 v[32:35], v[222:225], v[230:233], v[0:3]
	v_mfma_f32_16x16x32_bf16 v[0:3], v[210:213], v[234:237], v[194:197]
	v_mfma_f32_16x16x32_bf16 v[20:23], v[214:217], v[238:241], v[0:3]
	v_mfma_f32_16x16x32_bf16 v[0:3], v[218:221], v[234:237], v[198:201]
	v_mfma_f32_16x16x32_bf16 v[16:19], v[222:225], v[238:241], v[0:3]
	v_mfma_f32_16x16x32_bf16 v[0:3], v[210:213], v[242:245], v[202:205]
	v_mfma_f32_16x16x32_bf16 v[4:7], v[214:217], v[246:249], v[0:3]
	v_mfma_f32_16x16x32_bf16 v[0:3], v[218:221], v[242:245], v[206:209]
	v_mfma_f32_16x16x32_bf16 v[0:3], v[222:225], v[246:249], v[0:3]
	s_setprio 0
	s_barrier
	s_add_u32 s36, s36, 0x40180
	s_addc_u32 s37, s37, 0
	s_add_u32 s88, s30, 0x200
	s_addc_u32 s89, s31, 0
	s_mov_b32 s90, 0
.LBB0_237:
	ds_read_b128 v[146:149], v153
	ds_read_b128 v[158:161], v153 offset:1024
	ds_read_b128 v[162:165], v153 offset:2048
	ds_read_b128 v[166:169], v153 offset:3072
	ds_read_b128 v[170:173], v154
	ds_read_b128 v[174:177], v154 offset:1024
	ds_read_b128 v[178:181], v154 offset:2048
	ds_read_b128 v[182:185], v154 offset:3072
	s_add_u32 s30, s36, 0xfffc0080
	s_addc_u32 s31, s37, -1
	s_cmp_eq_u32 s90, 12
	s_cselect_b32 s41, s13, s31
	s_cselect_b32 s40, s21, s30
	s_cselect_b32 s31, s23, s89
	s_cselect_b32 s30, s60, s88
	s_mov_b32 m0, s61
	v_lshl_add_u64 v[140:141], s[36:37], 0, v[136:137]
	ds_read_b128 v[186:189], v155
	ds_read_b128 v[190:193], v155 offset:1024
	ds_read_b128 v[194:197], v155 offset:2048
	ds_read_b128 v[198:201], v155 offset:3072
	ds_read_b128 v[202:205], v155 offset:4096
	ds_read_b128 v[206:209], v155 offset:5120
	ds_read_b128 v[210:213], v155 offset:6144
	ds_read_b128 v[214:217], v155 offset:7168
	global_load_lds_dwordx4 v[140:141], off
	v_lshl_add_u64 v[140:141], s[36:37], 0, v[138:139]
	s_mov_b32 m0, s62
	s_nop 0
	global_load_lds_dwordx4 v[140:141], off
	s_waitcnt vmcnt(8)
	s_waitcnt lgkmcnt(0)
	s_barrier
; #define PG8_STAGE(bufoff, gbase, voff) do { _Pragma("unroll") for (int _i = 0; _i < 2; ++_i) \
;         __builtin_amdgcn_global_load_lds((const unsigned*)((const char*)(gbase) + (voff)[_i]), (PG8_LAS unsigned*)(lds + (bufoff) + ldsw + _i * 8192), 16, 0, 0); } while (0)
; #define PG8_WAIT_V(n) asm volatile("s_waitcnt vmcnt(" #n ")" ::: "memory")
; #define PG8_WAIT_L(n) asm volatile("s_waitcnt lgkmcnt(" #n ")" ::: "memory")
; #define PG8_BAR __builtin_amdgcn_s_barrier()
; #define PG8_SCHED __builtin_amdgcn_sched_barrier(0)
; template <class Epi, class Sched, bool ALIGN_EPI = false, bool SP2 = false, bool FP8 = false, bool PEEL = false>
; __device__ __forceinline__ void gemm_phase(PG8_LAS unsigned char* lds, const Gemm g, const Sched& S, const Epi& E, const int wid) {
;     ...
;             PG8_WAIT_V(8); PG8_WAIT_L(0); PG8_BAR; PG8_MMA(0, 0, At, B0); PG8_MMA(0, 1, At, B1); PG8_BAR; PG8_SCHED;
;             PG8_LDA(At, 0, 1); PG8_STAGE(PG8_SB(0, 0), b2, voffB); PG8_STAGE(PG8_SB(0, 1), b2 + hstep, voffB); PG8_STAGE(PG8_SA(0, 0), a2, voffA);
;             PG8_WAIT_V(8); PG8_WAIT_L(0); PG8_BAR; PG8_MMA(1, 0, At, B0); PG8_MMA(1, 1, At, B1); PG8_BAR; PG8_SCHED;
	s_setprio 1
	v_mfma_f32_16x16x32_bf16 v[124:127], v[146:149], v[186:189], v[124:127]
	v_mfma_f32_16x16x32_bf16 v[120:123], v[162:165], v[186:189], v[120:123]
	v_mfma_f32_16x16x32_bf16 v[108:111], v[146:149], v[194:197], v[108:111]
	v_mfma_f32_16x16x32_bf16 v[104:107], v[162:165], v[194:197], v[104:107]
	v_mfma_f32_16x16x32_bf16 v[92:95], v[146:149], v[202:205], v[92:95]
	v_mfma_f32_16x16x32_bf16 v[88:91], v[162:165], v[202:205], v[88:91]
	v_mfma_f32_16x16x32_bf16 v[76:79], v[146:149], v[210:213], v[76:79]
	v_mfma_f32_16x16x32_bf16 v[72:75], v[162:165], v[210:213], v[72:75]
	v_mfma_f32_16x16x32_bf16 v[124:127], v[158:161], v[190:193], v[124:127]
	v_mfma_f32_16x16x32_bf16 v[120:123], v[166:169], v[190:193], v[120:123]
	v_mfma_f32_16x16x32_bf16 v[108:111], v[158:161], v[198:201], v[108:111]
	v_mfma_f32_16x16x32_bf16 v[104:107], v[166:169], v[198:201], v[104:107]
	v_mfma_f32_16x16x32_bf16 v[92:95], v[158:161], v[206:209], v[92:95]
	v_mfma_f32_16x16x32_bf16 v[88:91], v[166:169], v[206:209], v[88:91]
	v_mfma_f32_16x16x32_bf16 v[76:79], v[158:161], v[214:217], v[76:79]
	v_mfma_f32_16x16x32_bf16 v[72:75], v[166:169], v[214:217], v[72:75]
	s_setprio 0
	s_setprio 1
	v_mfma_f32_16x16x32_bf16 v[116:119], v[170:173], v[186:189], v[116:119]
	v_mfma_f32_16x16x32_bf16 v[112:115], v[178:181], v[186:189], v[112:115]
	v_mfma_f32_16x16x32_bf16 v[100:103], v[170:173], v[194:197], v[100:103]
	v_mfma_f32_16x16x32_bf16 v[96:99], v[178:181], v[194:197], v[96:99]
	v_mfma_f32_16x16x32_bf16 v[84:87], v[170:173], v[202:205], v[84:87]
	v_mfma_f32_16x16x32_bf16 v[80:83], v[178:181], v[202:205], v[80:83]
	v_mfma_f32_16x16x32_bf16 v[68:71], v[170:173], v[210:213], v[68:71]
	v_mfma_f32_16x16x32_bf16 v[64:67], v[178:181], v[210:213], v[64:67]
	v_mfma_f32_16x16x32_bf16 v[116:119], v[174:177], v[190:193], v[116:119]
	v_mfma_f32_16x16x32_bf16 v[112:115], v[182:185], v[190:193], v[112:115]
	v_mfma_f32_16x16x32_bf16 v[100:103], v[174:177], v[198:201], v[100:103]
	v_mfma_f32_16x16x32_bf16 v[96:99], v[182:185], v[198:201], v[96:99]
	v_mfma_f32_16x16x32_bf16 v[84:87], v[174:177], v[206:209], v[84:87]
	v_mfma_f32_16x16x32_bf16 v[80:83], v[182:185], v[206:209], v[80:83]
	v_mfma_f32_16x16x32_bf16 v[68:71], v[174:177], v[214:217], v[68:71]
	v_mfma_f32_16x16x32_bf16 v[64:67], v[182:185], v[214:217], v[64:67]
	s_setprio 0
	s_barrier
	s_mov_b32 m0, s63
	v_lshl_add_u64 v[140:141], s[30:31], 0, v[130:131]
	s_add_u32 s92, s30, 0x40000
	ds_read_b128 v[186:189], v155 offset:16384
	ds_read_b128 v[190:193], v155 offset:17408
	ds_read_b128 v[194:197], v155 offset:18432
	ds_read_b128 v[198:201], v155 offset:19456
	ds_read_b128 v[202:205], v155 offset:20480
	ds_read_b128 v[206:209], v155 offset:21504
	ds_read_b128 v[210:213], v155 offset:22528
	ds_read_b128 v[214:217], v155 offset:23552
	global_load_lds_dwordx4 v[140:141], off
	v_lshl_add_u64 v[142:143], s[30:31], 0, v[134:135]
	s_mov_b32 m0, s64
	s_addc_u32 s93, s31, 0
	global_load_lds_dwordx4 v[142:143], off
	v_lshl_add_u64 v[218:219], s[92:93], 0, v[130:131]
	s_mov_b32 m0, s65
	v_lshl_add_u64 v[220:221], s[40:41], 0, v[132:133]
	global_load_lds_dwordx4 v[218:219], off
	v_lshl_add_u64 v[218:219], s[92:93], 0, v[134:135]
	s_mov_b32 m0, s66
	s_nop 0
	global_load_lds_dwordx4 v[218:219], off
	v_lshl_add_u64 v[218:219], s[40:41], 0, v[128:129]
	s_mov_b32 m0, s44
	s_nop 0
	global_load_lds_dwordx4 v[218:219], off
	s_mov_b32 m0, s45
	s_nop 0
	global_load_lds_dwordx4 v[220:221], off
	s_waitcnt vmcnt(8)
	s_waitcnt lgkmcnt(0)
	s_barrier
	s_setprio 1
	v_mfma_f32_16x16x32_bf16 v[60:63], v[146:149], v[186:189], v[60:63]
	v_mfma_f32_16x16x32_bf16 v[56:59], v[162:165], v[186:189], v[56:59]
	v_mfma_f32_16x16x32_bf16 v[44:47], v[146:149], v[194:197], v[44:47]
	v_mfma_f32_16x16x32_bf16 v[40:43], v[162:165], v[194:197], v[40:43]
	v_mfma_f32_16x16x32_bf16 v[28:31], v[146:149], v[202:205], v[28:31]
	v_mfma_f32_16x16x32_bf16 v[24:27], v[162:165], v[202:205], v[24:27]
	v_mfma_f32_16x16x32_bf16 v[12:15], v[146:149], v[210:213], v[12:15]
	v_mfma_f32_16x16x32_bf16 v[8:11], v[162:165], v[210:213], v[8:11]
	v_mfma_f32_16x16x32_bf16 v[60:63], v[158:161], v[190:193], v[60:63]
	v_mfma_f32_16x16x32_bf16 v[56:59], v[166:169], v[190:193], v[56:59]
	v_mfma_f32_16x16x32_bf16 v[44:47], v[158:161], v[198:201], v[44:47]
	v_mfma_f32_16x16x32_bf16 v[40:43], v[166:169], v[198:201], v[40:43]
	v_mfma_f32_16x16x32_bf16 v[28:31], v[158:161], v[206:209], v[28:31]
	v_mfma_f32_16x16x32_bf16 v[24:27], v[166:169], v[206:209], v[24:27]
	v_mfma_f32_16x16x32_bf16 v[12:15], v[158:161], v[214:217], v[12:15]
	v_mfma_f32_16x16x32_bf16 v[8:11], v[166:169], v[214:217], v[8:11]
	s_setprio 0
	s_setprio 1
	v_mfma_f32_16x16x32_bf16 v[52:55], v[170:173], v[186:189], v[52:55]
	v_mfma_f32_16x16x32_bf16 v[48:51], v[178:181], v[186:189], v[48:51]
	v_mfma_f32_16x16x32_bf16 v[36:39], v[170:173], v[194:197], v[36:39]
	v_mfma_f32_16x16x32_bf16 v[32:35], v[178:181], v[194:197], v[32:35]
	v_mfma_f32_16x16x32_bf16 v[20:23], v[170:173], v[202:205], v[20:23]
	v_mfma_f32_16x16x32_bf16 v[16:19], v[178:181], v[202:205], v[16:19]
	v_mfma_f32_16x16x32_bf16 v[4:7], v[170:173], v[210:213], v[4:7]
	v_mfma_f32_16x16x32_bf16 v[0:3], v[178:181], v[210:213], v[0:3]
	v_mfma_f32_16x16x32_bf16 v[52:55], v[174:177], v[190:193], v[52:55]
	v_mfma_f32_16x16x32_bf16 v[48:51], v[182:185], v[190:193], v[48:51]
	v_mfma_f32_16x16x32_bf16 v[36:39], v[174:177], v[198:201], v[36:39]
	v_mfma_f32_16x16x32_bf16 v[32:35], v[182:185], v[198:201], v[32:35]
	v_mfma_f32_16x16x32_bf16 v[20:23], v[174:177], v[206:209], v[20:23]
	v_mfma_f32_16x16x32_bf16 v[16:19], v[182:185], v[206:209], v[16:19]
	v_mfma_f32_16x16x32_bf16 v[4:7], v[174:177], v[214:217], v[4:7]
	v_mfma_f32_16x16x32_bf16 v[0:3], v[182:185], v[214:217], v[0:3]
	s_setprio 0
	s_barrier
; #define PG8_STAGE(bufoff, gbase, voff) do { _Pragma("unroll") for (int _i = 0; _i < 2; ++_i) \
;         __builtin_amdgcn_global_load_lds((const unsigned*)((const char*)(gbase) + (voff)[_i]), (PG8_LAS unsigned*)(lds + (bufoff) + ldsw + _i * 8192), 16, 0, 0); } while (0)
; #define PG8_WAIT_V(n) asm volatile("s_waitcnt vmcnt(" #n ")" ::: "memory")
; #define PG8_WAIT_L(n) asm volatile("s_waitcnt lgkmcnt(" #n ")" ::: "memory")
; #define PG8_BAR __builtin_amdgcn_s_barrier()
; #define PG8_SCHED __builtin_amdgcn_sched_barrier(0)
; template <class Epi, class Sched, bool ALIGN_EPI = false, bool SP2 = false, bool FP8 = false, bool PEEL = false>
; __device__ __forceinline__ void gemm_phase(PG8_LAS unsigned char* lds, const Gemm g, const Sched& S, const Epi& E, const int wid) {
;     ...
;             PG8_LDB(B0, 1, 0); PG8_LDB(B1, 1, 1); PG8_SCHED; PG8_LDA(At, 1, 0); PG8_STAGE(PG8_SA(0, 1), a2 + hstep, voffA);
;             PG8_WAIT_V(8); PG8_WAIT_L(0); PG8_BAR; PG8_MMA(0, 0, At, B0); PG8_MMA(0, 1, At, B1); PG8_BAR; PG8_SCHED;
;             PG8_LDA(At, 1, 1); PG8_STAGE(PG8_SB(1, 0), b3, voffB); PG8_STAGE(PG8_SB(1, 1), b3 + hstep, voffB); PG8_STAGE(PG8_SA(1, 0), a3, voffA);
;             PG8_WAIT_V(8); PG8_WAIT_L(0); PG8_BAR; PG8_MMA(1, 0, At, B0); PG8_MMA(1, 1, At, B1); PG8_BAR; PG8_SCHED;
;         }
;     ...
;         if constexpr (ALIGN_EPI) { if (wr == 0) PG8_BAR; }
	ds_read_b128 v[146:149], v144
	ds_read_b128 v[158:161], v144 offset:1024
	ds_read_b128 v[162:165], v144 offset:2048
	ds_read_b128 v[166:169], v144 offset:3072
	ds_read_b128 v[170:173], v145
	ds_read_b128 v[174:177], v145 offset:1024
	ds_read_b128 v[178:181], v145 offset:2048
	ds_read_b128 v[182:185], v145 offset:3072
	s_add_u32 s40, s40, 0x40000
	s_addc_u32 s41, s41, 0
	s_mov_b32 m0, s46
	v_lshl_add_u64 v[222:223], s[40:41], 0, v[128:129]
	ds_read_b128 v[186:189], v155 offset:32768
	ds_read_b128 v[190:193], v155 offset:33792
	ds_read_b128 v[194:197], v155 offset:34816
	ds_read_b128 v[198:201], v155 offset:35840
	ds_read_b128 v[202:205], v155 offset:36864
	ds_read_b128 v[206:209], v155 offset:37888
	ds_read_b128 v[210:213], v155 offset:38912
	ds_read_b128 v[214:217], v155 offset:39936
	global_load_lds_dwordx4 v[222:223], off
	v_lshl_add_u64 v[222:223], s[40:41], 0, v[132:133]
	s_mov_b32 m0, s47
	s_nop 0
	global_load_lds_dwordx4 v[222:223], off
	s_waitcnt vmcnt(8)
	s_waitcnt lgkmcnt(0)
	s_barrier
	s_setprio 1
	v_mfma_f32_16x16x32_bf16 v[124:127], v[146:149], v[186:189], v[124:127]
	v_mfma_f32_16x16x32_bf16 v[120:123], v[162:165], v[186:189], v[120:123]
	v_mfma_f32_16x16x32_bf16 v[108:111], v[146:149], v[194:197], v[108:111]
	v_mfma_f32_16x16x32_bf16 v[104:107], v[162:165], v[194:197], v[104:107]
	v_mfma_f32_16x16x32_bf16 v[92:95], v[146:149], v[202:205], v[92:95]
	v_mfma_f32_16x16x32_bf16 v[88:91], v[162:165], v[202:205], v[88:91]
	v_mfma_f32_16x16x32_bf16 v[76:79], v[146:149], v[210:213], v[76:79]
	v_mfma_f32_16x16x32_bf16 v[72:75], v[162:165], v[210:213], v[72:75]
	v_mfma_f32_16x16x32_bf16 v[124:127], v[158:161], v[190:193], v[124:127]
	v_mfma_f32_16x16x32_bf16 v[120:123], v[166:169], v[190:193], v[120:123]
	v_mfma_f32_16x16x32_bf16 v[108:111], v[158:161], v[198:201], v[108:111]
	v_mfma_f32_16x16x32_bf16 v[104:107], v[166:169], v[198:201], v[104:107]
	v_mfma_f32_16x16x32_bf16 v[92:95], v[158:161], v[206:209], v[92:95]
	v_mfma_f32_16x16x32_bf16 v[88:91], v[166:169], v[206:209], v[88:91]
	v_mfma_f32_16x16x32_bf16 v[76:79], v[158:161], v[214:217], v[76:79]
	v_mfma_f32_16x16x32_bf16 v[72:75], v[166:169], v[214:217], v[72:75]
	s_setprio 0
	s_setprio 1
	v_mfma_f32_16x16x32_bf16 v[116:119], v[170:173], v[186:189], v[116:119]
	v_mfma_f32_16x16x32_bf16 v[112:115], v[178:181], v[186:189], v[112:115]
	v_mfma_f32_16x16x32_bf16 v[100:103], v[170:173], v[194:197], v[100:103]
	v_mfma_f32_16x16x32_bf16 v[96:99], v[178:181], v[194:197], v[96:99]
	v_mfma_f32_16x16x32_bf16 v[84:87], v[170:173], v[202:205], v[84:87]
	v_mfma_f32_16x16x32_bf16 v[80:83], v[178:181], v[202:205], v[80:83]
	v_mfma_f32_16x16x32_bf16 v[68:71], v[170:173], v[210:213], v[68:71]
	v_mfma_f32_16x16x32_bf16 v[64:67], v[178:181], v[210:213], v[64:67]
	v_mfma_f32_16x16x32_bf16 v[116:119], v[174:177], v[190:193], v[116:119]
	v_mfma_f32_16x16x32_bf16 v[112:115], v[182:185], v[190:193], v[112:115]
	v_mfma_f32_16x16x32_bf16 v[100:103], v[174:177], v[198:201], v[100:103]
	v_mfma_f32_16x16x32_bf16 v[96:99], v[182:185], v[198:201], v[96:99]
	v_mfma_f32_16x16x32_bf16 v[84:87], v[174:177], v[206:209], v[84:87]
	v_mfma_f32_16x16x32_bf16 v[80:83], v[182:185], v[206:209], v[80:83]
	v_mfma_f32_16x16x32_bf16 v[68:71], v[174:177], v[214:217], v[68:71]
	v_mfma_f32_16x16x32_bf16 v[64:67], v[182:185], v[214:217], v[64:67]
	s_setprio 0
	s_barrier
	s_mov_b32 m0, s67
	v_lshl_add_u64 v[140:141], v[140:141], 0, s[14:15]
	s_add_u32 s30, s30, 0x40080
	ds_read_b128 v[186:189], v155 offset:49152
	ds_read_b128 v[190:193], v155 offset:50176
	ds_read_b128 v[194:197], v155 offset:51200
	ds_read_b128 v[198:201], v155 offset:52224
	ds_read_b128 v[202:205], v155 offset:53248
	ds_read_b128 v[206:209], v155 offset:54272
	ds_read_b128 v[210:213], v155 offset:55296
	ds_read_b128 v[214:217], v155 offset:56320
	global_load_lds_dwordx4 v[140:141], off
	v_lshl_add_u64 v[140:141], v[142:143], 0, s[14:15]
	s_mov_b32 m0, s75
	s_addc_u32 s31, s31, 0
	global_load_lds_dwordx4 v[140:141], off
	v_lshl_add_u64 v[140:141], s[30:31], 0, v[130:131]
	s_mov_b32 m0, s84
	s_nop 0
	global_load_lds_dwordx4 v[140:141], off
	v_lshl_add_u64 v[140:141], s[30:31], 0, v[134:135]
	s_mov_b32 m0, s85
	s_nop 0
	global_load_lds_dwordx4 v[140:141], off
	v_lshl_add_u64 v[140:141], v[218:219], 0, s[14:15]
	s_mov_b32 m0, s54
	s_nop 0
	global_load_lds_dwordx4 v[140:141], off
	v_lshl_add_u64 v[140:141], v[220:221], 0, s[14:15]
	s_mov_b32 m0, s55
	s_nop 0
	global_load_lds_dwordx4 v[140:141], off
	s_waitcnt vmcnt(8)
	s_waitcnt lgkmcnt(0)
	s_barrier
	s_setprio 1
	v_mfma_f32_16x16x32_bf16 v[60:63], v[146:149], v[186:189], v[60:63]
	v_mfma_f32_16x16x32_bf16 v[56:59], v[162:165], v[186:189], v[56:59]
	v_mfma_f32_16x16x32_bf16 v[44:47], v[146:149], v[194:197], v[44:47]
	v_mfma_f32_16x16x32_bf16 v[40:43], v[162:165], v[194:197], v[40:43]
	v_mfma_f32_16x16x32_bf16 v[28:31], v[146:149], v[202:205], v[28:31]
	v_mfma_f32_16x16x32_bf16 v[24:27], v[162:165], v[202:205], v[24:27]
	v_mfma_f32_16x16x32_bf16 v[12:15], v[146:149], v[210:213], v[12:15]
	v_mfma_f32_16x16x32_bf16 v[8:11], v[162:165], v[210:213], v[8:11]
	v_mfma_f32_16x16x32_bf16 v[60:63], v[158:161], v[190:193], v[60:63]
	v_mfma_f32_16x16x32_bf16 v[56:59], v[166:169], v[190:193], v[56:59]
	v_mfma_f32_16x16x32_bf16 v[44:47], v[158:161], v[198:201], v[44:47]
	v_mfma_f32_16x16x32_bf16 v[40:43], v[166:169], v[198:201], v[40:43]
	v_mfma_f32_16x16x32_bf16 v[28:31], v[158:161], v[206:209], v[28:31]
	v_mfma_f32_16x16x32_bf16 v[24:27], v[166:169], v[206:209], v[24:27]
	v_mfma_f32_16x16x32_bf16 v[12:15], v[158:161], v[214:217], v[12:15]
	v_mfma_f32_16x16x32_bf16 v[8:11], v[166:169], v[214:217], v[8:11]
	s_setprio 0
	s_setprio 1
	v_mfma_f32_16x16x32_bf16 v[52:55], v[170:173], v[186:189], v[52:55]
	v_mfma_f32_16x16x32_bf16 v[48:51], v[178:181], v[186:189], v[48:51]
	v_mfma_f32_16x16x32_bf16 v[36:39], v[170:173], v[194:197], v[36:39]
	v_mfma_f32_16x16x32_bf16 v[32:35], v[178:181], v[194:197], v[32:35]
	v_mfma_f32_16x16x32_bf16 v[20:23], v[170:173], v[202:205], v[20:23]
	v_mfma_f32_16x16x32_bf16 v[16:19], v[178:181], v[202:205], v[16:19]
	v_mfma_f32_16x16x32_bf16 v[4:7], v[170:173], v[210:213], v[4:7]
	v_mfma_f32_16x16x32_bf16 v[0:3], v[178:181], v[210:213], v[0:3]
	v_mfma_f32_16x16x32_bf16 v[52:55], v[174:177], v[190:193], v[52:55]
	v_mfma_f32_16x16x32_bf16 v[48:51], v[182:185], v[190:193], v[48:51]
	v_mfma_f32_16x16x32_bf16 v[36:39], v[174:177], v[198:201], v[36:39]
	v_mfma_f32_16x16x32_bf16 v[32:35], v[182:185], v[198:201], v[32:35]
	v_mfma_f32_16x16x32_bf16 v[20:23], v[174:177], v[206:209], v[20:23]
	v_mfma_f32_16x16x32_bf16 v[16:19], v[182:185], v[206:209], v[16:19]
	v_mfma_f32_16x16x32_bf16 v[4:7], v[174:177], v[214:217], v[4:7]
	v_mfma_f32_16x16x32_bf16 v[0:3], v[182:185], v[214:217], v[0:3]
	s_setprio 0
	s_barrier
	s_add_i32 s90, s90, 2
	s_add_u32 s36, s36, 0x100
	s_addc_u32 s37, s37, 0
	s_add_u32 s88, s88, 0x100
	s_addc_u32 s89, s89, 0
	s_cmp_gt_u32 s90, 13
	s_cbranch_scc0 .LBB0_237
	s_and_b64 vcc, exec, s[6:7]
	s_cbranch_vccz .LBB0_240
	s_barrier

; #define PG8_STAGE(bufoff, gbase, voff) do { _Pragma("unroll") for (int _i = 0; _i < 2; ++_i) \
;         __builtin_amdgcn_global_load_lds((const unsigned*)((const char*)(gbase) + (voff)[_i]), (PG8_LAS unsigned*)(lds + (bufoff) + ldsw + _i * 8192), 16, 0, 0); } while (0)
; #define PG8_WAIT_V(n) asm volatile("s_waitcnt vmcnt(" #n ")" ::: "memory")
; #define PG8_WAIT_L(n) asm volatile("s_waitcnt lgkmcnt(" #n ")" ::: "memory")
; #define PG8_BAR __builtin_amdgcn_s_barrier()
; #define PG8_SCHED __builtin_amdgcn_sched_barrier(0)
; template <class Epi, class Sched, bool ALIGN_EPI = false, bool SP2 = false, bool FP8 = false, bool PEEL = false>
; __device__ __forceinline__ void gemm_phase(PG8_LAS unsigned char* lds, const Gemm g, const Sched& S, const Epi& E, const int wid) {
;     ...
;         for (int t = 0; t < nt; t += 2) {
;             const bool last = (t == nt - 2);
;             const char* a1 = cA + (size_t)(t + 1) * kstep;
;             const char* a2 = last ? nA : cA + (size_t)(t + 2) * kstep; const char* b2 = last ? nB : cB + (size_t)(t + 2) * kstep;
;             const char* a3 = a2 + kstep; const char* b3 = b2 + kstep;
;             if (last && has_next) S.a_ready(nxt);
;             PG8_LDB(B0, 0, 0); PG8_LDB(B1, 0, 1); PG8_SCHED; PG8_LDA(At, 0, 0); PG8_STAGE(PG8_SA(1, 1), a1 + hstep, voffA);
;             PG8_WAIT_V(8); PG8_WAIT_L(0); PG8_BAR; PG8_MMA(0, 0, At, B0); PG8_MMA(0, 1, At, B1); PG8_BAR; PG8_SCHED;
;             PG8_LDA(At, 0, 1); PG8_STAGE(PG8_SB(0, 0), b2, voffB); PG8_STAGE(PG8_SB(0, 1), b2 + hstep, voffB); PG8_STAGE(PG8_SA(0, 0), a2, voffA);
;             PG8_WAIT_V(8); PG8_WAIT_L(0); PG8_BAR; PG8_MMA(1, 0, At, B0); PG8_MMA(1, 1, At, B1); PG8_BAR; PG8_SCHED;
.LBB0_659:
	v_add_u32_e32 v162, s50, v148
	v_add_u32_e32 v178, s51, v148
	s_add_u32 s26, s6, s24
	ds_read_b128 v[150:153], v162
	ds_read_b128 v[154:157], v162 offset:1024
	ds_read_b128 v[158:161], v162 offset:2048
	ds_read_b128 v[162:165], v162 offset:3072
	ds_read_b128 v[166:169], v178
	ds_read_b128 v[170:173], v178 offset:1024
	ds_read_b128 v[174:177], v178 offset:2048
	ds_read_b128 v[178:181], v178 offset:3072
	s_addc_u32 s27, s7, s25
	s_add_u32 s26, s26, 0x100
	s_addc_u32 s27, s27, 0
	s_add_u32 s59, s54, s24
	s_addc_u32 s60, s55, s25
	s_cmpk_eq_i32 s24, 0x700
	s_cselect_b32 s31, s17, s27
	s_cselect_b32 s30, s56, s26
	s_cselect_b32 s27, s15, s60
	s_cselect_b32 s26, s57, s59
	v_lshl_add_u64 v[218:219], v[144:145], 0, s[24:25]
	s_add_i32 m0, s43, 0xc000
	ds_read_b128 v[182:185], v149
	ds_read_b128 v[190:193], v149 offset:1024
	ds_read_b128 v[194:197], v149 offset:2048
	ds_read_b128 v[198:201], v149 offset:3072
	ds_read_b128 v[202:205], v149 offset:4096
	ds_read_b128 v[206:209], v149 offset:5120
	ds_read_b128 v[210:213], v149 offset:6144
	ds_read_b128 v[214:217], v149 offset:7168
	global_load_lds_dwordx4 v[218:219], off
	v_lshl_add_u64 v[218:219], v[146:147], 0, s[24:25]
	s_add_i32 m0, s43, 0xe000
	s_nop 0
	global_load_lds_dwordx4 v[218:219], off
	s_waitcnt vmcnt(8)
	s_waitcnt lgkmcnt(0)
	s_barrier
	s_setprio 1
	v_mfma_f32_16x16x32_bf16 v[124:127], v[150:153], v[182:185], v[124:127]
	v_mfma_f32_16x16x32_bf16 v[120:123], v[158:161], v[182:185], v[120:123]
	v_mfma_f32_16x16x32_bf16 v[112:115], v[150:153], v[194:197], v[112:115]
	v_mfma_f32_16x16x32_bf16 v[108:111], v[158:161], v[194:197], v[108:111]
	v_mfma_f32_16x16x32_bf16 v[100:103], v[150:153], v[202:205], v[100:103]
	v_mfma_f32_16x16x32_bf16 v[92:95], v[158:161], v[202:205], v[92:95]
	v_mfma_f32_16x16x32_bf16 v[84:87], v[150:153], v[210:213], v[84:87]
	v_mfma_f32_16x16x32_bf16 v[76:79], v[158:161], v[210:213], v[76:79]
	v_mfma_f32_16x16x32_bf16 v[124:127], v[154:157], v[190:193], v[124:127]
	v_mfma_f32_16x16x32_bf16 v[120:123], v[162:165], v[190:193], v[120:123]
	v_mfma_f32_16x16x32_bf16 v[112:115], v[154:157], v[198:201], v[112:115]
	v_mfma_f32_16x16x32_bf16 v[108:111], v[162:165], v[198:201], v[108:111]
	v_mfma_f32_16x16x32_bf16 v[100:103], v[154:157], v[206:209], v[100:103]
	v_mfma_f32_16x16x32_bf16 v[92:95], v[162:165], v[206:209], v[92:95]
	v_mfma_f32_16x16x32_bf16 v[84:87], v[154:157], v[214:217], v[84:87]
	v_mfma_f32_16x16x32_bf16 v[76:79], v[162:165], v[214:217], v[76:79]
	s_setprio 0
	s_setprio 1
	v_mfma_f32_16x16x32_bf16 v[116:119], v[166:169], v[182:185], v[116:119]
	v_mfma_f32_16x16x32_bf16 v[104:107], v[174:177], v[182:185], v[104:107]
	v_mfma_f32_16x16x32_bf16 v[96:99], v[166:169], v[194:197], v[96:99]
	v_mfma_f32_16x16x32_bf16 v[88:91], v[174:177], v[194:197], v[88:91]
	v_mfma_f32_16x16x32_bf16 v[80:83], v[166:169], v[202:205], v[80:83]
	v_mfma_f32_16x16x32_bf16 v[72:75], v[174:177], v[202:205], v[72:75]
	v_mfma_f32_16x16x32_bf16 v[68:71], v[166:169], v[210:213], v[68:71]
	v_mfma_f32_16x16x32_bf16 v[64:67], v[174:177], v[210:213], v[64:67]
	v_mfma_f32_16x16x32_bf16 v[116:119], v[170:173], v[190:193], v[116:119]
	v_mfma_f32_16x16x32_bf16 v[104:107], v[178:181], v[190:193], v[104:107]
	v_mfma_f32_16x16x32_bf16 v[96:99], v[170:173], v[198:201], v[96:99]
	v_mfma_f32_16x16x32_bf16 v[88:91], v[178:181], v[198:201], v[88:91]
	v_mfma_f32_16x16x32_bf16 v[80:83], v[170:173], v[206:209], v[80:83]
	v_mfma_f32_16x16x32_bf16 v[72:75], v[178:181], v[206:209], v[72:75]
	v_mfma_f32_16x16x32_bf16 v[68:71], v[170:173], v[214:217], v[68:71]
	v_mfma_f32_16x16x32_bf16 v[64:67], v[178:181], v[214:217], v[64:67]
	s_setprio 0
	s_barrier
	s_add_i32 s59, s50, s41
	v_lshl_add_u64 v[218:219], s[26:27], 0, v[132:133]
	s_mov_b32 m0, s59
	ds_read_b128 v[182:185], v149 offset:16384
	ds_read_b128 v[190:193], v149 offset:17408
	ds_read_b128 v[194:197], v149 offset:18432
	ds_read_b128 v[198:201], v149 offset:19456
	ds_read_b128 v[202:205], v149 offset:20480
	ds_read_b128 v[206:209], v149 offset:21504
	ds_read_b128 v[210:213], v149 offset:22528
	ds_read_b128 v[214:217], v149 offset:23552
	global_load_lds_dwordx4 v[218:219], off
	s_add_i32 m0, s59, 0x2000
	s_add_u32 s60, s26, 0x40000
	v_lshl_add_u64 v[220:221], s[26:27], 0, v[128:129]
	s_addc_u32 s61, s27, 0
	s_add_i32 s59, s51, s41
	global_load_lds_dwordx4 v[220:221], off
	v_lshl_add_u64 v[222:223], s[60:61], 0, v[132:133]
	s_mov_b32 m0, s59
	v_lshl_add_u64 v[224:225], s[30:31], 0, v[130:131]
	global_load_lds_dwordx4 v[222:223], off
	v_lshl_add_u64 v[222:223], s[60:61], 0, v[128:129]
	s_add_i32 m0, s59, 0x2000
	s_nop 0
	global_load_lds_dwordx4 v[222:223], off
	v_lshl_add_u64 v[222:223], s[30:31], 0, v[134:135]
	s_mov_b32 m0, s43
	s_nop 0
	global_load_lds_dwordx4 v[222:223], off
	s_mov_b32 m0, s44
	s_nop 0
	global_load_lds_dwordx4 v[224:225], off
	s_waitcnt vmcnt(8)
	s_waitcnt lgkmcnt(0)
	s_barrier
; #define PG8_STAGE(bufoff, gbase, voff) do { _Pragma("unroll") for (int _i = 0; _i < 2; ++_i) \
;         __builtin_amdgcn_global_load_lds((const unsigned*)((const char*)(gbase) + (voff)[_i]), (PG8_LAS unsigned*)(lds + (bufoff) + ldsw + _i * 8192), 16, 0, 0); } while (0)
; #define PG8_WAIT_V(n) asm volatile("s_waitcnt vmcnt(" #n ")" ::: "memory")
; #define PG8_WAIT_L(n) asm volatile("s_waitcnt lgkmcnt(" #n ")" ::: "memory")
; #define PG8_BAR __builtin_amdgcn_s_barrier()
; #define PG8_SCHED __builtin_amdgcn_sched_barrier(0)
; template <class Epi, class Sched, bool ALIGN_EPI = false, bool SP2 = false, bool FP8 = false, bool PEEL = false>
; __device__ __forceinline__ void gemm_phase(PG8_LAS unsigned char* lds, const Gemm g, const Sched& S, const Epi& E, const int wid) {
;     ...
;             PG8_WAIT_V(8); PG8_WAIT_L(0); PG8_BAR; PG8_MMA(1, 0, At, B0); PG8_MMA(1, 1, At, B1); PG8_BAR; PG8_SCHED;
;             PG8_LDB(B0, 1, 0); PG8_LDB(B1, 1, 1); PG8_SCHED; PG8_LDA(At, 1, 0); PG8_STAGE(PG8_SA(0, 1), a2 + hstep, voffA);
;             PG8_WAIT_V(8); PG8_WAIT_L(0); PG8_BAR; PG8_MMA(0, 0, At, B0); PG8_MMA(0, 1, At, B1); PG8_BAR; PG8_SCHED;
	s_setprio 1
	v_mfma_f32_16x16x32_bf16 v[60:63], v[150:153], v[182:185], v[60:63]
	v_mfma_f32_16x16x32_bf16 v[56:59], v[158:161], v[182:185], v[56:59]
	v_mfma_f32_16x16x32_bf16 v[52:55], v[150:153], v[194:197], v[52:55]
	v_mfma_f32_16x16x32_bf16 v[44:47], v[158:161], v[194:197], v[44:47]
	v_mfma_f32_16x16x32_bf16 v[36:39], v[150:153], v[202:205], v[36:39]
	v_mfma_f32_16x16x32_bf16 v[28:31], v[158:161], v[202:205], v[28:31]
	v_mfma_f32_16x16x32_bf16 v[20:23], v[150:153], v[210:213], v[20:23]
	v_mfma_f32_16x16x32_bf16 v[12:15], v[158:161], v[210:213], v[12:15]
	v_mfma_f32_16x16x32_bf16 v[60:63], v[154:157], v[190:193], v[60:63]
	v_mfma_f32_16x16x32_bf16 v[56:59], v[162:165], v[190:193], v[56:59]
	v_mfma_f32_16x16x32_bf16 v[52:55], v[154:157], v[198:201], v[52:55]
	v_mfma_f32_16x16x32_bf16 v[44:47], v[162:165], v[198:201], v[44:47]
	v_mfma_f32_16x16x32_bf16 v[36:39], v[154:157], v[206:209], v[36:39]
	v_mfma_f32_16x16x32_bf16 v[28:31], v[162:165], v[206:209], v[28:31]
	v_mfma_f32_16x16x32_bf16 v[20:23], v[154:157], v[214:217], v[20:23]
	v_mfma_f32_16x16x32_bf16 v[12:15], v[162:165], v[214:217], v[12:15]
	s_setprio 0
	s_setprio 1
	v_mfma_f32_16x16x32_bf16 v[48:51], v[166:169], v[182:185], v[48:51]
	v_mfma_f32_16x16x32_bf16 v[40:43], v[174:177], v[182:185], v[40:43]
	v_mfma_f32_16x16x32_bf16 v[32:35], v[166:169], v[194:197], v[32:35]
	v_mfma_f32_16x16x32_bf16 v[24:27], v[174:177], v[194:197], v[24:27]
	v_mfma_f32_16x16x32_bf16 v[16:19], v[166:169], v[202:205], v[16:19]
	v_mfma_f32_16x16x32_bf16 v[8:11], v[174:177], v[202:205], v[8:11]
	v_mfma_f32_16x16x32_bf16 v[4:7], v[166:169], v[210:213], v[4:7]
	v_mfma_f32_16x16x32_bf16 v[0:3], v[174:177], v[210:213], v[0:3]
	v_mfma_f32_16x16x32_bf16 v[48:51], v[170:173], v[190:193], v[48:51]
	v_mfma_f32_16x16x32_bf16 v[40:43], v[178:181], v[190:193], v[40:43]
	v_mfma_f32_16x16x32_bf16 v[32:35], v[170:173], v[198:201], v[32:35]
	v_mfma_f32_16x16x32_bf16 v[24:27], v[178:181], v[198:201], v[24:27]
	v_mfma_f32_16x16x32_bf16 v[16:19], v[170:173], v[206:209], v[16:19]
	v_mfma_f32_16x16x32_bf16 v[8:11], v[178:181], v[206:209], v[8:11]
	v_mfma_f32_16x16x32_bf16 v[4:7], v[170:173], v[214:217], v[4:7]
	v_mfma_f32_16x16x32_bf16 v[0:3], v[178:181], v[214:217], v[0:3]
	s_setprio 0
	s_barrier
	s_add_i32 s59, 0, 0x18000
	s_add_i32 s60, 0, 0x1c000
	v_add_u32_e32 v162, s59, v148
	v_add_u32_e32 v178, s60, v148
	ds_read_b128 v[150:153], v162
	ds_read_b128 v[154:157], v162 offset:1024
	ds_read_b128 v[158:161], v162 offset:2048
	ds_read_b128 v[162:165], v162 offset:3072
	ds_read_b128 v[166:169], v178
	ds_read_b128 v[170:173], v178 offset:1024
	ds_read_b128 v[174:177], v178 offset:2048
	ds_read_b128 v[178:181], v178 offset:3072
	s_add_u32 s30, s30, 0x40000
	s_addc_u32 s31, s31, 0
	s_mov_b32 m0, s45
	v_lshl_add_u64 v[226:227], s[30:31], 0, v[134:135]
	ds_read_b128 v[182:185], v149 offset:32768
	ds_read_b128 v[190:193], v149 offset:33792
	ds_read_b128 v[194:197], v149 offset:34816
	ds_read_b128 v[198:201], v149 offset:35840
	ds_read_b128 v[202:205], v149 offset:36864
	ds_read_b128 v[206:209], v149 offset:37888
	ds_read_b128 v[210:213], v149 offset:38912
	ds_read_b128 v[214:217], v149 offset:39936
	global_load_lds_dwordx4 v[226:227], off
	v_lshl_add_u64 v[226:227], s[30:31], 0, v[130:131]
	s_mov_b32 m0, s46
	s_nop 0
	global_load_lds_dwordx4 v[226:227], off
	s_waitcnt vmcnt(8)
	s_waitcnt lgkmcnt(0)
	s_barrier
	s_setprio 1
	v_mfma_f32_16x16x32_bf16 v[124:127], v[150:153], v[182:185], v[124:127]
	v_mfma_f32_16x16x32_bf16 v[120:123], v[158:161], v[182:185], v[120:123]
	v_mfma_f32_16x16x32_bf16 v[112:115], v[150:153], v[194:197], v[112:115]
	v_mfma_f32_16x16x32_bf16 v[108:111], v[158:161], v[194:197], v[108:111]
	v_mfma_f32_16x16x32_bf16 v[100:103], v[150:153], v[202:205], v[100:103]
	v_mfma_f32_16x16x32_bf16 v[92:95], v[158:161], v[202:205], v[92:95]
	v_mfma_f32_16x16x32_bf16 v[84:87], v[150:153], v[210:213], v[84:87]
	v_mfma_f32_16x16x32_bf16 v[76:79], v[158:161], v[210:213], v[76:79]
	v_mfma_f32_16x16x32_bf16 v[124:127], v[154:157], v[190:193], v[124:127]
	v_mfma_f32_16x16x32_bf16 v[120:123], v[162:165], v[190:193], v[120:123]
	v_mfma_f32_16x16x32_bf16 v[112:115], v[154:157], v[198:201], v[112:115]
	v_mfma_f32_16x16x32_bf16 v[108:111], v[162:165], v[198:201], v[108:111]
	v_mfma_f32_16x16x32_bf16 v[100:103], v[154:157], v[206:209], v[100:103]
	v_mfma_f32_16x16x32_bf16 v[92:95], v[162:165], v[206:209], v[92:95]
	v_mfma_f32_16x16x32_bf16 v[84:87], v[154:157], v[214:217], v[84:87]
	v_mfma_f32_16x16x32_bf16 v[76:79], v[162:165], v[214:217], v[76:79]
	s_setprio 0
	s_setprio 1
	v_mfma_f32_16x16x32_bf16 v[116:119], v[166:169], v[182:185], v[116:119]
	v_mfma_f32_16x16x32_bf16 v[104:107], v[174:177], v[182:185], v[104:107]
	v_mfma_f32_16x16x32_bf16 v[96:99], v[166:169], v[194:197], v[96:99]
	v_mfma_f32_16x16x32_bf16 v[88:91], v[174:177], v[194:197], v[88:91]
	v_mfma_f32_16x16x32_bf16 v[80:83], v[166:169], v[202:205], v[80:83]
	v_mfma_f32_16x16x32_bf16 v[72:75], v[174:177], v[202:205], v[72:75]
	v_mfma_f32_16x16x32_bf16 v[68:71], v[166:169], v[210:213], v[68:71]
	v_mfma_f32_16x16x32_bf16 v[64:67], v[174:177], v[210:213], v[64:67]
	v_mfma_f32_16x16x32_bf16 v[116:119], v[170:173], v[190:193], v[116:119]
	v_mfma_f32_16x16x32_bf16 v[104:107], v[178:181], v[190:193], v[104:107]
	v_mfma_f32_16x16x32_bf16 v[96:99], v[170:173], v[198:201], v[96:99]
	v_mfma_f32_16x16x32_bf16 v[88:91], v[178:181], v[198:201], v[88:91]
	v_mfma_f32_16x16x32_bf16 v[80:83], v[170:173], v[206:209], v[80:83]
	v_mfma_f32_16x16x32_bf16 v[72:75], v[178:181], v[206:209], v[72:75]
	v_mfma_f32_16x16x32_bf16 v[68:71], v[170:173], v[214:217], v[68:71]
	v_mfma_f32_16x16x32_bf16 v[64:67], v[178:181], v[214:217], v[64:67]
	s_setprio 0
	s_barrier
; #define PG8_STAGE(bufoff, gbase, voff) do { _Pragma("unroll") for (int _i = 0; _i < 2; ++_i) \
;         __builtin_amdgcn_global_load_lds((const unsigned*)((const char*)(gbase) + (voff)[_i]), (PG8_LAS unsigned*)(lds + (bufoff) + ldsw + _i * 8192), 16, 0, 0); } while (0)
; #define PG8_WAIT_V(n) asm volatile("s_waitcnt vmcnt(" #n ")" ::: "memory")
; #define PG8_WAIT_L(n) asm volatile("s_waitcnt lgkmcnt(" #n ")" ::: "memory")
; #define PG8_BAR __builtin_amdgcn_s_barrier()
; #define PG8_SCHED __builtin_amdgcn_sched_barrier(0)
; template <class Epi, class Sched, bool ALIGN_EPI = false, bool SP2 = false, bool FP8 = false, bool PEEL = false>
; __device__ __forceinline__ void gemm_phase(PG8_LAS unsigned char* lds, const Gemm g, const Sched& S, const Epi& E, const int wid) {
;     ...
;             PG8_LDA(At, 1, 1); PG8_STAGE(PG8_SB(1, 0), b3, voffB); PG8_STAGE(PG8_SB(1, 1), b3 + hstep, voffB); PG8_STAGE(PG8_SA(1, 0), a3, voffA);
;             PG8_WAIT_V(8); PG8_WAIT_L(0); PG8_BAR; PG8_MMA(1, 0, At, B0); PG8_MMA(1, 1, At, B1); PG8_BAR; PG8_SCHED;
;         }
;     ...
;         if (!has_next) break;
;         if constexpr (!PEEL) {
; #pragma unroll
;         for (int a = 0; a < 2; ++a)
; #pragma unroll
;             for (int b = 0; b < 2; ++b)
; #pragma unroll
;                 for (int m = 0; m < 4; ++m)
; #pragma unroll
;                     for (int n = 0; n < 2; ++n) acc[a][b][m][n] = (f32x4){0.f, 0.f, 0.f, 0.f};
;         }
;         cur = nxt; cA = nA; cB = nB; ++ui;
	s_add_i32 s30, s59, s41
	v_lshl_add_u64 v[218:219], v[218:219], 0, s[12:13]
	s_mov_b32 m0, s30
	ds_read_b128 v[182:185], v149 offset:49152
	ds_read_b128 v[190:193], v149 offset:50176
	ds_read_b128 v[194:197], v149 offset:51200
	ds_read_b128 v[198:201], v149 offset:52224
	ds_read_b128 v[202:205], v149 offset:53248
	ds_read_b128 v[206:209], v149 offset:54272
	ds_read_b128 v[210:213], v149 offset:55296
	ds_read_b128 v[214:217], v149 offset:56320
	global_load_lds_dwordx4 v[218:219], off
	s_add_i32 m0, s30, 0x2000
	s_add_u32 s26, s26, 0x40080
	v_lshl_add_u64 v[218:219], v[220:221], 0, s[12:13]
	s_addc_u32 s27, s27, 0
	s_add_i32 s30, s60, s41
	global_load_lds_dwordx4 v[218:219], off
	v_lshl_add_u64 v[218:219], s[26:27], 0, v[132:133]
	s_mov_b32 m0, s30
	s_nop 0
	global_load_lds_dwordx4 v[218:219], off
	v_lshl_add_u64 v[218:219], s[26:27], 0, v[128:129]
	s_add_i32 m0, s30, 0x2000
	s_nop 0
	global_load_lds_dwordx4 v[218:219], off
	v_lshl_add_u64 v[218:219], v[222:223], 0, s[12:13]
	s_mov_b32 m0, s47
	s_nop 0
	global_load_lds_dwordx4 v[218:219], off
	v_lshl_add_u64 v[218:219], v[224:225], 0, s[12:13]
	s_mov_b32 m0, s48
	s_nop 0
	global_load_lds_dwordx4 v[218:219], off
	s_waitcnt vmcnt(8)
	s_waitcnt lgkmcnt(0)
	s_barrier
	s_setprio 1
	v_mfma_f32_16x16x32_bf16 v[60:63], v[150:153], v[182:185], v[60:63]
	v_mfma_f32_16x16x32_bf16 v[56:59], v[158:161], v[182:185], v[56:59]
	v_mfma_f32_16x16x32_bf16 v[52:55], v[150:153], v[194:197], v[52:55]
	v_mfma_f32_16x16x32_bf16 v[44:47], v[158:161], v[194:197], v[44:47]
	v_mfma_f32_16x16x32_bf16 v[36:39], v[150:153], v[202:205], v[36:39]
	v_mfma_f32_16x16x32_bf16 v[28:31], v[158:161], v[202:205], v[28:31]
	v_mfma_f32_16x16x32_bf16 v[20:23], v[150:153], v[210:213], v[20:23]
	v_mfma_f32_16x16x32_bf16 v[12:15], v[158:161], v[210:213], v[12:15]
	v_mfma_f32_16x16x32_bf16 v[60:63], v[154:157], v[190:193], v[60:63]
	v_mfma_f32_16x16x32_bf16 v[56:59], v[162:165], v[190:193], v[56:59]
	v_mfma_f32_16x16x32_bf16 v[52:55], v[154:157], v[198:201], v[52:55]
	v_mfma_f32_16x16x32_bf16 v[44:47], v[162:165], v[198:201], v[44:47]
	v_mfma_f32_16x16x32_bf16 v[36:39], v[154:157], v[206:209], v[36:39]
	v_mfma_f32_16x16x32_bf16 v[28:31], v[162:165], v[206:209], v[28:31]
	v_mfma_f32_16x16x32_bf16 v[20:23], v[154:157], v[214:217], v[20:23]
	v_mfma_f32_16x16x32_bf16 v[12:15], v[162:165], v[214:217], v[12:15]
	s_setprio 0
	s_setprio 1
	v_mfma_f32_16x16x32_bf16 v[48:51], v[166:169], v[182:185], v[48:51]
	v_mfma_f32_16x16x32_bf16 v[40:43], v[174:177], v[182:185], v[40:43]
	v_mfma_f32_16x16x32_bf16 v[32:35], v[166:169], v[194:197], v[32:35]
	v_mfma_f32_16x16x32_bf16 v[24:27], v[174:177], v[194:197], v[24:27]
	v_mfma_f32_16x16x32_bf16 v[16:19], v[166:169], v[202:205], v[16:19]
	v_mfma_f32_16x16x32_bf16 v[8:11], v[174:177], v[202:205], v[8:11]
	v_mfma_f32_16x16x32_bf16 v[4:7], v[166:169], v[210:213], v[4:7]
	v_mfma_f32_16x16x32_bf16 v[0:3], v[174:177], v[210:213], v[0:3]
	v_mfma_f32_16x16x32_bf16 v[48:51], v[170:173], v[190:193], v[48:51]
	v_mfma_f32_16x16x32_bf16 v[40:43], v[178:181], v[190:193], v[40:43]
	v_mfma_f32_16x16x32_bf16 v[32:35], v[170:173], v[198:201], v[32:35]
	v_mfma_f32_16x16x32_bf16 v[24:27], v[178:181], v[198:201], v[24:27]
	v_mfma_f32_16x16x32_bf16 v[16:19], v[170:173], v[206:209], v[16:19]
	v_mfma_f32_16x16x32_bf16 v[8:11], v[178:181], v[206:209], v[8:11]
	v_mfma_f32_16x16x32_bf16 v[4:7], v[170:173], v[214:217], v[4:7]
	v_mfma_f32_16x16x32_bf16 v[0:3], v[178:181], v[214:217], v[0:3]
	s_setprio 0
	s_barrier
	s_add_i32 s58, s58, 2
	s_add_u32 s24, s24, 0x100
	s_addc_u32 s25, s25, 0
	s_cmp_gt_u32 s58, 13
	s_cbranch_scc0 .LBB0_659
	s_add_u32 s24, s54, 0xffffff00
	s_addc_u32 s25, s55, -1
	s_andn2_b64 vcc, exec, s[10:11]
	s_cbranch_vccnz .LBB0_662
	v_mov_b32_e32 v0, 0
	s_mov_b32 s4, s14
	s_mov_b32 s3, s52
	s_mov_b64 s[6:7], s[22:23]
	s_mov_b32 s49, s53
	v_mov_b32_e32 v1, v0
	v_mov_b32_e32 v2, v0
	v_mov_b32_e32 v3, v0
	v_mov_b32_e32 v4, v0
	v_mov_b32_e32 v5, v0
	v_mov_b32_e32 v6, v0
	v_mov_b32_e32 v7, v0
	v_mov_b32_e32 v8, v0
	v_mov_b32_e32 v9, v0
	v_mov_b32_e32 v10, v0
	v_mov_b32_e32 v11, v0
	v_mov_b32_e32 v16, v0
	v_mov_b32_e32 v17, v0
	v_mov_b32_e32 v18, v0
	v_mov_b32_e32 v19, v0
	v_mov_b32_e32 v24, v0
	v_mov_b32_e32 v25, v0
	v_mov_b32_e32 v26, v0
	v_mov_b32_e32 v27, v0
	v_mov_b32_e32 v32, v0
	v_mov_b32_e32 v33, v0
	v_mov_b32_e32 v34, v0
	v_mov_b32_e32 v35, v0
	v_mov_b32_e32 v40, v0
	v_mov_b32_e32 v41, v0
	v_mov_b32_e32 v42, v0
	v_mov_b32_e32 v43, v0
	v_mov_b32_e32 v48, v0
	v_mov_b32_e32 v49, v0
	v_mov_b32_e32 v50, v0
	v_mov_b32_e32 v51, v0
	v_mov_b32_e32 v12, v0
	v_mov_b32_e32 v13, v0
	v_mov_b32_e32 v14, v0
	v_mov_b32_e32 v15, v0
	v_mov_b32_e32 v20, v0
	v_mov_b32_e32 v21, v0
	v_mov_b32_e32 v22, v0
	v_mov_b32_e32 v23, v0
	v_mov_b32_e32 v28, v0
	v_mov_b32_e32 v29, v0
	v_mov_b32_e32 v30, v0
	v_mov_b32_e32 v31, v0
	v_mov_b32_e32 v36, v0
	v_mov_b32_e32 v37, v0
	v_mov_b32_e32 v38, v0
	v_mov_b32_e32 v39, v0
	v_mov_b32_e32 v44, v0
	v_mov_b32_e32 v45, v0
	v_mov_b32_e32 v46, v0
	v_mov_b32_e32 v47, v0
	v_mov_b32_e32 v52, v0
	v_mov_b32_e32 v53, v0
	v_mov_b32_e32 v54, v0
	v_mov_b32_e32 v55, v0
	v_mov_b32_e32 v56, v0
	v_mov_b32_e32 v57, v0
	v_mov_b32_e32 v58, v0
	v_mov_b32_e32 v59, v0
	v_mov_b32_e32 v60, v0
	v_mov_b32_e32 v61, v0
	v_mov_b32_e32 v62, v0
	v_mov_b32_e32 v63, v0
	v_mov_b32_e32 v64, v0
	v_mov_b32_e32 v65, v0
	v_mov_b32_e32 v66, v0
	v_mov_b32_e32 v67, v0
	v_mov_b32_e32 v68, v0
	v_mov_b32_e32 v69, v0
	v_mov_b32_e32 v70, v0
	v_mov_b32_e32 v71, v0
	v_mov_b32_e32 v72, v0
	v_mov_b32_e32 v73, v0
	v_mov_b32_e32 v74, v0
	v_mov_b32_e32 v75, v0
	v_mov_b32_e32 v80, v0
	v_mov_b32_e32 v81, v0
	v_mov_b32_e32 v82, v0
	v_mov_b32_e32 v83, v0
	v_mov_b32_e32 v88, v0
	v_mov_b32_e32 v89, v0
	v_mov_b32_e32 v90, v0
	v_mov_b32_e32 v91, v0
	v_mov_b32_e32 v96, v0
	v_mov_b32_e32 v97, v0
	v_mov_b32_e32 v98, v0
	v_mov_b32_e32 v99, v0
	v_mov_b32_e32 v104, v0
	v_mov_b32_e32 v105, v0
	v_mov_b32_e32 v106, v0
	v_mov_b32_e32 v107, v0
	v_mov_b32_e32 v116, v0
	v_mov_b32_e32 v117, v0
	v_mov_b32_e32 v118, v0
	v_mov_b32_e32 v119, v0
	v_mov_b32_e32 v76, v0
	v_mov_b32_e32 v77, v0
	v_mov_b32_e32 v78, v0
	v_mov_b32_e32 v79, v0
	v_mov_b32_e32 v84, v0
	v_mov_b32_e32 v85, v0
	v_mov_b32_e32 v86, v0
	v_mov_b32_e32 v87, v0
	v_mov_b32_e32 v92, v0
	v_mov_b32_e32 v93, v0
	v_mov_b32_e32 v94, v0
	v_mov_b32_e32 v95, v0
	v_mov_b32_e32 v100, v0
	v_mov_b32_e32 v101, v0
	v_mov_b32_e32 v102, v0
	v_mov_b32_e32 v103, v0
	v_mov_b32_e32 v108, v0
	v_mov_b32_e32 v109, v0
	v_mov_b32_e32 v110, v0
	v_mov_b32_e32 v111, v0
	v_mov_b32_e32 v112, v0
	v_mov_b32_e32 v113, v0
	v_mov_b32_e32 v114, v0
	v_mov_b32_e32 v115, v0
	v_mov_b32_e32 v120, v0
	v_mov_b32_e32 v121, v0
	v_mov_b32_e32 v122, v0
	v_mov_b32_e32 v123, v0
	v_mov_b32_e32 v124, v0
	v_mov_b32_e32 v125, v0
	v_mov_b32_e32 v126, v0
	v_mov_b32_e32 v127, v0
	s_andn2_b64 vcc, exec, s[8:9]
	s_cbranch_vccnz .LBB0_663
	s_branch .LBB0_664

; __device__ __forceinline__ unsigned cvt_pk4_fp8(float a, float b, float c, float d) { int w = 0; w = __builtin_amdgcn_cvt_pk_fp8_f32(a, b, w, false); w = __builtin_amdgcn_cvt_pk_fp8_f32(c, d, w, true); return (unsigned)w; }
;     __device__ __forceinline__ void fused(f32x4 (&acc)[2][2][4][2], const Unit& u, int wr, int wc, int fr, int fq, PG8_LAS unsigned char* lds, int wid, int lane) const {
;     ...
;                     if constexpr (XN8) { const f32x4 ya = acc[ai][bj][m][0] * rs * gs[bj][0] + sh[bj][0], yb = acc[ai][bj][m][1] * rs * gs[bj][1] + sh[bj][1]; typedef unsigned u32x2 __attribute__((ext_vector_type(2)));
;                         u32x2 q; q.x = bad ? 0x7f7f7f7fu : cvt_pk4_fp8(ya[0], ya[1], ya[2], ya[3]); q.y = bad ? 0x7f7f7f7fu : cvt_pk4_fp8(yb[0], yb[1], yb[2], yb[3]); *(u32x2*)((unsigned char*)XN + off + bj * HALF) = q; }
.LBB0_757:
	v_cvt_pk_fp8_f32 v30, v140, v141
	v_cvt_pk_fp8_f32 v30, v138, v139 op_sel:[0,0,1]
	s_and_b64 vcc, exec, s[8:9]
	s_cbranch_vccnz .LBB0_712
.LBB0_758:
	v_cvt_pk_fp8_f32 v31, v28, v29
	v_cvt_pk_fp8_f32 v31, v20, v21 op_sel:[0,0,1]
	s_branch .LBB0_712
.LBB0_759:
	v_cvt_pk_fp8_f32 v28, v138, v139
	v_cvt_pk_fp8_f32 v28, v136, v137 op_sel:[0,0,1]
	s_and_b64 vcc, exec, s[8:9]
	v_mov_b32_e32 v21, v20
	s_cbranch_vccnz .LBB0_714
.LBB0_760:
	v_cvt_pk_fp8_f32 v29, v30, v31
	v_cvt_pk_fp8_f32 v29, v22, v23 op_sel:[0,0,1]
	s_branch .LBB0_714
.LBB0_761:
	v_cvt_pk_fp8_f32 v30, v138, v139
	v_cvt_pk_fp8_f32 v30, v136, v137 op_sel:[0,0,1]
	s_and_b64 vcc, exec, s[8:9]
	s_cbranch_vccnz .LBB0_716

; __device__ __forceinline__ unsigned cvt_pk4_fp8(float a, float b, float c, float d) { int w = 0; w = __builtin_amdgcn_cvt_pk_fp8_f32(a, b, w, false); w = __builtin_amdgcn_cvt_pk_fp8_f32(c, d, w, true); return (unsigned)w; }
;     __device__ __forceinline__ void fused(f32x4 (&acc)[2][2][4][2], const Unit& u, int wr, int wc, int fr, int fq, PG8_LAS unsigned char* lds, int wid, int lane) const {
;     ...
;                     if constexpr (XN8) { const f32x4 ya = acc[ai][bj][m][0] * rs * gs[bj][0] + sh[bj][0], yb = acc[ai][bj][m][1] * rs * gs[bj][1] + sh[bj][1]; typedef unsigned u32x2 __attribute__((ext_vector_type(2)));
;                         u32x2 q; q.x = bad ? 0x7f7f7f7fu : cvt_pk4_fp8(ya[0], ya[1], ya[2], ya[3]); q.y = bad ? 0x7f7f7f7fu : cvt_pk4_fp8(yb[0], yb[1], yb[2], yb[3]); *(u32x2*)((unsigned char*)XN + off + bj * HALF) = q; }
.LBB0_763:
	v_cvt_pk_fp8_f32 v28, v124, v125
	v_cvt_pk_fp8_f32 v28, v122, v123 op_sel:[0,0,1]
	s_and_b64 vcc, exec, s[8:9]
	v_mov_b32_e32 v21, v20
	s_cbranch_vccnz .LBB0_718

; __device__ __forceinline__ unsigned cvt_pk4_fp8(float a, float b, float c, float d) { int w = 0; w = __builtin_amdgcn_cvt_pk_fp8_f32(a, b, w, false); w = __builtin_amdgcn_cvt_pk_fp8_f32(c, d, w, true); return (unsigned)w; }
;     __device__ __forceinline__ void fused(f32x4 (&acc)[2][2][4][2], const Unit& u, int wr, int wc, int fr, int fq, PG8_LAS unsigned char* lds, int wid, int lane) const {
;     ...
;                     if constexpr (XN8) { const f32x4 ya = acc[ai][bj][m][0] * rs * gs[bj][0] + sh[bj][0], yb = acc[ai][bj][m][1] * rs * gs[bj][1] + sh[bj][1]; typedef unsigned u32x2 __attribute__((ext_vector_type(2)));
;                         u32x2 q; q.x = bad ? 0x7f7f7f7fu : cvt_pk4_fp8(ya[0], ya[1], ya[2], ya[3]); q.y = bad ? 0x7f7f7f7fu : cvt_pk4_fp8(yb[0], yb[1], yb[2], yb[3]); *(u32x2*)((unsigned char*)XN + off + bj * HALF) = q; }
.LBB0_765:
	v_cvt_pk_fp8_f32 v30, v118, v119
	v_cvt_pk_fp8_f32 v30, v114, v115 op_sel:[0,0,1]
	s_and_b64 vcc, exec, s[8:9]
	s_cbranch_vccnz .LBB0_720

; __device__ __forceinline__ unsigned cvt_pk4_fp8(float a, float b, float c, float d) { int w = 0; w = __builtin_amdgcn_cvt_pk_fp8_f32(a, b, w, false); w = __builtin_amdgcn_cvt_pk_fp8_f32(c, d, w, true); return (unsigned)w; }
;     __device__ __forceinline__ void fused(f32x4 (&acc)[2][2][4][2], const Unit& u, int wr, int wc, int fr, int fq, PG8_LAS unsigned char* lds, int wid, int lane) const {
;     ...
;                     if constexpr (XN8) { const f32x4 ya = acc[ai][bj][m][0] * rs * gs[bj][0] + sh[bj][0], yb = acc[ai][bj][m][1] * rs * gs[bj][1] + sh[bj][1]; typedef unsigned u32x2 __attribute__((ext_vector_type(2)));
;                         u32x2 q; q.x = bad ? 0x7f7f7f7fu : cvt_pk4_fp8(ya[0], ya[1], ya[2], ya[3]); q.y = bad ? 0x7f7f7f7fu : cvt_pk4_fp8(yb[0], yb[1], yb[2], yb[3]); *(u32x2*)((unsigned char*)XN + off + bj * HALF) = q; }
.LBB0_767:
	v_cvt_pk_fp8_f32 v28, v108, v109
	v_cvt_pk_fp8_f32 v28, v106, v107 op_sel:[0,0,1]
	s_and_b64 vcc, exec, s[8:9]
	v_mov_b32_e32 v21, v20
	s_cbranch_vccnz .LBB0_722

; __device__ __forceinline__ unsigned cvt_pk4_fp8(float a, float b, float c, float d) { int w = 0; w = __builtin_amdgcn_cvt_pk_fp8_f32(a, b, w, false); w = __builtin_amdgcn_cvt_pk_fp8_f32(c, d, w, true); return (unsigned)w; }
;     __device__ __forceinline__ void fused(f32x4 (&acc)[2][2][4][2], const Unit& u, int wr, int wc, int fr, int fq, PG8_LAS unsigned char* lds, int wid, int lane) const {
;     ...
;                     if constexpr (XN8) { const f32x4 ya = acc[ai][bj][m][0] * rs * gs[bj][0] + sh[bj][0], yb = acc[ai][bj][m][1] * rs * gs[bj][1] + sh[bj][1]; typedef unsigned u32x2 __attribute__((ext_vector_type(2)));
;                         u32x2 q; q.x = bad ? 0x7f7f7f7fu : cvt_pk4_fp8(ya[0], ya[1], ya[2], ya[3]); q.y = bad ? 0x7f7f7f7fu : cvt_pk4_fp8(yb[0], yb[1], yb[2], yb[3]); *(u32x2*)((unsigned char*)XN + off + bj * HALF) = q; }
.LBB0_769:
	v_cvt_pk_fp8_f32 v30, v94, v95
	v_cvt_pk_fp8_f32 v30, v90, v91 op_sel:[0,0,1]
	s_and_b64 vcc, exec, s[8:9]
	s_cbranch_vccnz .LBB0_724

; __device__ __forceinline__ unsigned cvt_pk4_fp8(float a, float b, float c, float d) { int w = 0; w = __builtin_amdgcn_cvt_pk_fp8_f32(a, b, w, false); w = __builtin_amdgcn_cvt_pk_fp8_f32(c, d, w, true); return (unsigned)w; }
;     __device__ __forceinline__ void fused(f32x4 (&acc)[2][2][4][2], const Unit& u, int wr, int wc, int fr, int fq, PG8_LAS unsigned char* lds, int wid, int lane) const {
;     ...
;                     if constexpr (XN8) { const f32x4 ya = acc[ai][bj][m][0] * rs * gs[bj][0] + sh[bj][0], yb = acc[ai][bj][m][1] * rs * gs[bj][1] + sh[bj][1]; typedef unsigned u32x2 __attribute__((ext_vector_type(2)));
;                         u32x2 q; q.x = bad ? 0x7f7f7f7fu : cvt_pk4_fp8(ya[0], ya[1], ya[2], ya[3]); q.y = bad ? 0x7f7f7f7fu : cvt_pk4_fp8(yb[0], yb[1], yb[2], yb[3]); *(u32x2*)((unsigned char*)XN + off + bj * HALF) = q; }
.LBB0_771:
	v_cvt_pk_fp8_f32 v28, v90, v91
	v_cvt_pk_fp8_f32 v28, v88, v89 op_sel:[0,0,1]
	s_and_b64 vcc, exec, s[8:9]
	v_mov_b32_e32 v21, v20
	s_cbranch_vccnz .LBB0_726

; __device__ __forceinline__ unsigned cvt_pk4_fp8(float a, float b, float c, float d) { int w = 0; w = __builtin_amdgcn_cvt_pk_fp8_f32(a, b, w, false); w = __builtin_amdgcn_cvt_pk_fp8_f32(c, d, w, true); return (unsigned)w; }
;     __device__ __forceinline__ void fused(f32x4 (&acc)[2][2][4][2], const Unit& u, int wr, int wc, int fr, int fq, PG8_LAS unsigned char* lds, int wid, int lane) const {
;     ...
;                     if constexpr (XN8) { const f32x4 ya = acc[ai][bj][m][0] * rs * gs[bj][0] + sh[bj][0], yb = acc[ai][bj][m][1] * rs * gs[bj][1] + sh[bj][1]; typedef unsigned u32x2 __attribute__((ext_vector_type(2)));
;                         u32x2 q; q.x = bad ? 0x7f7f7f7fu : cvt_pk4_fp8(ya[0], ya[1], ya[2], ya[3]); q.y = bad ? 0x7f7f7f7fu : cvt_pk4_fp8(yb[0], yb[1], yb[2], yb[3]); *(u32x2*)((unsigned char*)XN + off + bj * HALF) = q; }
.LBB0_773:
	v_cvt_pk_fp8_f32 v30, v86, v87
	v_cvt_pk_fp8_f32 v30, v82, v83 op_sel:[0,0,1]
	s_and_b64 vcc, exec, s[8:9]
	s_cbranch_vccnz .LBB0_728

; __device__ __forceinline__ unsigned cvt_pk4_fp8(float a, float b, float c, float d) { int w = 0; w = __builtin_amdgcn_cvt_pk_fp8_f32(a, b, w, false); w = __builtin_amdgcn_cvt_pk_fp8_f32(c, d, w, true); return (unsigned)w; }
;     __device__ __forceinline__ void fused(f32x4 (&acc)[2][2][4][2], const Unit& u, int wr, int wc, int fr, int fq, PG8_LAS unsigned char* lds, int wid, int lane) const {
;     ...
;                     if constexpr (XN8) { const f32x4 ya = acc[ai][bj][m][0] * rs * gs[bj][0] + sh[bj][0], yb = acc[ai][bj][m][1] * rs * gs[bj][1] + sh[bj][1]; typedef unsigned u32x2 __attribute__((ext_vector_type(2)));
;                         u32x2 q; q.x = bad ? 0x7f7f7f7fu : cvt_pk4_fp8(ya[0], ya[1], ya[2], ya[3]); q.y = bad ? 0x7f7f7f7fu : cvt_pk4_fp8(yb[0], yb[1], yb[2], yb[3]); *(u32x2*)((unsigned char*)XN + off + bj * HALF) = q; }
.LBB0_775:
	v_cvt_pk_fp8_f32 v28, v76, v77
	v_cvt_pk_fp8_f32 v28, v74, v75 op_sel:[0,0,1]
	s_and_b64 vcc, exec, s[8:9]
	v_mov_b32_e32 v21, v20
	s_cbranch_vccnz .LBB0_730

; __device__ __forceinline__ unsigned cvt_pk4_fp8(float a, float b, float c, float d) { int w = 0; w = __builtin_amdgcn_cvt_pk_fp8_f32(a, b, w, false); w = __builtin_amdgcn_cvt_pk_fp8_f32(c, d, w, true); return (unsigned)w; }
;     __device__ __forceinline__ void fused(f32x4 (&acc)[2][2][4][2], const Unit& u, int wr, int wc, int fr, int fq, PG8_LAS unsigned char* lds, int wid, int lane) const {
;     ...
;                     if constexpr (XN8) { const f32x4 ya = acc[ai][bj][m][0] * rs * gs[bj][0] + sh[bj][0], yb = acc[ai][bj][m][1] * rs * gs[bj][1] + sh[bj][1]; typedef unsigned u32x2 __attribute__((ext_vector_type(2)));
;                         u32x2 q; q.x = bad ? 0x7f7f7f7fu : cvt_pk4_fp8(ya[0], ya[1], ya[2], ya[3]); q.y = bad ? 0x7f7f7f7fu : cvt_pk4_fp8(yb[0], yb[1], yb[2], yb[3]); *(u32x2*)((unsigned char*)XN + off + bj * HALF) = q; }
.LBB0_777:
	v_cvt_pk_fp8_f32 v30, v70, v71
	v_cvt_pk_fp8_f32 v30, v66, v67 op_sel:[0,0,1]
	s_and_b64 vcc, exec, s[8:9]
	s_cbranch_vccnz .LBB0_732

; __device__ __forceinline__ unsigned cvt_pk4_fp8(float a, float b, float c, float d) { int w = 0; w = __builtin_amdgcn_cvt_pk_fp8_f32(a, b, w, false); w = __builtin_amdgcn_cvt_pk_fp8_f32(c, d, w, true); return (unsigned)w; }
;     __device__ __forceinline__ void fused(f32x4 (&acc)[2][2][4][2], const Unit& u, int wr, int wc, int fr, int fq, PG8_LAS unsigned char* lds, int wid, int lane) const {
;     ...
;                     if constexpr (XN8) { const f32x4 ya = acc[ai][bj][m][0] * rs * gs[bj][0] + sh[bj][0], yb = acc[ai][bj][m][1] * rs * gs[bj][1] + sh[bj][1]; typedef unsigned u32x2 __attribute__((ext_vector_type(2)));
;                         u32x2 q; q.x = bad ? 0x7f7f7f7fu : cvt_pk4_fp8(ya[0], ya[1], ya[2], ya[3]); q.y = bad ? 0x7f7f7f7fu : cvt_pk4_fp8(yb[0], yb[1], yb[2], yb[3]); *(u32x2*)((unsigned char*)XN + off + bj * HALF) = q; }
.LBB0_779:
	v_cvt_pk_fp8_f32 v28, v60, v61
	v_cvt_pk_fp8_f32 v28, v58, v59 op_sel:[0,0,1]
	s_and_b64 vcc, exec, s[8:9]
	v_mov_b32_e32 v21, v20
	s_cbranch_vccnz .LBB0_734

; __device__ __forceinline__ unsigned cvt_pk4_fp8(float a, float b, float c, float d) { int w = 0; w = __builtin_amdgcn_cvt_pk_fp8_f32(a, b, w, false); w = __builtin_amdgcn_cvt_pk_fp8_f32(c, d, w, true); return (unsigned)w; }
;     __device__ __forceinline__ void fused(f32x4 (&acc)[2][2][4][2], const Unit& u, int wr, int wc, int fr, int fq, PG8_LAS unsigned char* lds, int wid, int lane) const {
;     ...
;                     if constexpr (XN8) { const f32x4 ya = acc[ai][bj][m][0] * rs * gs[bj][0] + sh[bj][0], yb = acc[ai][bj][m][1] * rs * gs[bj][1] + sh[bj][1]; typedef unsigned u32x2 __attribute__((ext_vector_type(2)));
;                         u32x2 q; q.x = bad ? 0x7f7f7f7fu : cvt_pk4_fp8(ya[0], ya[1], ya[2], ya[3]); q.y = bad ? 0x7f7f7f7fu : cvt_pk4_fp8(yb[0], yb[1], yb[2], yb[3]); *(u32x2*)((unsigned char*)XN + off + bj * HALF) = q; }
.LBB0_781:
	v_cvt_pk_fp8_f32 v30, v54, v55
	v_cvt_pk_fp8_f32 v30, v50, v51 op_sel:[0,0,1]
	s_and_b64 vcc, exec, s[8:9]
	s_cbranch_vccnz .LBB0_736

; __device__ __forceinline__ unsigned cvt_pk4_fp8(float a, float b, float c, float d) { int w = 0; w = __builtin_amdgcn_cvt_pk_fp8_f32(a, b, w, false); w = __builtin_amdgcn_cvt_pk_fp8_f32(c, d, w, true); return (unsigned)w; }
;     __device__ __forceinline__ void fused(f32x4 (&acc)[2][2][4][2], const Unit& u, int wr, int wc, int fr, int fq, PG8_LAS unsigned char* lds, int wid, int lane) const {
;     ...
;                     if constexpr (XN8) { const f32x4 ya = acc[ai][bj][m][0] * rs * gs[bj][0] + sh[bj][0], yb = acc[ai][bj][m][1] * rs * gs[bj][1] + sh[bj][1]; typedef unsigned u32x2 __attribute__((ext_vector_type(2)));
;                         u32x2 q; q.x = bad ? 0x7f7f7f7fu : cvt_pk4_fp8(ya[0], ya[1], ya[2], ya[3]); q.y = bad ? 0x7f7f7f7fu : cvt_pk4_fp8(yb[0], yb[1], yb[2], yb[3]); *(u32x2*)((unsigned char*)XN + off + bj * HALF) = q; }
.LBB0_783:
	v_cvt_pk_fp8_f32 v12, v22, v23
	v_cvt_pk_fp8_f32 v12, v14, v15 op_sel:[0,0,1]
	s_and_b64 vcc, exec, s[8:9]
	v_mov_b32_e32 v21, v20
	s_cbranch_vccnz .LBB0_738
.LBB0_784:
	v_cvt_pk_fp8_f32 v13, v8, v9
	v_cvt_pk_fp8_f32 v13, v10, v11 op_sel:[0,0,1]
	s_branch .LBB0_738
.LBB0_785:
	v_cvt_pk_fp8_f32 v10, v4, v5
	v_cvt_pk_fp8_f32 v10, v6, v7 op_sel:[0,0,1]
	s_and_b64 vcc, exec, s[8:9]
	s_cbranch_vccnz .LBB0_740
.LBB0_786:
	v_cvt_pk_fp8_f32 v11, v0, v1
	v_cvt_pk_fp8_f32 v11, v2, v3 op_sel:[0,0,1]
	s_branch .LBB0_740

; #define PG8_STAGE(bufoff, gbase, voff) do { _Pragma("unroll") for (int _i = 0; _i < 2; ++_i) \
;         __builtin_amdgcn_global_load_lds((const unsigned*)((const char*)(gbase) + (voff)[_i]), (PG8_LAS unsigned*)(lds + (bufoff) + ldsw + _i * 8192), 16, 0, 0); } while (0)
; #define PG8_WAIT_V(n) asm volatile("s_waitcnt vmcnt(" #n ")" ::: "memory")
; #define PG8_WAIT_L(n) asm volatile("s_waitcnt lgkmcnt(" #n ")" ::: "memory")
; #define PG8_BAR __builtin_amdgcn_s_barrier()
; #define PG8_SCHED __builtin_amdgcn_sched_barrier(0)
; template <class Epi, class Sched, bool ALIGN_EPI = false, bool SP2 = false, bool FP8 = false, bool PEEL = false>
; __device__ __forceinline__ void gemm_phase(PG8_LAS unsigned char* lds, const Gemm g, const Sched& S, const Epi& E, const int wid) {
;     ...
;         const char* nA = has_next ? (const char*)g.A + (size_t)nxt.pm * tstep + nxt.koff : cA; const char* nB = has_next ? (const char*)g.Bt + (size_t)nxt.pn * tstep + nxt.koff : cB;
;         if constexpr (SP2 && PEEL) {
;         {
;             const int t = 0;
;             const bool last = (t == nt - 2);
;             const char* a1 = cA + (size_t)(t + 1) * kstep;
;             const char* a2 = last ? nA : cA + (size_t)(t + 2) * kstep; const char* b2 = last ? nB : cB + (size_t)(t + 2) * kstep;
;             const char* a3 = a2 + kstep; const char* b3 = b2 + kstep;
;             if (last && has_next) S.a_ready(nxt);
;             PG8_LDB(B0, 0, 0); PG8_LDB(B1, 0, 1); PG8_SCHED; PG8_LDA(At, 0, 0); PG8_STAGE(PG8_SA(1, 1), a1 + hstep, voffA);
;             PG8_WAIT_V(8); PG8_WAIT_L(0); PG8_BAR; PG8_MMAZ(0, 0, At, B0); PG8_MMAZ(0, 1, At, B1); PG8_BAR; PG8_SCHED;
;             PG8_LDA(At, 0, 1); PG8_STAGE(PG8_SB(0, 0), b2, voffB); PG8_STAGE(PG8_SB(0, 1), b2 + hstep, voffB); PG8_STAGE(PG8_SA(0, 0), a2, voffA);
;             PG8_WAIT_V(8); PG8_WAIT_L(0); PG8_BAR; PG8_MMAZ(1, 0, At, B0); PG8_MMAZ(1, 1, At, B1); PG8_BAR; PG8_SCHED;
;             PG8_LDB(B0, 1, 0); PG8_LDB(B1, 1, 1); PG8_SCHED; PG8_LDA(At, 1, 0); PG8_STAGE(PG8_SA(0, 1), a2 + hstep, voffA);
.LBB0_866:
	s_ashr_i32 s27, s26, 31
	s_lshl_b64 s[30:31], s[26:27], 18
	v_add_u32_e32 v188, s56, v185
	v_add_u32_e32 v189, s57, v185
	s_add_u32 s30, s38, s30
	ds_read_b128 v[16:19], v188
	ds_read_b128 v[20:23], v188 offset:1024
	ds_read_b128 v[24:27], v188 offset:2048
	ds_read_b128 v[28:31], v188 offset:3072
	ds_read_b128 v[0:3], v189
	ds_read_b128 v[4:7], v189 offset:1024
	ds_read_b128 v[8:11], v189 offset:2048
	ds_read_b128 v[12:15], v189 offset:3072
	s_addc_u32 s31, s39, s31
	s_ashr_i32 s25, s24, 31
	s_lshl_b64 s[36:37], s[24:25], 18
	s_add_u32 s36, s3, s36
	s_addc_u32 s37, s17, s37
	s_and_b64 s[48:49], s[8:9], exec
	s_cselect_b32 s25, s31, s47
	s_cselect_b32 s27, s30, s46
	s_cselect_b32 s63, s37, s45
	s_cselect_b32 s64, s36, s44
	s_add_u32 s48, s46, 0x20080
	s_addc_u32 s49, s47, 0
	s_mov_b32 m0, s59
	v_lshl_add_u64 v[214:215], s[48:49], 0, v[166:167]
	s_add_i32 s65, s42, 0xe000
	ds_read_b128 v[176:179], v187
	ds_read_b128 v[180:183], v187 offset:1024
	ds_read_b128 v[190:193], v187 offset:2048
	ds_read_b128 v[194:197], v187 offset:3072
	ds_read_b128 v[198:201], v187 offset:4096
	ds_read_b128 v[202:205], v187 offset:5120
	ds_read_b128 v[206:209], v187 offset:6144
	ds_read_b128 v[210:213], v187 offset:7168
	global_load_lds_dwordx4 v[214:215], off
	v_lshl_add_u64 v[214:215], s[48:49], 0, v[162:163]
	s_mov_b32 m0, s65
	s_nop 0
	global_load_lds_dwordx4 v[214:215], off
	s_waitcnt vmcnt(8)
	s_waitcnt lgkmcnt(0)
	s_barrier
	s_setprio 1
	v_mfma_f32_16x16x128_f8f6f4 v[156:159], v[16:23], v[176:183], 0
	v_mfma_f32_16x16x128_f8f6f4 v[152:155], v[24:31], v[176:183], 0
	v_mfma_f32_16x16x128_f8f6f4 v[148:151], v[16:23], v[190:197], 0
	v_mfma_f32_16x16x128_f8f6f4 v[144:147], v[24:31], v[190:197], 0
	v_mfma_f32_16x16x128_f8f6f4 v[140:143], v[16:23], v[198:205], 0
	v_mfma_f32_16x16x128_f8f6f4 v[136:139], v[24:31], v[198:205], 0
	v_mfma_f32_16x16x128_f8f6f4 v[132:135], v[16:23], v[206:213], 0
	v_mfma_f32_16x16x128_f8f6f4 v[128:131], v[24:31], v[206:213], 0
	s_setprio 0
	s_setprio 1
	v_mfma_f32_16x16x128_f8f6f4 v[124:127], v[0:7], v[176:183], 0
	v_mfma_f32_16x16x128_f8f6f4 v[120:123], v[8:15], v[176:183], 0
	v_mfma_f32_16x16x128_f8f6f4 v[116:119], v[0:7], v[190:197], 0
	v_mfma_f32_16x16x128_f8f6f4 v[112:115], v[8:15], v[190:197], 0
	v_mfma_f32_16x16x128_f8f6f4 v[108:111], v[0:7], v[198:205], 0
	v_mfma_f32_16x16x128_f8f6f4 v[104:107], v[8:15], v[198:205], 0
	v_mfma_f32_16x16x128_f8f6f4 v[100:103], v[0:7], v[206:213], 0
	v_mfma_f32_16x16x128_f8f6f4 v[96:99], v[8:15], v[206:213], 0
	s_setprio 0
	s_barrier
	v_lshl_add_u64 v[176:177], s[44:45], 0, v[164:165]
	s_add_i32 s66, s56, s23
	v_lshl_add_u64 v[178:179], v[176:177], 0, s[12:13]
	s_mov_b32 m0, s66
	s_add_i32 s67, s66, 0x2000
	ds_read_b128 v[190:193], v187 offset:16384
	ds_read_b128 v[194:197], v187 offset:17408
	ds_read_b128 v[198:201], v187 offset:18432
	ds_read_b128 v[202:205], v187 offset:19456
	ds_read_b128 v[206:209], v187 offset:20480
	ds_read_b128 v[210:213], v187 offset:21504
	ds_read_b128 v[214:217], v187 offset:22528
	ds_read_b128 v[218:221], v187 offset:23552
	global_load_lds_dwordx4 v[178:179], off
	v_lshl_add_u64 v[178:179], s[44:45], 0, v[160:161]
	s_add_u32 s48, s44, 0x20100
	v_lshl_add_u64 v[180:181], v[178:179], 0, s[12:13]
	s_mov_b32 m0, s67
	s_addc_u32 s49, s45, 0
	s_add_i32 s75, s57, s23
	global_load_lds_dwordx4 v[180:181], off
	v_lshl_add_u64 v[180:181], s[48:49], 0, v[164:165]
	s_mov_b32 m0, s75
	s_add_i32 s84, s75, 0x2000
	global_load_lds_dwordx4 v[180:181], off
	v_lshl_add_u64 v[180:181], s[48:49], 0, v[160:161]
	s_mov_b32 m0, s84
	s_nop 0
	global_load_lds_dwordx4 v[180:181], off
	v_lshl_add_u64 v[180:181], s[46:47], 0, v[166:167]
	v_lshl_add_u64 v[182:183], v[180:181], 0, s[12:13]
	s_mov_b32 m0, s42
	s_nop 0
	global_load_lds_dwordx4 v[182:183], off
	v_lshl_add_u64 v[182:183], s[46:47], 0, v[162:163]
	v_lshl_add_u64 v[222:223], v[182:183], 0, s[12:13]
	s_mov_b32 m0, s43
	s_nop 0
	global_load_lds_dwordx4 v[222:223], off
	s_waitcnt vmcnt(8)
	s_waitcnt lgkmcnt(0)
	s_barrier
	s_setprio 1
	v_mfma_f32_16x16x128_f8f6f4 v[92:95], v[16:23], v[190:197], 0
	v_mfma_f32_16x16x128_f8f6f4 v[88:91], v[24:31], v[190:197], 0
	v_mfma_f32_16x16x128_f8f6f4 v[84:87], v[16:23], v[198:205], 0
	v_mfma_f32_16x16x128_f8f6f4 v[80:83], v[24:31], v[198:205], 0
	v_mfma_f32_16x16x128_f8f6f4 v[76:79], v[16:23], v[206:213], 0
	v_mfma_f32_16x16x128_f8f6f4 v[72:75], v[24:31], v[206:213], 0
	v_mfma_f32_16x16x128_f8f6f4 v[68:71], v[16:23], v[214:221], 0
	v_mfma_f32_16x16x128_f8f6f4 v[64:67], v[24:31], v[214:221], 0
	s_setprio 0
	s_setprio 1
	v_mfma_f32_16x16x128_f8f6f4 v[60:63], v[0:7], v[190:197], 0
	v_mfma_f32_16x16x128_f8f6f4 v[56:59], v[8:15], v[190:197], 0
	v_mfma_f32_16x16x128_f8f6f4 v[52:55], v[0:7], v[198:205], 0
	v_mfma_f32_16x16x128_f8f6f4 v[48:51], v[8:15], v[198:205], 0
	v_mfma_f32_16x16x128_f8f6f4 v[44:47], v[0:7], v[206:213], 0
	v_mfma_f32_16x16x128_f8f6f4 v[40:43], v[8:15], v[206:213], 0
	v_mfma_f32_16x16x128_f8f6f4 v[36:39], v[0:7], v[214:221], 0
	v_mfma_f32_16x16x128_f8f6f4 v[32:35], v[8:15], v[214:221], 0
	s_setprio 0
	s_barrier
	s_add_i32 s85, 0, 0x18000
	s_add_i32 s87, 0, 0x1c000
	v_add_u32_e32 v190, s85, v185
	v_add_u32_e32 v191, s87, v185
	ds_read_b128 v[16:19], v190
	ds_read_b128 v[20:23], v190 offset:1024
	ds_read_b128 v[24:27], v190 offset:2048
	ds_read_b128 v[28:31], v190 offset:3072
	ds_read_b128 v[0:3], v191
	ds_read_b128 v[4:7], v191 offset:1024
	ds_read_b128 v[8:11], v191 offset:2048
	ds_read_b128 v[12:15], v191 offset:3072
	s_add_u32 s48, s46, 0x20100
	s_addc_u32 s49, s47, 0
	s_mov_b32 m0, s50
	v_lshl_add_u64 v[224:225], s[48:49], 0, v[166:167]
	ds_read_b128 v[192:195], v187 offset:32768
	ds_read_b128 v[196:199], v187 offset:33792
	ds_read_b128 v[200:203], v187 offset:34816
	ds_read_b128 v[204:207], v187 offset:35840
	ds_read_b128 v[208:211], v187 offset:36864
	ds_read_b128 v[212:215], v187 offset:37888
	ds_read_b128 v[216:219], v187 offset:38912
	ds_read_b128 v[220:223], v187 offset:39936
	global_load_lds_dwordx4 v[224:225], off
	v_lshl_add_u64 v[224:225], s[48:49], 0, v[162:163]
	s_mov_b32 m0, s51
	s_nop 0
	global_load_lds_dwordx4 v[224:225], off
	s_waitcnt vmcnt(8)
	s_waitcnt lgkmcnt(0)
	s_barrier
; #define PG8_STAGE(bufoff, gbase, voff) do { _Pragma("unroll") for (int _i = 0; _i < 2; ++_i) \
;         __builtin_amdgcn_global_load_lds((const unsigned*)((const char*)(gbase) + (voff)[_i]), (PG8_LAS unsigned*)(lds + (bufoff) + ldsw + _i * 8192), 16, 0, 0); } while (0)
; #define PG8_WAIT_V(n) asm volatile("s_waitcnt vmcnt(" #n ")" ::: "memory")
; #define PG8_WAIT_L(n) asm volatile("s_waitcnt lgkmcnt(" #n ")" ::: "memory")
; #define PG8_BAR __builtin_amdgcn_s_barrier()
; #define PG8_SCHED __builtin_amdgcn_sched_barrier(0)
; template <class Epi, class Sched, bool ALIGN_EPI = false, bool SP2 = false, bool FP8 = false, bool PEEL = false>
; __device__ __forceinline__ void gemm_phase(PG8_LAS unsigned char* lds, const Gemm g, const Sched& S, const Epi& E, const int wid) {
;     ...
;             PG8_WAIT_V(8); PG8_WAIT_L(0); PG8_BAR; PG8_MMA(0, 0, At, B0); PG8_MMA(0, 1, At, B1); PG8_BAR; PG8_SCHED;
;             PG8_LDA(At, 1, 1); PG8_STAGE(PG8_SB(1, 0), b3, voffB); PG8_STAGE(PG8_SB(1, 1), b3 + hstep, voffB); PG8_STAGE(PG8_SA(1, 0), a3, voffA);
;             PG8_WAIT_V(8); PG8_WAIT_L(0); PG8_BAR; PG8_MMA(1, 0, At, B0); PG8_MMA(1, 1, At, B1); PG8_BAR; PG8_SCHED;
;         }
; #pragma unroll 1
;         for (int t = 2; t < nt; t += 2) {
;             const bool last = (t == nt - 2);
;             const char* a1 = cA + (size_t)(t + 1) * kstep;
;             const char* a2 = last ? nA : cA + (size_t)(t + 2) * kstep; const char* b2 = last ? nB : cB + (size_t)(t + 2) * kstep;
;             const char* a3 = a2 + kstep; const char* b3 = b2 + kstep;
;             if (last && has_next) S.a_ready(nxt);
;             PG8_LDB(B0, 0, 0); PG8_LDB(B1, 0, 1); PG8_SCHED; PG8_LDA(At, 0, 0); PG8_STAGE(PG8_SA(1, 1), a1 + hstep, voffA);
;             PG8_WAIT_V(8); PG8_WAIT_L(0); PG8_BAR; PG8_MMA(0, 0, At, B0); PG8_MMA(0, 1, At, B1); PG8_BAR; PG8_SCHED;
	s_setprio 1
	v_mfma_f32_16x16x128_f8f6f4 v[156:159], v[16:23], v[192:199], v[156:159]
	v_mfma_f32_16x16x128_f8f6f4 v[152:155], v[24:31], v[192:199], v[152:155]
	v_mfma_f32_16x16x128_f8f6f4 v[148:151], v[16:23], v[200:207], v[148:151]
	v_mfma_f32_16x16x128_f8f6f4 v[144:147], v[24:31], v[200:207], v[144:147]
	v_mfma_f32_16x16x128_f8f6f4 v[140:143], v[16:23], v[208:215], v[140:143]
	v_mfma_f32_16x16x128_f8f6f4 v[136:139], v[24:31], v[208:215], v[136:139]
	v_mfma_f32_16x16x128_f8f6f4 v[132:135], v[16:23], v[216:223], v[132:135]
	v_mfma_f32_16x16x128_f8f6f4 v[128:131], v[24:31], v[216:223], v[128:131]
	s_setprio 0
	s_setprio 1
	v_mfma_f32_16x16x128_f8f6f4 v[124:127], v[0:7], v[192:199], v[124:127]
	v_mfma_f32_16x16x128_f8f6f4 v[120:123], v[8:15], v[192:199], v[120:123]
	v_mfma_f32_16x16x128_f8f6f4 v[116:119], v[0:7], v[200:207], v[116:119]
	v_mfma_f32_16x16x128_f8f6f4 v[112:115], v[8:15], v[200:207], v[112:115]
	v_mfma_f32_16x16x128_f8f6f4 v[108:111], v[0:7], v[208:215], v[108:111]
	v_mfma_f32_16x16x128_f8f6f4 v[104:107], v[8:15], v[208:215], v[104:107]
	v_mfma_f32_16x16x128_f8f6f4 v[100:103], v[0:7], v[216:223], v[100:103]
	v_mfma_f32_16x16x128_f8f6f4 v[96:99], v[8:15], v[216:223], v[96:99]
	s_setprio 0
	s_barrier
	s_add_i32 s85, s85, s23
	s_add_i32 s86, s85, 0x2000
	v_lshl_add_u64 v[176:177], v[176:177], 0, s[14:15]
	s_mov_b32 m0, s85
	s_add_u32 s48, s44, 0x20180
	ds_read_b128 v[192:195], v187 offset:49152
	ds_read_b128 v[196:199], v187 offset:50176
	ds_read_b128 v[200:203], v187 offset:51200
	ds_read_b128 v[204:207], v187 offset:52224
	ds_read_b128 v[208:211], v187 offset:53248
	ds_read_b128 v[212:215], v187 offset:54272
	ds_read_b128 v[216:219], v187 offset:55296
	ds_read_b128 v[220:223], v187 offset:56320
	global_load_lds_dwordx4 v[176:177], off
	v_lshl_add_u64 v[176:177], v[178:179], 0, s[14:15]
	s_mov_b32 m0, s86
	s_addc_u32 s49, s45, 0
	s_add_i32 s87, s87, s23
	global_load_lds_dwordx4 v[176:177], off
	v_lshl_add_u64 v[176:177], s[48:49], 0, v[164:165]
	s_mov_b32 m0, s87
	s_add_i32 s88, s87, 0x2000
	global_load_lds_dwordx4 v[176:177], off
	v_lshl_add_u64 v[176:177], s[48:49], 0, v[160:161]
	s_mov_b32 m0, s88
	s_nop 0
	global_load_lds_dwordx4 v[176:177], off
	v_lshl_add_u64 v[176:177], v[180:181], 0, s[14:15]
	s_mov_b32 m0, s54
	s_nop 0
	global_load_lds_dwordx4 v[176:177], off
	v_lshl_add_u64 v[176:177], v[182:183], 0, s[14:15]
	s_mov_b32 m0, s55
	s_nop 0
	global_load_lds_dwordx4 v[176:177], off
	s_waitcnt vmcnt(8)
	s_waitcnt lgkmcnt(0)
	s_barrier
	s_setprio 1
	v_mfma_f32_16x16x128_f8f6f4 v[92:95], v[16:23], v[192:199], v[92:95]
	v_mfma_f32_16x16x128_f8f6f4 v[88:91], v[24:31], v[192:199], v[88:91]
	v_mfma_f32_16x16x128_f8f6f4 v[84:87], v[16:23], v[200:207], v[84:87]
	v_mfma_f32_16x16x128_f8f6f4 v[80:83], v[24:31], v[200:207], v[80:83]
	v_mfma_f32_16x16x128_f8f6f4 v[76:79], v[16:23], v[208:215], v[76:79]
	v_mfma_f32_16x16x128_f8f6f4 v[72:75], v[24:31], v[208:215], v[72:75]
	v_mfma_f32_16x16x128_f8f6f4 v[68:71], v[16:23], v[216:223], v[68:71]
	v_mfma_f32_16x16x128_f8f6f4 v[64:67], v[24:31], v[216:223], v[64:67]
	s_setprio 0
	s_setprio 1
	v_mfma_f32_16x16x128_f8f6f4 v[60:63], v[0:7], v[192:199], v[60:63]
	v_mfma_f32_16x16x128_f8f6f4 v[56:59], v[8:15], v[192:199], v[56:59]
	v_mfma_f32_16x16x128_f8f6f4 v[52:55], v[0:7], v[200:207], v[52:55]
	v_mfma_f32_16x16x128_f8f6f4 v[48:51], v[8:15], v[200:207], v[48:51]
	v_mfma_f32_16x16x128_f8f6f4 v[44:47], v[0:7], v[208:215], v[44:47]
	v_mfma_f32_16x16x128_f8f6f4 v[40:43], v[8:15], v[208:215], v[40:43]
	v_mfma_f32_16x16x128_f8f6f4 v[36:39], v[0:7], v[216:223], v[36:39]
	v_mfma_f32_16x16x128_f8f6f4 v[32:35], v[8:15], v[216:223], v[32:35]
	s_setprio 0
	s_barrier
	s_add_u32 s46, s46, 0x20180
	s_addc_u32 s47, s47, 0
	s_add_u32 s89, s44, 0x200
	s_addc_u32 s90, s45, 0
	s_mov_b32 s91, 0
.LBB0_867:
	ds_read_b128 v[0:3], v188
	ds_read_b128 v[4:7], v188 offset:1024
	ds_read_b128 v[16:19], v188 offset:2048
	ds_read_b128 v[20:23], v188 offset:3072
	ds_read_b128 v[24:27], v189
	ds_read_b128 v[28:31], v189 offset:1024
	ds_read_b128 v[176:179], v189 offset:2048
	ds_read_b128 v[180:183], v189 offset:3072
	s_add_u32 s44, s46, 0xfffe0080
	s_addc_u32 s45, s47, -1
	s_cmp_eq_u32 s91, 4
	s_cselect_b32 s49, s25, s45
	s_cselect_b32 s48, s27, s44
	s_cselect_b32 s45, s63, s90
	s_cselect_b32 s44, s64, s89
	s_mov_b32 m0, s59
	v_lshl_add_u64 v[216:217], s[46:47], 0, v[168:169]
	ds_read_b128 v[8:11], v187
	ds_read_b128 v[12:15], v187 offset:1024
	ds_read_b128 v[192:195], v187 offset:2048
	ds_read_b128 v[196:199], v187 offset:3072
	ds_read_b128 v[200:203], v187 offset:4096
	ds_read_b128 v[204:207], v187 offset:5120
	ds_read_b128 v[208:211], v187 offset:6144
	ds_read_b128 v[212:215], v187 offset:7168
	global_load_lds_dwordx4 v[216:217], off
	v_lshl_add_u64 v[216:217], s[46:47], 0, v[170:171]
	s_mov_b32 m0, s65
	s_nop 0
	global_load_lds_dwordx4 v[216:217], off
	s_waitcnt vmcnt(8)
	s_waitcnt lgkmcnt(0)
	s_barrier
	s_setprio 1
	v_mfma_f32_16x16x128_f8f6f4 v[156:159], v[0:7], v[8:15], v[156:159]
	v_mfma_f32_16x16x128_f8f6f4 v[152:155], v[16:23], v[8:15], v[152:155]
	v_mfma_f32_16x16x128_f8f6f4 v[148:151], v[0:7], v[192:199], v[148:151]
	v_mfma_f32_16x16x128_f8f6f4 v[144:147], v[16:23], v[192:199], v[144:147]
	v_mfma_f32_16x16x128_f8f6f4 v[140:143], v[0:7], v[200:207], v[140:143]
	v_mfma_f32_16x16x128_f8f6f4 v[136:139], v[16:23], v[200:207], v[136:139]
	v_mfma_f32_16x16x128_f8f6f4 v[132:135], v[0:7], v[208:215], v[132:135]
	v_mfma_f32_16x16x128_f8f6f4 v[128:131], v[16:23], v[208:215], v[128:131]
	s_setprio 0
	s_setprio 1
	v_mfma_f32_16x16x128_f8f6f4 v[124:127], v[24:31], v[8:15], v[124:127]
	v_mfma_f32_16x16x128_f8f6f4 v[120:123], v[176:183], v[8:15], v[120:123]
	v_mfma_f32_16x16x128_f8f6f4 v[116:119], v[24:31], v[192:199], v[116:119]
	v_mfma_f32_16x16x128_f8f6f4 v[112:115], v[176:183], v[192:199], v[112:115]
	v_mfma_f32_16x16x128_f8f6f4 v[108:111], v[24:31], v[200:207], v[108:111]
	v_mfma_f32_16x16x128_f8f6f4 v[104:107], v[176:183], v[200:207], v[104:107]
	v_mfma_f32_16x16x128_f8f6f4 v[100:103], v[24:31], v[208:215], v[100:103]
	v_mfma_f32_16x16x128_f8f6f4 v[96:99], v[176:183], v[208:215], v[96:99]
	s_setprio 0
	s_barrier
; #define PG8_STAGE(bufoff, gbase, voff) do { _Pragma("unroll") for (int _i = 0; _i < 2; ++_i) \
;         __builtin_amdgcn_global_load_lds((const unsigned*)((const char*)(gbase) + (voff)[_i]), (PG8_LAS unsigned*)(lds + (bufoff) + ldsw + _i * 8192), 16, 0, 0); } while (0)
; #define PG8_WAIT_V(n) asm volatile("s_waitcnt vmcnt(" #n ")" ::: "memory")
; #define PG8_WAIT_L(n) asm volatile("s_waitcnt lgkmcnt(" #n ")" ::: "memory")
; #define PG8_BAR __builtin_amdgcn_s_barrier()
; #define PG8_SCHED __builtin_amdgcn_sched_barrier(0)
; template <class Epi, class Sched, bool ALIGN_EPI = false, bool SP2 = false, bool FP8 = false, bool PEEL = false>
; __device__ __forceinline__ void gemm_phase(PG8_LAS unsigned char* lds, const Gemm g, const Sched& S, const Epi& E, const int wid) {
;     ...
;             PG8_LDA(At, 0, 1); PG8_STAGE(PG8_SB(0, 0), b2, voffB); PG8_STAGE(PG8_SB(0, 1), b2 + hstep, voffB); PG8_STAGE(PG8_SA(0, 0), a2, voffA);
;             PG8_WAIT_V(8); PG8_WAIT_L(0); PG8_BAR; PG8_MMA(1, 0, At, B0); PG8_MMA(1, 1, At, B1); PG8_BAR; PG8_SCHED;
;             PG8_LDB(B0, 1, 0); PG8_LDB(B1, 1, 1); PG8_SCHED; PG8_LDA(At, 1, 0); PG8_STAGE(PG8_SA(0, 1), a2 + hstep, voffA);
;             PG8_WAIT_V(8); PG8_WAIT_L(0); PG8_BAR; PG8_MMA(0, 0, At, B0); PG8_MMA(0, 1, At, B1); PG8_BAR; PG8_SCHED;
;             PG8_LDA(At, 1, 1); PG8_STAGE(PG8_SB(1, 0), b3, voffB); PG8_STAGE(PG8_SB(1, 1), b3 + hstep, voffB); PG8_STAGE(PG8_SA(1, 0), a3, voffA);
	s_mov_b32 m0, s66
	v_lshl_add_u64 v[8:9], s[44:45], 0, v[164:165]
	s_add_u32 s92, s44, 0x20000
	ds_read_b128 v[192:195], v187 offset:16384
	ds_read_b128 v[196:199], v187 offset:17408
	ds_read_b128 v[200:203], v187 offset:18432
	ds_read_b128 v[204:207], v187 offset:19456
	ds_read_b128 v[208:211], v187 offset:20480
	ds_read_b128 v[212:215], v187 offset:21504
	ds_read_b128 v[216:219], v187 offset:22528
	ds_read_b128 v[220:223], v187 offset:23552
	global_load_lds_dwordx4 v[8:9], off
	v_lshl_add_u64 v[10:11], s[44:45], 0, v[160:161]
	s_mov_b32 m0, s67
	s_addc_u32 s93, s45, 0
	global_load_lds_dwordx4 v[10:11], off
	v_lshl_add_u64 v[12:13], s[92:93], 0, v[164:165]
	s_mov_b32 m0, s75
	v_lshl_add_u64 v[14:15], s[48:49], 0, v[162:163]
	global_load_lds_dwordx4 v[12:13], off
	v_lshl_add_u64 v[12:13], s[92:93], 0, v[160:161]
	s_mov_b32 m0, s84
	s_nop 0
	global_load_lds_dwordx4 v[12:13], off
	v_lshl_add_u64 v[12:13], s[48:49], 0, v[166:167]
	s_mov_b32 m0, s42
	s_nop 0
	global_load_lds_dwordx4 v[12:13], off
	s_mov_b32 m0, s43
	s_nop 0
	global_load_lds_dwordx4 v[14:15], off
	s_waitcnt vmcnt(8)
	s_waitcnt lgkmcnt(0)
	s_barrier
	s_setprio 1
	v_mfma_f32_16x16x128_f8f6f4 v[92:95], v[0:7], v[192:199], v[92:95]
	v_mfma_f32_16x16x128_f8f6f4 v[88:91], v[16:23], v[192:199], v[88:91]
	v_mfma_f32_16x16x128_f8f6f4 v[84:87], v[0:7], v[200:207], v[84:87]
	v_mfma_f32_16x16x128_f8f6f4 v[80:83], v[16:23], v[200:207], v[80:83]
	v_mfma_f32_16x16x128_f8f6f4 v[76:79], v[0:7], v[208:215], v[76:79]
	v_mfma_f32_16x16x128_f8f6f4 v[72:75], v[16:23], v[208:215], v[72:75]
	v_mfma_f32_16x16x128_f8f6f4 v[68:71], v[0:7], v[216:223], v[68:71]
	v_mfma_f32_16x16x128_f8f6f4 v[64:67], v[16:23], v[216:223], v[64:67]
	s_setprio 0
	s_setprio 1
	v_mfma_f32_16x16x128_f8f6f4 v[60:63], v[24:31], v[192:199], v[60:63]
	v_mfma_f32_16x16x128_f8f6f4 v[56:59], v[176:183], v[192:199], v[56:59]
	v_mfma_f32_16x16x128_f8f6f4 v[52:55], v[24:31], v[200:207], v[52:55]
	v_mfma_f32_16x16x128_f8f6f4 v[48:51], v[176:183], v[200:207], v[48:51]
	v_mfma_f32_16x16x128_f8f6f4 v[44:47], v[24:31], v[208:215], v[44:47]
	v_mfma_f32_16x16x128_f8f6f4 v[40:43], v[176:183], v[208:215], v[40:43]
	v_mfma_f32_16x16x128_f8f6f4 v[36:39], v[24:31], v[216:223], v[36:39]
	v_mfma_f32_16x16x128_f8f6f4 v[32:35], v[176:183], v[216:223], v[32:35]
	s_setprio 0
	s_barrier
	ds_read_b128 v[16:19], v190
	ds_read_b128 v[20:23], v190 offset:1024
	ds_read_b128 v[24:27], v190 offset:2048
	ds_read_b128 v[28:31], v190 offset:3072
	ds_read_b128 v[0:3], v191
	ds_read_b128 v[4:7], v191 offset:1024
	ds_read_b128 v[176:179], v191 offset:2048
	ds_read_b128 v[180:183], v191 offset:3072
	s_add_u32 s48, s48, 0x20000
	s_addc_u32 s49, s49, 0
	s_mov_b32 m0, s50
	v_lshl_add_u64 v[224:225], s[48:49], 0, v[166:167]
	ds_read_b128 v[192:195], v187 offset:32768
	ds_read_b128 v[196:199], v187 offset:33792
	ds_read_b128 v[200:203], v187 offset:34816
	ds_read_b128 v[204:207], v187 offset:35840
	ds_read_b128 v[208:211], v187 offset:36864
	ds_read_b128 v[212:215], v187 offset:37888
	ds_read_b128 v[216:219], v187 offset:38912
	ds_read_b128 v[220:223], v187 offset:39936
	global_load_lds_dwordx4 v[224:225], off
	v_lshl_add_u64 v[224:225], s[48:49], 0, v[162:163]
	s_mov_b32 m0, s51
	s_nop 0
	global_load_lds_dwordx4 v[224:225], off
	s_waitcnt vmcnt(8)
	s_waitcnt lgkmcnt(0)
	s_barrier
	s_setprio 1
	v_mfma_f32_16x16x128_f8f6f4 v[156:159], v[16:23], v[192:199], v[156:159]
	v_mfma_f32_16x16x128_f8f6f4 v[152:155], v[24:31], v[192:199], v[152:155]
	v_mfma_f32_16x16x128_f8f6f4 v[148:151], v[16:23], v[200:207], v[148:151]
	v_mfma_f32_16x16x128_f8f6f4 v[144:147], v[24:31], v[200:207], v[144:147]
	v_mfma_f32_16x16x128_f8f6f4 v[140:143], v[16:23], v[208:215], v[140:143]
	v_mfma_f32_16x16x128_f8f6f4 v[136:139], v[24:31], v[208:215], v[136:139]
	v_mfma_f32_16x16x128_f8f6f4 v[132:135], v[16:23], v[216:223], v[132:135]
	v_mfma_f32_16x16x128_f8f6f4 v[128:131], v[24:31], v[216:223], v[128:131]
	s_setprio 0
	s_setprio 1
	v_mfma_f32_16x16x128_f8f6f4 v[124:127], v[0:7], v[192:199], v[124:127]
	v_mfma_f32_16x16x128_f8f6f4 v[120:123], v[176:183], v[192:199], v[120:123]
	v_mfma_f32_16x16x128_f8f6f4 v[116:119], v[0:7], v[200:207], v[116:119]
	v_mfma_f32_16x16x128_f8f6f4 v[112:115], v[176:183], v[200:207], v[112:115]
	v_mfma_f32_16x16x128_f8f6f4 v[108:111], v[0:7], v[208:215], v[108:111]
	v_mfma_f32_16x16x128_f8f6f4 v[104:107], v[176:183], v[208:215], v[104:107]
	v_mfma_f32_16x16x128_f8f6f4 v[100:103], v[0:7], v[216:223], v[100:103]
	v_mfma_f32_16x16x128_f8f6f4 v[96:99], v[176:183], v[216:223], v[96:99]
	s_setprio 0
	s_barrier
	s_mov_b32 m0, s85
	v_lshl_add_u64 v[8:9], v[8:9], 0, s[10:11]
	s_add_u32 s44, s44, 0x20080
	ds_read_b128 v[192:195], v187 offset:49152
	ds_read_b128 v[196:199], v187 offset:50176
	ds_read_b128 v[200:203], v187 offset:51200
	ds_read_b128 v[204:207], v187 offset:52224
	ds_read_b128 v[208:211], v187 offset:53248
	ds_read_b128 v[212:215], v187 offset:54272
	ds_read_b128 v[216:219], v187 offset:55296
	ds_read_b128 v[220:223], v187 offset:56320
	global_load_lds_dwordx4 v[8:9], off
	v_lshl_add_u64 v[8:9], v[10:11], 0, s[10:11]
	s_mov_b32 m0, s86
	s_addc_u32 s45, s45, 0
	global_load_lds_dwordx4 v[8:9], off
	v_lshl_add_u64 v[8:9], s[44:45], 0, v[164:165]
	s_mov_b32 m0, s87
	s_nop 0
	global_load_lds_dwordx4 v[8:9], off
	v_lshl_add_u64 v[8:9], s[44:45], 0, v[160:161]
	s_mov_b32 m0, s88
	s_nop 0
	global_load_lds_dwordx4 v[8:9], off
	v_lshl_add_u64 v[8:9], v[12:13], 0, s[10:11]
	s_mov_b32 m0, s54
	s_nop 0
	global_load_lds_dwordx4 v[8:9], off
	v_lshl_add_u64 v[8:9], v[14:15], 0, s[10:11]
	s_mov_b32 m0, s55
	s_nop 0
	global_load_lds_dwordx4 v[8:9], off
	s_waitcnt vmcnt(8)
	s_waitcnt lgkmcnt(0)
	s_barrier
; __device__ __forceinline__ unsigned cvt_pk4_fp8(float a, float b, float c, float d) { int w = 0; w = __builtin_amdgcn_cvt_pk_fp8_f32(a, b, w, false); w = __builtin_amdgcn_cvt_pk_fp8_f32(c, d, w, true); return (unsigned)w; }
; __device__ __forceinline__ unsigned cvt_pk_bf16(float lo, float hi) { unsigned r; asm volatile("v_cvt_pk_bf16_f32 %0, %1, %2" : "=v"(r) : "v"(lo), "v"(hi)); return r; }
; __device__ __forceinline__ f32x2p silu_mul2k(f32x2p ag, f32x2p au, float kt, float ci) { const f32x2p t = ag * kt; f32x2p e; e.x = __builtin_amdgcn_exp2f(t.x); e.y = __builtin_amdgcn_exp2f(t.y);
;     const f32x2p d = e * ci + ci; f32x2p r; r.x = __builtin_amdgcn_rcpf(d.x); r.y = __builtin_amdgcn_rcpf(d.y); return (ag * au) * r; }
;     __device__ __forceinline__ void operator()(const f32x4 (&acc)[2][2][4][2], const Unit& u, int wr, int wc, int fr, int fq) const {
;         const int row0 = u.orow + wr * 64 + fr, col0 = u.ocol * HALF + wc * 32 + 8 * fq;
;         const float kt = -1.4426950408889634f * sc, ci = 1.f / (sc * sc * oscale);
; #pragma unroll
;         for (int ai = 0; ai < 2; ++ai)
; #pragma unroll
;             for (int m = 0; m < 4; ++m) { const size_t off = (size_t)(row0 + ai * HALF + m * 16) * ldc + col0;
;                 const f32x4 g0 = acc[ai][0][m][0], g1 = acc[ai][0][m][1], u0 = acc[ai][1][m][0], u1 = acc[ai][1][m][1];
;                 float v[8];
;                 { const f32x2p a = silu_mul2k((f32x2p){g0[0], g0[1]}, (f32x2p){u0[0], u0[1]}, kt, ci), b = silu_mul2k((f32x2p){g0[2], g0[3]}, (f32x2p){u0[2], u0[3]}, kt, ci), c = silu_mul2k((f32x2p){g1[0], g1[1]}, (f32x2p){u1[0], u1[1]}, kt, ci), d = silu_mul2k((f32x2p){g1[2], g1[3]}, (f32x2p){u1[2], u1[3]}, kt, ci);
;                   v[0] = a.x; v[1] = a.y; v[2] = b.x; v[3] = b.y; v[4] = c.x; v[5] = c.y; v[6] = d.x; v[7] = d.y; }
;                 if constexpr (FP8OUT) { typedef unsigned u32x2 __attribute__((ext_vector_type(2))); u32x2 w; w.x = cvt_pk4_fp8(v[0], v[1], v[2], v[3]); w.y = cvt_pk4_fp8(v[4], v[5], v[6], v[7]); __builtin_nontemporal_store(w, (u32x2*)((unsigned char*)O + off)); }
;                 else { u32x4 w; w.x = cvt_pk_bf16(v[0], v[1]); w.y = cvt_pk_bf16(v[2], v[3]); w.z = cvt_pk_bf16(v[4], v[5]); w.w = cvt_pk_bf16(v[6], v[7]); __builtin_nontemporal_store(w, (u32x4*)((bf16_t*)O + off)); } }
	s_setprio 1
	v_mfma_f32_16x16x128_f8f6f4 v[92:95], v[16:23], v[192:199], v[92:95]
	v_mfma_f32_16x16x128_f8f6f4 v[88:91], v[24:31], v[192:199], v[88:91]
	v_mfma_f32_16x16x128_f8f6f4 v[84:87], v[16:23], v[200:207], v[84:87]
	v_mfma_f32_16x16x128_f8f6f4 v[80:83], v[24:31], v[200:207], v[80:83]
	v_mfma_f32_16x16x128_f8f6f4 v[76:79], v[16:23], v[208:215], v[76:79]
	v_mfma_f32_16x16x128_f8f6f4 v[72:75], v[24:31], v[208:215], v[72:75]
	v_mfma_f32_16x16x128_f8f6f4 v[68:71], v[16:23], v[216:223], v[68:71]
	v_mfma_f32_16x16x128_f8f6f4 v[64:67], v[24:31], v[216:223], v[64:67]
	s_setprio 0
	s_setprio 1
	v_mfma_f32_16x16x128_f8f6f4 v[60:63], v[0:7], v[192:199], v[60:63]
	v_mfma_f32_16x16x128_f8f6f4 v[56:59], v[176:183], v[192:199], v[56:59]
	v_mfma_f32_16x16x128_f8f6f4 v[52:55], v[0:7], v[200:207], v[52:55]
	v_mfma_f32_16x16x128_f8f6f4 v[48:51], v[176:183], v[200:207], v[48:51]
	v_mfma_f32_16x16x128_f8f6f4 v[44:47], v[0:7], v[208:215], v[44:47]
	v_mfma_f32_16x16x128_f8f6f4 v[40:43], v[176:183], v[208:215], v[40:43]
	v_mfma_f32_16x16x128_f8f6f4 v[36:39], v[0:7], v[216:223], v[36:39]
	v_mfma_f32_16x16x128_f8f6f4 v[32:35], v[176:183], v[216:223], v[32:35]
	s_setprio 0
	s_barrier
	s_add_i32 s91, s91, 2
	s_add_u32 s46, s46, 0x100
	s_addc_u32 s47, s47, 0
	s_add_u32 s89, s89, 0x100
	s_addc_u32 s90, s90, 0
	s_cmp_gt_u32 s91, 5
	s_cbranch_scc0 .LBB0_867
	s_and_b64 vcc, exec, s[6:7]
	s_cbranch_vccz .LBB0_870
	s_barrier
.LBB0_870:
	v_pk_mul_f32 v[0:1], v[156:157], s[16:17] op_sel_hi:[1,0]
	v_pk_mul_f32 v[8:9], v[156:157], v[124:125]
	v_exp_f32_e32 v2, v0
	v_exp_f32_e32 v3, v1
	v_pk_mul_f32 v[10:11], v[152:153], s[16:17] op_sel_hi:[1,0]
	v_pk_mul_f32 v[12:13], v[154:155], s[16:17] op_sel_hi:[1,0]
	v_exp_f32_e32 v10, v10
	v_pk_fma_f32 v[2:3], v[2:3], s[22:23], s[22:23] op_sel_hi:[1,0,0]
	v_exp_f32_e32 v11, v11
	v_rcp_f32_e32 v2, v2
	v_rcp_f32_e32 v3, v3
	v_exp_f32_e32 v12, v12
	v_pk_fma_f32 v[10:11], v[10:11], s[22:23], s[22:23] op_sel_hi:[1,0,0]
	v_exp_f32_e32 v13, v13
	v_pk_mul_f32 v[2:3], v[8:9], v[2:3]
	v_pk_mul_f32 v[8:9], v[158:159], s[16:17] op_sel_hi:[1,0]
	v_rcp_f32_e32 v10, v10
	v_exp_f32_e32 v8, v8
	v_exp_f32_e32 v9, v9
	v_rcp_f32_e32 v11, v11
	v_pk_mul_f32 v[6:7], v[158:159], v[126:127]
	v_add_u32_e32 v4, s61, v184
	v_pk_fma_f32 v[8:9], v[8:9], s[22:23], s[22:23] op_sel_hi:[1,0,0]
	v_lshl_add_u32 v0, s62, 7, v186
	v_rcp_f32_e32 v8, v8
	v_rcp_f32_e32 v9, v9
	v_ashrrev_i32_e32 v1, 31, v0
	s_nop 15
	s_nop 15
	v_pk_mul_f32 v[14:15], v[146:147], s[16:17] op_sel_hi:[1,0]
	v_pk_mul_f32 v[6:7], v[6:7], v[8:9]
	v_pk_mul_f32 v[8:9], v[152:153], v[120:121]
	v_exp_f32_e32 v14, v14
	v_pk_mul_f32 v[8:9], v[8:9], v[10:11]
	v_pk_fma_f32 v[10:11], v[12:13], s[22:23], s[22:23] op_sel_hi:[1,0,0]
	v_cvt_pk_fp8_f32 v12, v2, v3
	v_rcp_f32_e32 v10, v10
	v_rcp_f32_e32 v11, v11
	v_cvt_pk_fp8_f32 v12, v6, v7 op_sel:[0,0,1]
	v_pk_mul_f32 v[6:7], v[148:149], s[16:17] op_sel_hi:[1,0]
	v_cvt_pk_fp8_f32 v13, v8, v9
	v_exp_f32_e32 v6, v6
	v_exp_f32_e32 v7, v7
	v_pk_mul_f32 v[2:3], v[154:155], v[122:123]
	v_exp_f32_e32 v15, v15
	v_pk_mul_f32 v[2:3], v[2:3], v[10:11]
	v_pk_fma_f32 v[6:7], v[6:7], s[22:23], s[22:23] op_sel_hi:[1,0,0]
	v_cvt_pk_fp8_f32 v13, v2, v3 op_sel:[0,0,1]
	v_rcp_f32_e32 v6, v6
	v_rcp_f32_e32 v7, v7
	v_mov_b64_e32 v[2:3], s[20:21]
	v_mad_i64_i32 v[8:9], s[44:45], v4, s58, v[2:3]
	v_pk_mul_f32 v[10:11], v[148:149], v[116:117]
	v_lshl_add_u64 v[8:9], v[8:9], 0, v[0:1]
	v_pk_mul_f32 v[6:7], v[10:11], v[6:7]
	v_pk_mul_f32 v[10:11], v[150:151], s[16:17] op_sel_hi:[1,0]
	global_store_dwordx2 v[8:9], v[12:13], off
	v_exp_f32_e32 v10, v10
	v_exp_f32_e32 v11, v11
	v_pk_mul_f32 v[12:13], v[144:145], s[16:17] op_sel_hi:[1,0]
	v_pk_mul_f32 v[8:9], v[150:151], v[118:119]
	v_exp_f32_e32 v12, v12
	v_exp_f32_e32 v13, v13
	v_pk_fma_f32 v[10:11], v[10:11], s[22:23], s[22:23] op_sel_hi:[1,0,0]
	v_add_u32_e32 v5, 16, v4
	v_rcp_f32_e32 v10, v10
	v_rcp_f32_e32 v11, v11
	v_pk_fma_f32 v[12:13], v[12:13], s[22:23], s[22:23] op_sel_hi:[1,0,0]
	v_readlane_b32 s68, v254, 28
	v_rcp_f32_e32 v12, v12
	v_rcp_f32_e32 v13, v13
	v_pk_mul_f32 v[8:9], v[8:9], v[10:11]
	v_pk_mul_f32 v[10:11], v[144:145], v[112:113]
	s_andn2_b64 vcc, exec, s[8:9]
	v_pk_mul_f32 v[10:11], v[10:11], v[12:13]
	v_pk_fma_f32 v[12:13], v[14:15], s[22:23], s[22:23] op_sel_hi:[1,0,0]
	v_rcp_f32_e32 v12, v12
	v_rcp_f32_e32 v13, v13
	v_cvt_pk_fp8_f32 v15, v10, v11
	v_cvt_pk_fp8_f32 v14, v6, v7
	v_pk_mul_f32 v[6:7], v[146:147], v[114:115]
	v_pk_mul_f32 v[10:11], v[140:141], v[108:109]
	v_pk_mul_f32 v[6:7], v[6:7], v[12:13]
	v_pk_mul_f32 v[12:13], v[136:137], s[16:17] op_sel_hi:[1,0]
	v_cvt_pk_fp8_f32 v15, v6, v7 op_sel:[0,0,1]
	v_pk_mul_f32 v[6:7], v[140:141], s[16:17] op_sel_hi:[1,0]
	v_cvt_pk_fp8_f32 v14, v8, v9 op_sel:[0,0,1]
	v_exp_f32_e32 v6, v6
	v_exp_f32_e32 v7, v7
	v_exp_f32_e32 v12, v12
	v_exp_f32_e32 v13, v13
	v_mad_i64_i32 v[8:9], s[44:45], v5, s58, v[2:3]
	v_pk_fma_f32 v[6:7], v[6:7], s[22:23], s[22:23] op_sel_hi:[1,0,0]
	v_lshl_add_u64 v[8:9], v[8:9], 0, v[0:1]
	v_rcp_f32_e32 v6, v6
	v_rcp_f32_e32 v7, v7
	global_store_dwordx2 v[8:9], v[14:15], off
	v_pk_fma_f32 v[12:13], v[12:13], s[22:23], s[22:23] op_sel_hi:[1,0,0]
	v_pk_mul_f32 v[14:15], v[138:139], s[16:17] op_sel_hi:[1,0]
	v_pk_mul_f32 v[6:7], v[10:11], v[6:7]
	v_pk_mul_f32 v[10:11], v[142:143], s[16:17] op_sel_hi:[1,0]
	v_rcp_f32_e32 v12, v12
	v_exp_f32_e32 v10, v10
	v_exp_f32_e32 v11, v11
	v_rcp_f32_e32 v13, v13
	v_exp_f32_e32 v14, v14
	v_exp_f32_e32 v15, v15
	v_pk_fma_f32 v[10:11], v[10:11], s[22:23], s[22:23] op_sel_hi:[1,0,0]
	v_pk_mul_f32 v[8:9], v[142:143], v[110:111]
	v_rcp_f32_e32 v10, v10
	v_rcp_f32_e32 v11, v11
	v_add_u32_e32 v5, 32, v4
; __device__ __forceinline__ unsigned cvt_pk4_fp8(float a, float b, float c, float d) { int w = 0; w = __builtin_amdgcn_cvt_pk_fp8_f32(a, b, w, false); w = __builtin_amdgcn_cvt_pk_fp8_f32(c, d, w, true); return (unsigned)w; }
; __device__ __forceinline__ unsigned cvt_pk_bf16(float lo, float hi) { unsigned r; asm volatile("v_cvt_pk_bf16_f32 %0, %1, %2" : "=v"(r) : "v"(lo), "v"(hi)); return r; }
; __device__ __forceinline__ f32x2p silu_mul2k(f32x2p ag, f32x2p au, float kt, float ci) { const f32x2p t = ag * kt; f32x2p e; e.x = __builtin_amdgcn_exp2f(t.x); e.y = __builtin_amdgcn_exp2f(t.y);
;     const f32x2p d = e * ci + ci; f32x2p r; r.x = __builtin_amdgcn_rcpf(d.x); r.y = __builtin_amdgcn_rcpf(d.y); return (ag * au) * r; }
;     __device__ __forceinline__ void operator()(const f32x4 (&acc)[2][2][4][2], const Unit& u, int wr, int wc, int fr, int fq) const {
;         const int row0 = u.orow + wr * 64 + fr, col0 = u.ocol * HALF + wc * 32 + 8 * fq;
;         const float kt = -1.4426950408889634f * sc, ci = 1.f / (sc * sc * oscale);
; #pragma unroll
;         for (int ai = 0; ai < 2; ++ai)
; #pragma unroll
;             for (int m = 0; m < 4; ++m) { const size_t off = (size_t)(row0 + ai * HALF + m * 16) * ldc + col0;
;                 const f32x4 g0 = acc[ai][0][m][0], g1 = acc[ai][0][m][1], u0 = acc[ai][1][m][0], u1 = acc[ai][1][m][1];
;                 float v[8];
;                 { const f32x2p a = silu_mul2k((f32x2p){g0[0], g0[1]}, (f32x2p){u0[0], u0[1]}, kt, ci), b = silu_mul2k((f32x2p){g0[2], g0[3]}, (f32x2p){u0[2], u0[3]}, kt, ci), c = silu_mul2k((f32x2p){g1[0], g1[1]}, (f32x2p){u1[0], u1[1]}, kt, ci), d = silu_mul2k((f32x2p){g1[2], g1[3]}, (f32x2p){u1[2], u1[3]}, kt, ci);
;                   v[0] = a.x; v[1] = a.y; v[2] = b.x; v[3] = b.y; v[4] = c.x; v[5] = c.y; v[6] = d.x; v[7] = d.y; }
;                 if constexpr (FP8OUT) { typedef unsigned u32x2 __attribute__((ext_vector_type(2))); u32x2 w; w.x = cvt_pk4_fp8(v[0], v[1], v[2], v[3]); w.y = cvt_pk4_fp8(v[4], v[5], v[6], v[7]); __builtin_nontemporal_store(w, (u32x2*)((unsigned char*)O + off)); }
;                 else { u32x4 w; w.x = cvt_pk_bf16(v[0], v[1]); w.y = cvt_pk_bf16(v[2], v[3]); w.z = cvt_pk_bf16(v[4], v[5]); w.w = cvt_pk_bf16(v[6], v[7]); __builtin_nontemporal_store(w, (u32x4*)((bf16_t*)O + off)); } }
	s_mov_b64 s[8:9], -1
	v_readlane_b32 s69, v254, 29
	v_pk_mul_f32 v[8:9], v[8:9], v[10:11]
	v_pk_mul_f32 v[10:11], v[136:137], v[104:105]
	v_readlane_b32 s70, v254, 30
	v_pk_mul_f32 v[10:11], v[10:11], v[12:13]
	v_pk_fma_f32 v[12:13], v[14:15], s[22:23], s[22:23] op_sel_hi:[1,0,0]
	v_rcp_f32_e32 v12, v12
	v_rcp_f32_e32 v13, v13
	v_cvt_pk_fp8_f32 v15, v10, v11
	v_cvt_pk_fp8_f32 v14, v6, v7
	v_pk_mul_f32 v[6:7], v[138:139], v[106:107]
	v_pk_mul_f32 v[10:11], v[132:133], v[100:101]
	v_pk_mul_f32 v[6:7], v[6:7], v[12:13]
	v_pk_mul_f32 v[12:13], v[128:129], s[16:17] op_sel_hi:[1,0]
	v_cvt_pk_fp8_f32 v15, v6, v7 op_sel:[0,0,1]
	v_pk_mul_f32 v[6:7], v[132:133], s[16:17] op_sel_hi:[1,0]
	v_cvt_pk_fp8_f32 v14, v8, v9 op_sel:[0,0,1]
	v_exp_f32_e32 v6, v6
	v_exp_f32_e32 v7, v7
	v_exp_f32_e32 v12, v12
	v_exp_f32_e32 v13, v13
	v_mad_i64_i32 v[8:9], s[44:45], v5, s58, v[2:3]
	v_pk_fma_f32 v[6:7], v[6:7], s[22:23], s[22:23] op_sel_hi:[1,0,0]
	v_lshl_add_u64 v[8:9], v[8:9], 0, v[0:1]
	v_rcp_f32_e32 v6, v6
	v_rcp_f32_e32 v7, v7
	global_store_dwordx2 v[8:9], v[14:15], off
	v_pk_fma_f32 v[12:13], v[12:13], s[22:23], s[22:23] op_sel_hi:[1,0,0]
	v_pk_mul_f32 v[14:15], v[130:131], s[16:17] op_sel_hi:[1,0]
	v_pk_mul_f32 v[6:7], v[10:11], v[6:7]
	v_pk_mul_f32 v[10:11], v[134:135], s[16:17] op_sel_hi:[1,0]
	v_rcp_f32_e32 v12, v12
	v_exp_f32_e32 v10, v10
	v_exp_f32_e32 v11, v11
	v_rcp_f32_e32 v13, v13
	v_exp_f32_e32 v14, v14
	v_exp_f32_e32 v15, v15
	v_pk_fma_f32 v[10:11], v[10:11], s[22:23], s[22:23] op_sel_hi:[1,0,0]
	v_pk_mul_f32 v[8:9], v[134:135], v[102:103]
	v_rcp_f32_e32 v10, v10
	v_rcp_f32_e32 v11, v11
	v_add_u32_e32 v5, 48, v4
	v_readlane_b32 s71, v254, 31
	v_readlane_b32 s72, v254, 32
	v_pk_mul_f32 v[8:9], v[8:9], v[10:11]
	v_pk_mul_f32 v[10:11], v[128:129], v[96:97]
	v_readlane_b32 s73, v254, 33
	v_pk_mul_f32 v[10:11], v[10:11], v[12:13]
	v_pk_fma_f32 v[12:13], v[14:15], s[22:23], s[22:23] op_sel_hi:[1,0,0]
	v_rcp_f32_e32 v12, v12
	v_rcp_f32_e32 v13, v13
	v_cvt_pk_fp8_f32 v15, v10, v11
	v_cvt_pk_fp8_f32 v14, v6, v7
	v_pk_mul_f32 v[6:7], v[130:131], v[98:99]
	v_pk_mul_f32 v[10:11], v[92:93], v[60:61]
	v_pk_mul_f32 v[6:7], v[6:7], v[12:13]
	v_pk_mul_f32 v[12:13], v[88:89], s[16:17] op_sel_hi:[1,0]
	v_cvt_pk_fp8_f32 v15, v6, v7 op_sel:[0,0,1]
	v_pk_mul_f32 v[6:7], v[92:93], s[16:17] op_sel_hi:[1,0]
	v_cvt_pk_fp8_f32 v14, v8, v9 op_sel:[0,0,1]
	v_exp_f32_e32 v6, v6
	v_exp_f32_e32 v7, v7
	v_exp_f32_e32 v12, v12
	v_exp_f32_e32 v13, v13
	v_mad_i64_i32 v[8:9], s[44:45], v5, s58, v[2:3]
	v_pk_fma_f32 v[6:7], v[6:7], s[22:23], s[22:23] op_sel_hi:[1,0,0]
	v_lshl_add_u64 v[8:9], v[8:9], 0, v[0:1]
	v_rcp_f32_e32 v6, v6
	v_rcp_f32_e32 v7, v7
	global_store_dwordx2 v[8:9], v[14:15], off
	v_pk_fma_f32 v[12:13], v[12:13], s[22:23], s[22:23] op_sel_hi:[1,0,0]
	v_pk_mul_f32 v[14:15], v[90:91], s[16:17] op_sel_hi:[1,0]
	v_pk_mul_f32 v[6:7], v[10:11], v[6:7]
	v_pk_mul_f32 v[10:11], v[94:95], s[16:17] op_sel_hi:[1,0]
	v_rcp_f32_e32 v12, v12
	v_exp_f32_e32 v10, v10
	v_exp_f32_e32 v11, v11
	v_rcp_f32_e32 v13, v13
	v_exp_f32_e32 v14, v14
	v_exp_f32_e32 v15, v15
	v_pk_fma_f32 v[10:11], v[10:11], s[22:23], s[22:23] op_sel_hi:[1,0,0]
	v_pk_mul_f32 v[8:9], v[94:95], v[62:63]
	v_rcp_f32_e32 v10, v10
	v_rcp_f32_e32 v11, v11
	v_add_u32_e32 v5, 0x80, v4
	v_readlane_b32 s74, v254, 34
	v_readlane_b32 s75, v254, 35
	v_pk_mul_f32 v[8:9], v[8:9], v[10:11]
	v_pk_mul_f32 v[10:11], v[88:89], v[56:57]
	s_nop 0
	v_pk_mul_f32 v[10:11], v[10:11], v[12:13]
	v_pk_fma_f32 v[12:13], v[14:15], s[22:23], s[22:23] op_sel_hi:[1,0,0]
	v_rcp_f32_e32 v12, v12
	v_rcp_f32_e32 v13, v13
	v_cvt_pk_fp8_f32 v15, v10, v11
	v_cvt_pk_fp8_f32 v14, v6, v7
	v_pk_mul_f32 v[6:7], v[90:91], v[58:59]
	v_pk_mul_f32 v[10:11], v[84:85], v[52:53]
	v_pk_mul_f32 v[6:7], v[6:7], v[12:13]
	v_pk_mul_f32 v[12:13], v[80:81], s[16:17] op_sel_hi:[1,0]
	v_cvt_pk_fp8_f32 v15, v6, v7 op_sel:[0,0,1]
	v_pk_mul_f32 v[6:7], v[84:85], s[16:17] op_sel_hi:[1,0]
	v_cvt_pk_fp8_f32 v14, v8, v9 op_sel:[0,0,1]
	v_exp_f32_e32 v6, v6
	v_exp_f32_e32 v7, v7
	v_exp_f32_e32 v12, v12
	v_exp_f32_e32 v13, v13
	v_mad_i64_i32 v[8:9], s[44:45], v5, s58, v[2:3]
	v_pk_fma_f32 v[6:7], v[6:7], s[22:23], s[22:23] op_sel_hi:[1,0,0]
	v_lshl_add_u64 v[8:9], v[8:9], 0, v[0:1]
	v_rcp_f32_e32 v6, v6
	v_rcp_f32_e32 v7, v7
	global_store_dwordx2 v[8:9], v[14:15], off
; __device__ __forceinline__ unsigned cvt_pk4_fp8(float a, float b, float c, float d) { int w = 0; w = __builtin_amdgcn_cvt_pk_fp8_f32(a, b, w, false); w = __builtin_amdgcn_cvt_pk_fp8_f32(c, d, w, true); return (unsigned)w; }
; __device__ __forceinline__ unsigned cvt_pk_bf16(float lo, float hi) { unsigned r; asm volatile("v_cvt_pk_bf16_f32 %0, %1, %2" : "=v"(r) : "v"(lo), "v"(hi)); return r; }
; __device__ __forceinline__ f32x2p silu_mul2k(f32x2p ag, f32x2p au, float kt, float ci) { const f32x2p t = ag * kt; f32x2p e; e.x = __builtin_amdgcn_exp2f(t.x); e.y = __builtin_amdgcn_exp2f(t.y);
;     const f32x2p d = e * ci + ci; f32x2p r; r.x = __builtin_amdgcn_rcpf(d.x); r.y = __builtin_amdgcn_rcpf(d.y); return (ag * au) * r; }
;     __device__ __forceinline__ void operator()(const f32x4 (&acc)[2][2][4][2], const Unit& u, int wr, int wc, int fr, int fq) const {
;         const int row0 = u.orow + wr * 64 + fr, col0 = u.ocol * HALF + wc * 32 + 8 * fq;
;         const float kt = -1.4426950408889634f * sc, ci = 1.f / (sc * sc * oscale);
; #pragma unroll
;         for (int ai = 0; ai < 2; ++ai)
; #pragma unroll
;             for (int m = 0; m < 4; ++m) { const size_t off = (size_t)(row0 + ai * HALF + m * 16) * ldc + col0;
;                 const f32x4 g0 = acc[ai][0][m][0], g1 = acc[ai][0][m][1], u0 = acc[ai][1][m][0], u1 = acc[ai][1][m][1];
;                 float v[8];
;                 { const f32x2p a = silu_mul2k((f32x2p){g0[0], g0[1]}, (f32x2p){u0[0], u0[1]}, kt, ci), b = silu_mul2k((f32x2p){g0[2], g0[3]}, (f32x2p){u0[2], u0[3]}, kt, ci), c = silu_mul2k((f32x2p){g1[0], g1[1]}, (f32x2p){u1[0], u1[1]}, kt, ci), d = silu_mul2k((f32x2p){g1[2], g1[3]}, (f32x2p){u1[2], u1[3]}, kt, ci);
;                   v[0] = a.x; v[1] = a.y; v[2] = b.x; v[3] = b.y; v[4] = c.x; v[5] = c.y; v[6] = d.x; v[7] = d.y; }
;                 if constexpr (FP8OUT) { typedef unsigned u32x2 __attribute__((ext_vector_type(2))); u32x2 w; w.x = cvt_pk4_fp8(v[0], v[1], v[2], v[3]); w.y = cvt_pk4_fp8(v[4], v[5], v[6], v[7]); __builtin_nontemporal_store(w, (u32x2*)((unsigned char*)O + off)); }
;                 else { u32x4 w; w.x = cvt_pk_bf16(v[0], v[1]); w.y = cvt_pk_bf16(v[2], v[3]); w.z = cvt_pk_bf16(v[4], v[5]); w.w = cvt_pk_bf16(v[6], v[7]); __builtin_nontemporal_store(w, (u32x4*)((bf16_t*)O + off)); } }
	v_pk_fma_f32 v[12:13], v[12:13], s[22:23], s[22:23] op_sel_hi:[1,0,0]
	v_pk_mul_f32 v[14:15], v[82:83], s[16:17] op_sel_hi:[1,0]
	v_pk_mul_f32 v[6:7], v[10:11], v[6:7]
	v_pk_mul_f32 v[10:11], v[86:87], s[16:17] op_sel_hi:[1,0]
	v_rcp_f32_e32 v12, v12
	v_exp_f32_e32 v10, v10
	v_exp_f32_e32 v11, v11
	v_rcp_f32_e32 v13, v13
	v_exp_f32_e32 v14, v14
	v_exp_f32_e32 v15, v15
	v_pk_fma_f32 v[10:11], v[10:11], s[22:23], s[22:23] op_sel_hi:[1,0,0]
	v_pk_mul_f32 v[8:9], v[86:87], v[54:55]
	v_rcp_f32_e32 v10, v10
	v_rcp_f32_e32 v11, v11
	v_add_u32_e32 v5, 0x90, v4
	v_pk_mul_f32 v[8:9], v[8:9], v[10:11]
	v_pk_mul_f32 v[10:11], v[80:81], v[48:49]
	s_nop 0
	v_pk_mul_f32 v[10:11], v[10:11], v[12:13]
	v_pk_fma_f32 v[12:13], v[14:15], s[22:23], s[22:23] op_sel_hi:[1,0,0]
	v_rcp_f32_e32 v12, v12
	v_rcp_f32_e32 v13, v13
	v_cvt_pk_fp8_f32 v15, v10, v11
	v_cvt_pk_fp8_f32 v14, v6, v7
	v_pk_mul_f32 v[6:7], v[82:83], v[50:51]
	v_pk_mul_f32 v[10:11], v[76:77], v[44:45]
	v_pk_mul_f32 v[6:7], v[6:7], v[12:13]
	v_pk_mul_f32 v[12:13], v[72:73], s[16:17] op_sel_hi:[1,0]
	v_cvt_pk_fp8_f32 v15, v6, v7 op_sel:[0,0,1]
	v_pk_mul_f32 v[6:7], v[76:77], s[16:17] op_sel_hi:[1,0]
	v_cvt_pk_fp8_f32 v14, v8, v9 op_sel:[0,0,1]
	v_exp_f32_e32 v6, v6
	v_exp_f32_e32 v7, v7
	v_exp_f32_e32 v12, v12
	v_exp_f32_e32 v13, v13
	v_mad_i64_i32 v[8:9], s[44:45], v5, s58, v[2:3]
	v_pk_fma_f32 v[6:7], v[6:7], s[22:23], s[22:23] op_sel_hi:[1,0,0]
	v_lshl_add_u64 v[8:9], v[8:9], 0, v[0:1]
	v_rcp_f32_e32 v6, v6
	v_rcp_f32_e32 v7, v7
	global_store_dwordx2 v[8:9], v[14:15], off
	v_pk_fma_f32 v[12:13], v[12:13], s[22:23], s[22:23] op_sel_hi:[1,0,0]
	v_pk_mul_f32 v[14:15], v[74:75], s[16:17] op_sel_hi:[1,0]
	v_pk_mul_f32 v[6:7], v[10:11], v[6:7]
	v_pk_mul_f32 v[10:11], v[78:79], s[16:17] op_sel_hi:[1,0]
	v_rcp_f32_e32 v12, v12
	v_exp_f32_e32 v10, v10
	v_exp_f32_e32 v11, v11
	v_rcp_f32_e32 v13, v13
	v_exp_f32_e32 v14, v14
	v_exp_f32_e32 v15, v15
	v_pk_fma_f32 v[10:11], v[10:11], s[22:23], s[22:23] op_sel_hi:[1,0,0]
	v_pk_mul_f32 v[8:9], v[78:79], v[46:47]
	v_rcp_f32_e32 v10, v10
	v_rcp_f32_e32 v11, v11
	v_add_u32_e32 v5, 0xa0, v4
	v_pk_mul_f32 v[8:9], v[8:9], v[10:11]
	v_pk_mul_f32 v[10:11], v[72:73], v[40:41]
	s_nop 0
	v_pk_mul_f32 v[10:11], v[10:11], v[12:13]
	v_pk_fma_f32 v[12:13], v[14:15], s[22:23], s[22:23] op_sel_hi:[1,0,0]
	v_rcp_f32_e32 v12, v12
	v_rcp_f32_e32 v13, v13
	v_cvt_pk_fp8_f32 v15, v10, v11
	v_cvt_pk_fp8_f32 v14, v6, v7
	v_pk_mul_f32 v[6:7], v[74:75], v[42:43]
	v_pk_mul_f32 v[10:11], v[64:65], s[16:17] op_sel_hi:[1,0]
	v_pk_mul_f32 v[6:7], v[6:7], v[12:13]
	v_cvt_pk_fp8_f32 v14, v8, v9 op_sel:[0,0,1]
	v_cvt_pk_fp8_f32 v15, v6, v7 op_sel:[0,0,1]
	v_pk_mul_f32 v[6:7], v[68:69], s[16:17] op_sel_hi:[1,0]
	v_mad_i64_i32 v[8:9], s[44:45], v5, s58, v[2:3]
	v_exp_f32_e32 v6, v6
	v_exp_f32_e32 v7, v7
	v_lshl_add_u64 v[8:9], v[8:9], 0, v[0:1]
	global_store_dwordx2 v[8:9], v[14:15], off
	v_pk_mul_f32 v[8:9], v[68:69], v[36:37]
	v_pk_fma_f32 v[6:7], v[6:7], s[22:23], s[22:23] op_sel_hi:[1,0,0]
	v_exp_f32_e32 v10, v10
	v_rcp_f32_e32 v6, v6
	v_rcp_f32_e32 v7, v7
	v_exp_f32_e32 v11, v11
	v_pk_mul_f32 v[12:13], v[66:67], s[16:17] op_sel_hi:[1,0]
	v_add_u32_e32 v14, 0xb0, v4
	v_pk_mul_f32 v[6:7], v[8:9], v[6:7]
	v_pk_mul_f32 v[8:9], v[70:71], s[16:17] op_sel_hi:[1,0]
	v_pk_fma_f32 v[10:11], v[10:11], s[22:23], s[22:23] op_sel_hi:[1,0,0]
	v_exp_f32_e32 v8, v8
	v_exp_f32_e32 v9, v9
	v_rcp_f32_e32 v10, v10
	v_rcp_f32_e32 v11, v11
	v_exp_f32_e32 v12, v12
	v_pk_fma_f32 v[8:9], v[8:9], s[22:23], s[22:23] op_sel_hi:[1,0,0]
	v_exp_f32_e32 v13, v13
	v_rcp_f32_e32 v8, v8
	v_rcp_f32_e32 v9, v9
	v_pk_mul_f32 v[4:5], v[70:71], v[38:39]
	v_mad_i64_i32 v[2:3], s[44:45], v14, s58, v[2:3]
	v_pk_mul_f32 v[4:5], v[4:5], v[8:9]
	v_pk_mul_f32 v[8:9], v[64:65], v[32:33]
	v_lshl_add_u64 v[0:1], v[2:3], 0, v[0:1]
	v_pk_mul_f32 v[8:9], v[8:9], v[10:11]
	v_pk_fma_f32 v[10:11], v[12:13], s[22:23], s[22:23] op_sel_hi:[1,0,0]
	v_rcp_f32_e32 v10, v10
	v_rcp_f32_e32 v11, v11
	v_cvt_pk_fp8_f32 v12, v6, v7
	v_cvt_pk_fp8_f32 v13, v8, v9
	v_pk_mul_f32 v[6:7], v[66:67], v[34:35]
	v_cvt_pk_fp8_f32 v12, v4, v5 op_sel:[0,0,1]
	v_pk_mul_f32 v[6:7], v[6:7], v[10:11]
	s_nop 0
	v_cvt_pk_fp8_f32 v13, v6, v7 op_sel:[0,0,1]
	global_store_dwordx2 v[0:1], v[12:13], off
	s_cbranch_vccnz .LBB0_863
	s_andn2_b64 vcc, exec, s[4:5]
	s_cbranch_vccnz .LBB0_862
	s_barrier
	s_branch .LBB0_862

; #define PG8_STAGE(bufoff, gbase, voff) do { _Pragma("unroll") for (int _i = 0; _i < 2; ++_i) \
;         __builtin_amdgcn_global_load_lds((const unsigned*)((const char*)(gbase) + (voff)[_i]), (PG8_LAS unsigned*)(lds + (bufoff) + ldsw + _i * 8192), 16, 0, 0); } while (0)
; #define PG8_WAIT_V(n) asm volatile("s_waitcnt vmcnt(" #n ")" ::: "memory")
; #define PG8_WAIT_L(n) asm volatile("s_waitcnt lgkmcnt(" #n ")" ::: "memory")
; #define PG8_BAR __builtin_amdgcn_s_barrier()
; #define PG8_SCHED __builtin_amdgcn_sched_barrier(0)
; template <class Epi, class Sched, bool ALIGN_EPI = false, bool SP2 = false, bool FP8 = false, bool PEEL = false>
; __device__ __forceinline__ void gemm_phase(PG8_LAS unsigned char* lds, const Gemm g, const Sched& S, const Epi& E, const int wid) {
;     ...
;         for (int t = 0; t < nt; t += 2) {
;             const bool last = (t == nt - 2);
;             const char* a1 = cA + (size_t)(t + 1) * kstep;
;             const char* a2 = last ? nA : cA + (size_t)(t + 2) * kstep; const char* b2 = last ? nB : cB + (size_t)(t + 2) * kstep;
;             const char* a3 = a2 + kstep; const char* b3 = b2 + kstep;
;             if (last && has_next) S.a_ready(nxt);
;             PG8_LDB(B0, 0, 0); PG8_LDB(B1, 0, 1); PG8_SCHED; PG8_LDA(At, 0, 0); PG8_STAGE(PG8_SA(1, 1), a1 + hstep, voffA);
;             PG8_WAIT_V(8); PG8_WAIT_L(0); PG8_BAR; PG8_MMA(0, 0, At, B0); PG8_MMA(0, 1, At, B1); PG8_BAR; PG8_SCHED;
;             PG8_LDA(At, 0, 1); PG8_STAGE(PG8_SB(0, 0), b2, voffB); PG8_STAGE(PG8_SB(0, 1), b2 + hstep, voffB); PG8_STAGE(PG8_SA(0, 0), a2, voffA);
;             PG8_WAIT_V(8); PG8_WAIT_L(0); PG8_BAR; PG8_MMA(1, 0, At, B0); PG8_MMA(1, 1, At, B1); PG8_BAR; PG8_SCHED;
;             PG8_LDB(B0, 1, 0); PG8_LDB(B1, 1, 1); PG8_SCHED; PG8_LDA(At, 1, 0); PG8_STAGE(PG8_SA(0, 1), a2 + hstep, voffA);
;             PG8_WAIT_V(8); PG8_WAIT_L(0); PG8_BAR; PG8_MMA(0, 0, At, B0); PG8_MMA(0, 1, At, B1); PG8_BAR; PG8_SCHED;
.LBB0_976:
	v_add_u32_e32 v12, s50, v180
	v_add_u32_e32 v172, s51, v180
	s_add_u32 s26, s6, s24
	ds_read_b128 v[0:3], v12
	ds_read_b128 v[4:7], v12 offset:1024
	ds_read_b128 v[8:11], v12 offset:2048
	ds_read_b128 v[12:15], v12 offset:3072
	ds_read_b128 v[16:19], v172
	ds_read_b128 v[20:23], v172 offset:1024
	ds_read_b128 v[182:185], v172 offset:2048
	ds_read_b128 v[186:189], v172 offset:3072
	s_addc_u32 s27, s7, s25
	s_add_u32 s26, s26, 0x100
	s_addc_u32 s27, s27, 0
	s_add_u32 s59, s56, s24
	s_addc_u32 s60, s57, s25
	s_cmpk_eq_i32 s24, 0xd00
	s_cselect_b32 s31, s17, s27
	s_cselect_b32 s30, s16, s26
	s_cselect_b32 s27, s13, s60
	s_cselect_b32 s26, s12, s59
	v_lshl_add_u64 v[198:199], v[168:169], 0, s[24:25]
	s_add_i32 m0, s43, 0xc000
	ds_read_b128 v[172:175], v181
	ds_read_b128 v[176:179], v181 offset:1024
	ds_read_b128 v[190:193], v181 offset:2048
	ds_read_b128 v[194:197], v181 offset:3072
	ds_read_b128 v[206:209], v181 offset:4096
	ds_read_b128 v[210:213], v181 offset:5120
	ds_read_b128 v[214:217], v181 offset:6144
	ds_read_b128 v[218:221], v181 offset:7168
	global_load_lds_dwordx4 v[198:199], off
	v_lshl_add_u64 v[198:199], v[170:171], 0, s[24:25]
	s_add_i32 m0, s43, 0xe000
	s_nop 0
	global_load_lds_dwordx4 v[198:199], off
	s_waitcnt vmcnt(8)
	s_waitcnt lgkmcnt(0)
	s_barrier
	s_setprio 1
	v_mfma_f32_16x16x128_f8f6f4 v[148:151], v[0:7], v[172:179], v[148:151]
	v_mfma_f32_16x16x128_f8f6f4 v[144:147], v[8:15], v[172:179], v[144:147]
	v_mfma_f32_16x16x128_f8f6f4 v[136:139], v[0:7], v[190:197], v[136:139]
	v_mfma_f32_16x16x128_f8f6f4 v[128:131], v[8:15], v[190:197], v[128:131]
	v_mfma_f32_16x16x128_f8f6f4 v[120:123], v[0:7], v[206:213], v[120:123]
	v_mfma_f32_16x16x128_f8f6f4 v[112:115], v[8:15], v[206:213], v[112:115]
	v_mfma_f32_16x16x128_f8f6f4 v[104:107], v[0:7], v[214:221], v[104:107]
	v_mfma_f32_16x16x128_f8f6f4 v[96:99], v[8:15], v[214:221], v[96:99]
	s_setprio 0
	s_setprio 1
	v_mfma_f32_16x16x128_f8f6f4 v[140:143], v[16:23], v[172:179], v[140:143]
	v_mfma_f32_16x16x128_f8f6f4 v[132:135], v[182:189], v[172:179], v[132:135]
	v_mfma_f32_16x16x128_f8f6f4 v[124:127], v[16:23], v[190:197], v[124:127]
	v_mfma_f32_16x16x128_f8f6f4 v[116:119], v[182:189], v[190:197], v[116:119]
	v_mfma_f32_16x16x128_f8f6f4 v[108:111], v[16:23], v[206:213], v[108:111]
	v_mfma_f32_16x16x128_f8f6f4 v[100:103], v[182:189], v[206:213], v[100:103]
	v_mfma_f32_16x16x128_f8f6f4 v[92:95], v[16:23], v[214:221], v[92:95]
	v_mfma_f32_16x16x128_f8f6f4 v[88:91], v[182:189], v[214:221], v[88:91]
	s_setprio 0
	s_barrier
	s_add_i32 s59, s50, s40
	v_lshl_add_u64 v[172:173], s[26:27], 0, v[156:157]
	s_mov_b32 m0, s59
	ds_read_b128 v[190:193], v181 offset:16384
	ds_read_b128 v[194:197], v181 offset:17408
	ds_read_b128 v[206:209], v181 offset:18432
	ds_read_b128 v[210:213], v181 offset:19456
	ds_read_b128 v[214:217], v181 offset:20480
	ds_read_b128 v[218:221], v181 offset:21504
	ds_read_b128 v[222:225], v181 offset:22528
	ds_read_b128 v[226:229], v181 offset:23552
	global_load_lds_dwordx4 v[172:173], off
	s_add_i32 m0, s59, 0x2000
	s_add_u32 s60, s26, 0x70000
	v_lshl_add_u64 v[174:175], s[26:27], 0, v[152:153]
	s_addc_u32 s61, s27, 0
	s_add_i32 s59, s51, s40
	global_load_lds_dwordx4 v[174:175], off
	v_lshl_add_u64 v[176:177], s[60:61], 0, v[156:157]
	s_mov_b32 m0, s59
	v_lshl_add_u64 v[178:179], s[30:31], 0, v[154:155]
	global_load_lds_dwordx4 v[176:177], off
	v_lshl_add_u64 v[176:177], s[60:61], 0, v[152:153]
	s_add_i32 m0, s59, 0x2000
	s_nop 0
	global_load_lds_dwordx4 v[176:177], off
	v_lshl_add_u64 v[176:177], s[30:31], 0, v[158:159]
	s_mov_b32 m0, s43
	s_nop 0
	global_load_lds_dwordx4 v[176:177], off
	s_mov_b32 m0, s44
	s_nop 0
	global_load_lds_dwordx4 v[178:179], off
	s_waitcnt vmcnt(8)
	s_waitcnt lgkmcnt(0)
	s_barrier
	s_setprio 1
	v_mfma_f32_16x16x128_f8f6f4 v[84:87], v[0:7], v[190:197], v[84:87]
	v_mfma_f32_16x16x128_f8f6f4 v[80:83], v[8:15], v[190:197], v[80:83]
	v_mfma_f32_16x16x128_f8f6f4 v[72:75], v[0:7], v[206:213], v[72:75]
	v_mfma_f32_16x16x128_f8f6f4 v[64:67], v[8:15], v[206:213], v[64:67]
	v_mfma_f32_16x16x128_f8f6f4 v[56:59], v[0:7], v[214:221], v[56:59]
	v_mfma_f32_16x16x128_f8f6f4 v[48:51], v[8:15], v[214:221], v[48:51]
	v_mfma_f32_16x16x128_f8f6f4 v[40:43], v[0:7], v[222:229], v[40:43]
	v_mfma_f32_16x16x128_f8f6f4 v[32:35], v[8:15], v[222:229], v[32:35]
	s_setprio 0
	s_setprio 1
	v_mfma_f32_16x16x128_f8f6f4 v[76:79], v[16:23], v[190:197], v[76:79]
	v_mfma_f32_16x16x128_f8f6f4 v[68:71], v[182:189], v[190:197], v[68:71]
	v_mfma_f32_16x16x128_f8f6f4 v[60:63], v[16:23], v[206:213], v[60:63]
	v_mfma_f32_16x16x128_f8f6f4 v[52:55], v[182:189], v[206:213], v[52:55]
	v_mfma_f32_16x16x128_f8f6f4 v[44:47], v[16:23], v[214:221], v[44:47]
	v_mfma_f32_16x16x128_f8f6f4 v[36:39], v[182:189], v[214:221], v[36:39]
	v_mfma_f32_16x16x128_f8f6f4 v[28:31], v[16:23], v[222:229], v[28:31]
	v_mfma_f32_16x16x128_f8f6f4 v[24:27], v[182:189], v[222:229], v[24:27]
	s_setprio 0
	s_barrier
	s_add_i32 s59, 0, 0x18000
	s_add_i32 s60, 0, 0x1c000
	v_add_u32_e32 v0, s59, v180
	v_add_u32_e32 v20, s60, v180
	ds_read_b128 v[8:11], v0
	ds_read_b128 v[12:15], v0 offset:1024
	ds_read_b128 v[182:185], v0 offset:2048
	ds_read_b128 v[186:189], v0 offset:3072
	ds_read_b128 v[0:3], v20
	ds_read_b128 v[4:7], v20 offset:1024
	ds_read_b128 v[16:19], v20 offset:2048
	ds_read_b128 v[20:23], v20 offset:3072
	s_add_u32 s30, s30, 0x70000
	s_addc_u32 s31, s31, 0
	s_mov_b32 m0, s45
	v_lshl_add_u64 v[198:199], s[30:31], 0, v[158:159]
	ds_read_b128 v[190:193], v181 offset:32768
	ds_read_b128 v[194:197], v181 offset:33792
	ds_read_b128 v[206:209], v181 offset:34816
	ds_read_b128 v[210:213], v181 offset:35840
	ds_read_b128 v[214:217], v181 offset:36864
	ds_read_b128 v[218:221], v181 offset:37888
	ds_read_b128 v[222:225], v181 offset:38912
	ds_read_b128 v[226:229], v181 offset:39936
	global_load_lds_dwordx4 v[198:199], off
	v_lshl_add_u64 v[198:199], s[30:31], 0, v[154:155]
	s_mov_b32 m0, s46
	s_nop 0
	global_load_lds_dwordx4 v[198:199], off
	s_waitcnt vmcnt(8)
	s_waitcnt lgkmcnt(0)
	s_barrier
; #define PG8_STAGE(bufoff, gbase, voff) do { _Pragma("unroll") for (int _i = 0; _i < 2; ++_i) \
;         __builtin_amdgcn_global_load_lds((const unsigned*)((const char*)(gbase) + (voff)[_i]), (PG8_LAS unsigned*)(lds + (bufoff) + ldsw + _i * 8192), 16, 0, 0); } while (0)
; #define PG8_WAIT_V(n) asm volatile("s_waitcnt vmcnt(" #n ")" ::: "memory")
; #define PG8_WAIT_L(n) asm volatile("s_waitcnt lgkmcnt(" #n ")" ::: "memory")
; #define PG8_BAR __builtin_amdgcn_s_barrier()
; #define PG8_SCHED __builtin_amdgcn_sched_barrier(0)
; template <class Epi, class Sched, bool ALIGN_EPI = false, bool SP2 = false, bool FP8 = false, bool PEEL = false>
; __device__ __forceinline__ void gemm_phase(PG8_LAS unsigned char* lds, const Gemm g, const Sched& S, const Epi& E, const int wid) {
;     ...
;             PG8_WAIT_V(8); PG8_WAIT_L(0); PG8_BAR; PG8_MMA(0, 0, At, B0); PG8_MMA(0, 1, At, B1); PG8_BAR; PG8_SCHED;
;             PG8_LDA(At, 1, 1); PG8_STAGE(PG8_SB(1, 0), b3, voffB); PG8_STAGE(PG8_SB(1, 1), b3 + hstep, voffB); PG8_STAGE(PG8_SA(1, 0), a3, voffA);
;             PG8_WAIT_V(8); PG8_WAIT_L(0); PG8_BAR; PG8_MMA(1, 0, At, B0); PG8_MMA(1, 1, At, B1); PG8_BAR; PG8_SCHED;
	s_setprio 1
	v_mfma_f32_16x16x128_f8f6f4 v[148:151], v[8:15], v[190:197], v[148:151]
	v_mfma_f32_16x16x128_f8f6f4 v[144:147], v[182:189], v[190:197], v[144:147]
	v_mfma_f32_16x16x128_f8f6f4 v[136:139], v[8:15], v[206:213], v[136:139]
	v_mfma_f32_16x16x128_f8f6f4 v[128:131], v[182:189], v[206:213], v[128:131]
	v_mfma_f32_16x16x128_f8f6f4 v[120:123], v[8:15], v[214:221], v[120:123]
	v_mfma_f32_16x16x128_f8f6f4 v[112:115], v[182:189], v[214:221], v[112:115]
	v_mfma_f32_16x16x128_f8f6f4 v[104:107], v[8:15], v[222:229], v[104:107]
	v_mfma_f32_16x16x128_f8f6f4 v[96:99], v[182:189], v[222:229], v[96:99]
	s_setprio 0
	s_setprio 1
	v_mfma_f32_16x16x128_f8f6f4 v[140:143], v[0:7], v[190:197], v[140:143]
	v_mfma_f32_16x16x128_f8f6f4 v[132:135], v[16:23], v[190:197], v[132:135]
	v_mfma_f32_16x16x128_f8f6f4 v[124:127], v[0:7], v[206:213], v[124:127]
	v_mfma_f32_16x16x128_f8f6f4 v[116:119], v[16:23], v[206:213], v[116:119]
	v_mfma_f32_16x16x128_f8f6f4 v[108:111], v[0:7], v[214:221], v[108:111]
	v_mfma_f32_16x16x128_f8f6f4 v[100:103], v[16:23], v[214:221], v[100:103]
	v_mfma_f32_16x16x128_f8f6f4 v[92:95], v[0:7], v[222:229], v[92:95]
	v_mfma_f32_16x16x128_f8f6f4 v[88:91], v[16:23], v[222:229], v[88:91]
	s_setprio 0
	s_barrier
	s_add_i32 s30, s59, s40
	v_lshl_add_u64 v[172:173], v[172:173], 0, s[14:15]
	s_mov_b32 m0, s30
	ds_read_b128 v[190:193], v181 offset:49152
	ds_read_b128 v[194:197], v181 offset:50176
	ds_read_b128 v[206:209], v181 offset:51200
	ds_read_b128 v[210:213], v181 offset:52224
	ds_read_b128 v[214:217], v181 offset:53248
	ds_read_b128 v[218:221], v181 offset:54272
	ds_read_b128 v[222:225], v181 offset:55296
	ds_read_b128 v[226:229], v181 offset:56320
	global_load_lds_dwordx4 v[172:173], off
	s_add_i32 m0, s30, 0x2000
	s_add_u32 s26, s26, 0x70080
	v_lshl_add_u64 v[172:173], v[174:175], 0, s[14:15]
	s_addc_u32 s27, s27, 0
	s_add_i32 s30, s60, s40
	global_load_lds_dwordx4 v[172:173], off
	v_lshl_add_u64 v[172:173], s[26:27], 0, v[156:157]
	s_mov_b32 m0, s30
	s_nop 0
	global_load_lds_dwordx4 v[172:173], off
	v_lshl_add_u64 v[172:173], s[26:27], 0, v[152:153]
	s_add_i32 m0, s30, 0x2000
	s_nop 0
	global_load_lds_dwordx4 v[172:173], off
	v_lshl_add_u64 v[172:173], v[176:177], 0, s[14:15]
	s_mov_b32 m0, s47
	s_nop 0
	global_load_lds_dwordx4 v[172:173], off
	v_lshl_add_u64 v[172:173], v[178:179], 0, s[14:15]
	s_mov_b32 m0, s48
	s_nop 0
	global_load_lds_dwordx4 v[172:173], off
	s_waitcnt vmcnt(8)
	s_waitcnt lgkmcnt(0)
	s_barrier
	s_setprio 1
	v_mfma_f32_16x16x128_f8f6f4 v[84:87], v[8:15], v[190:197], v[84:87]
	v_mfma_f32_16x16x128_f8f6f4 v[80:83], v[182:189], v[190:197], v[80:83]
	v_mfma_f32_16x16x128_f8f6f4 v[72:75], v[8:15], v[206:213], v[72:75]
	v_mfma_f32_16x16x128_f8f6f4 v[64:67], v[182:189], v[206:213], v[64:67]
	v_mfma_f32_16x16x128_f8f6f4 v[56:59], v[8:15], v[214:221], v[56:59]
	v_mfma_f32_16x16x128_f8f6f4 v[48:51], v[182:189], v[214:221], v[48:51]
	v_mfma_f32_16x16x128_f8f6f4 v[40:43], v[8:15], v[222:229], v[40:43]
	v_mfma_f32_16x16x128_f8f6f4 v[32:35], v[182:189], v[222:229], v[32:35]
	s_setprio 0
	s_setprio 1
	v_mfma_f32_16x16x128_f8f6f4 v[76:79], v[0:7], v[190:197], v[76:79]
	v_mfma_f32_16x16x128_f8f6f4 v[68:71], v[16:23], v[190:197], v[68:71]
	v_mfma_f32_16x16x128_f8f6f4 v[60:63], v[0:7], v[206:213], v[60:63]
	v_mfma_f32_16x16x128_f8f6f4 v[52:55], v[16:23], v[206:213], v[52:55]
	v_mfma_f32_16x16x128_f8f6f4 v[44:47], v[0:7], v[214:221], v[44:47]
	v_mfma_f32_16x16x128_f8f6f4 v[36:39], v[16:23], v[214:221], v[36:39]
	v_mfma_f32_16x16x128_f8f6f4 v[28:31], v[0:7], v[222:229], v[28:31]
	v_mfma_f32_16x16x128_f8f6f4 v[24:27], v[16:23], v[222:229], v[24:27]
	s_setprio 0
	s_barrier
; template <class Epi, class Sched, bool ALIGN_EPI = false, bool SP2 = false, bool FP8 = false, bool PEEL = false>
; __device__ __forceinline__ void gemm_phase(PG8_LAS unsigned char* lds, const Gemm g, const Sched& S, const Epi& E, const int wid) {
;     ...
;         }
;     ...
;         if constexpr (FP8) asm volatile("s_nop 15\n\ts_nop 15" ::: "memory");
;         if constexpr (!Epi::AFTER_DRAIN) { E(acc, cur, wr, wc, fr, fq); S.done(cur); }
;         if (!has_next) break;
;         if constexpr (!PEEL) {
; #pragma unroll
;         for (int a = 0; a < 2; ++a)
; #pragma unroll
;             for (int b = 0; b < 2; ++b)
; #pragma unroll
;                 for (int m = 0; m < 4; ++m)
; #pragma unroll
;                     for (int n = 0; n < 2; ++n) acc[a][b][m][n] = (f32x4){0.f, 0.f, 0.f, 0.f};
;         }
;         cur = nxt; cA = nA; cB = nB; ++ui;
	s_add_i32 s58, s58, 2
	s_add_u32 s24, s24, 0x100
	s_addc_u32 s25, s25, 0
	s_cmp_gt_u32 s58, 25
	s_cbranch_scc0 .LBB0_976
	s_nop 15
	s_nop 15
	s_add_u32 s24, s56, 0xffffff00
	s_addc_u32 s25, s57, -1
	s_and_b64 vcc, exec, s[10:11]
	s_cbranch_vccnz .LBB0_979
	v_mov_b32_e32 v24, 0
	s_mov_b32 s4, s52
	s_mov_b32 s3, s53
	s_mov_b64 s[6:7], s[16:17]
	s_mov_b32 s49, s55
	v_mov_b32_e32 v25, v24
	v_mov_b32_e32 v26, v24
	v_mov_b32_e32 v27, v24
	v_mov_b32_e32 v28, v24
	v_mov_b32_e32 v29, v24
	v_mov_b32_e32 v30, v24
	v_mov_b32_e32 v31, v24
	v_mov_b32_e32 v36, v24
	v_mov_b32_e32 v37, v24
	v_mov_b32_e32 v38, v24
	v_mov_b32_e32 v39, v24
	v_mov_b32_e32 v44, v24
	v_mov_b32_e32 v45, v24
	v_mov_b32_e32 v46, v24
	v_mov_b32_e32 v47, v24
	v_mov_b32_e32 v52, v24
	v_mov_b32_e32 v53, v24
	v_mov_b32_e32 v54, v24
	v_mov_b32_e32 v55, v24
	v_mov_b32_e32 v60, v24
	v_mov_b32_e32 v61, v24
	v_mov_b32_e32 v62, v24
	v_mov_b32_e32 v63, v24
	v_mov_b32_e32 v68, v24
	v_mov_b32_e32 v69, v24
	v_mov_b32_e32 v70, v24
	v_mov_b32_e32 v71, v24
	v_mov_b32_e32 v76, v24
	v_mov_b32_e32 v77, v24
	v_mov_b32_e32 v78, v24
	v_mov_b32_e32 v79, v24
	v_mov_b32_e32 v32, v24
	v_mov_b32_e32 v33, v24
	v_mov_b32_e32 v34, v24
	v_mov_b32_e32 v35, v24
	v_mov_b32_e32 v40, v24
	v_mov_b32_e32 v41, v24
	v_mov_b32_e32 v42, v24
	v_mov_b32_e32 v43, v24
	v_mov_b32_e32 v48, v24
	v_mov_b32_e32 v49, v24
	v_mov_b32_e32 v50, v24
	v_mov_b32_e32 v51, v24
	v_mov_b32_e32 v56, v24
	v_mov_b32_e32 v57, v24
	v_mov_b32_e32 v58, v24
	v_mov_b32_e32 v59, v24
	v_mov_b32_e32 v64, v24
	v_mov_b32_e32 v65, v24
	v_mov_b32_e32 v66, v24
	v_mov_b32_e32 v67, v24
	v_mov_b32_e32 v72, v24
	v_mov_b32_e32 v73, v24
	v_mov_b32_e32 v74, v24
	v_mov_b32_e32 v75, v24
	v_mov_b32_e32 v80, v24
	v_mov_b32_e32 v81, v24
	v_mov_b32_e32 v82, v24
	v_mov_b32_e32 v83, v24
	v_mov_b32_e32 v84, v24
	v_mov_b32_e32 v85, v24
	v_mov_b32_e32 v86, v24
	v_mov_b32_e32 v87, v24
	v_mov_b32_e32 v88, v24
	v_mov_b32_e32 v89, v24
	v_mov_b32_e32 v90, v24
	v_mov_b32_e32 v91, v24
	v_mov_b32_e32 v92, v24
	v_mov_b32_e32 v93, v24
	v_mov_b32_e32 v94, v24
	v_mov_b32_e32 v95, v24
	v_mov_b32_e32 v100, v24
	v_mov_b32_e32 v101, v24
	v_mov_b32_e32 v102, v24
	v_mov_b32_e32 v103, v24
	v_mov_b32_e32 v108, v24
	v_mov_b32_e32 v109, v24
	v_mov_b32_e32 v110, v24
	v_mov_b32_e32 v111, v24
	v_mov_b32_e32 v116, v24
	v_mov_b32_e32 v117, v24
	v_mov_b32_e32 v118, v24
	v_mov_b32_e32 v119, v24
	v_mov_b32_e32 v124, v24
	v_mov_b32_e32 v125, v24
	v_mov_b32_e32 v126, v24
	v_mov_b32_e32 v127, v24
	v_mov_b32_e32 v132, v24
	v_mov_b32_e32 v133, v24
	v_mov_b32_e32 v134, v24
	v_mov_b32_e32 v135, v24
	v_mov_b32_e32 v140, v24
	v_mov_b32_e32 v141, v24
	v_mov_b32_e32 v142, v24
	v_mov_b32_e32 v143, v24
	v_mov_b32_e32 v96, v24
	v_mov_b32_e32 v97, v24
	v_mov_b32_e32 v98, v24
	v_mov_b32_e32 v99, v24
	v_mov_b32_e32 v104, v24
	v_mov_b32_e32 v105, v24
	v_mov_b32_e32 v106, v24
	v_mov_b32_e32 v107, v24
	v_mov_b32_e32 v112, v24
	v_mov_b32_e32 v113, v24
	v_mov_b32_e32 v114, v24
	v_mov_b32_e32 v115, v24
	v_mov_b32_e32 v120, v24
	v_mov_b32_e32 v121, v24
	v_mov_b32_e32 v122, v24
	v_mov_b32_e32 v123, v24
	v_mov_b32_e32 v128, v24
	v_mov_b32_e32 v129, v24
	v_mov_b32_e32 v130, v24
	v_mov_b32_e32 v131, v24
	v_mov_b32_e32 v136, v24
	v_mov_b32_e32 v137, v24
	v_mov_b32_e32 v138, v24
	v_mov_b32_e32 v139, v24
	v_mov_b32_e32 v144, v24
	v_mov_b32_e32 v145, v24
	v_mov_b32_e32 v146, v24
	v_mov_b32_e32 v147, v24
	v_mov_b32_e32 v148, v24
	v_mov_b32_e32 v149, v24
	v_mov_b32_e32 v150, v24
	v_mov_b32_e32 v151, v24
	s_andn2_b64 vcc, exec, s[8:9]
	s_cbranch_vccnz .LBB0_980
	s_branch .LBB0_981

; #define PG8_STAGE(bufoff, gbase, voff) do { _Pragma("unroll") for (int _i = 0; _i < 2; ++_i) \
;         __builtin_amdgcn_global_load_lds((const unsigned*)((const char*)(gbase) + (voff)[_i]), (PG8_LAS unsigned*)(lds + (bufoff) + ldsw + _i * 8192), 16, 0, 0); } while (0)
; #define PG8_WAIT_V(n) asm volatile("s_waitcnt vmcnt(" #n ")" ::: "memory")
; #define PG8_WAIT_L(n) asm volatile("s_waitcnt lgkmcnt(" #n ")" ::: "memory")
; #define PG8_BAR __builtin_amdgcn_s_barrier()
; #define PG8_SCHED __builtin_amdgcn_sched_barrier(0)
; template <class Epi, class Sched, bool ALIGN_EPI = false, bool SP2 = false, bool FP8 = false, bool PEEL = false>
; __device__ __forceinline__ void gemm_phase(PG8_LAS unsigned char* lds, const Gemm g, const Sched& S, const Epi& E, const int wid) {
;     ...
;         for (int t = 0; t < nt; t += 2) {
;             const bool last = (t == nt - 2);
;             const char* a1 = cA + (size_t)(t + 1) * kstep;
;             const char* a2 = last ? nA : cA + (size_t)(t + 2) * kstep; const char* b2 = last ? nB : cB + (size_t)(t + 2) * kstep;
;             const char* a3 = a2 + kstep; const char* b3 = b2 + kstep;
;             if (last && has_next) S.a_ready(nxt);
;             PG8_LDB(B0, 0, 0); PG8_LDB(B1, 0, 1); PG8_SCHED; PG8_LDA(At, 0, 0); PG8_STAGE(PG8_SA(1, 1), a1 + hstep, voffA);
;             PG8_WAIT_V(8); PG8_WAIT_L(0); PG8_BAR; PG8_MMA(0, 0, At, B0); PG8_MMA(0, 1, At, B1); PG8_BAR; PG8_SCHED;
;             PG8_LDA(At, 0, 1); PG8_STAGE(PG8_SB(0, 0), b2, voffB); PG8_STAGE(PG8_SB(0, 1), b2 + hstep, voffB); PG8_STAGE(PG8_SA(0, 0), a2, voffA);
;             PG8_WAIT_V(8); PG8_WAIT_L(0); PG8_BAR; PG8_MMA(1, 0, At, B0); PG8_MMA(1, 1, At, B1); PG8_BAR; PG8_SCHED;
.LBB0_1120:
	ds_read_b128 v[146:149], v152
	ds_read_b128 v[156:159], v152 offset:1024
	ds_read_b128 v[160:163], v152 offset:2048
	ds_read_b128 v[164:167], v152 offset:3072
	ds_read_b128 v[168:171], v153
	ds_read_b128 v[172:175], v153 offset:1024
	ds_read_b128 v[176:179], v153 offset:2048
	ds_read_b128 v[180:183], v153 offset:3072
	s_add_u32 s44, s36, 0xfffc0080
	s_addc_u32 s45, s37, -1
	s_cmp_eq_u32 s61, 12
	s_cselect_b32 s47, s10, s45
	s_cselect_b32 s46, s25, s44
	s_cselect_b32 s45, s17, s60
	s_cselect_b32 s44, s58, s59
	v_lshl_add_u64 v[216:217], s[36:37], 0, v[136:137]
	s_add_i32 m0, s41, 0xc000
	ds_read_b128 v[184:187], v154
	ds_read_b128 v[188:191], v154 offset:1024
	ds_read_b128 v[192:195], v154 offset:2048
	ds_read_b128 v[196:199], v154 offset:3072
	ds_read_b128 v[200:203], v154 offset:4096
	ds_read_b128 v[204:207], v154 offset:5120
	ds_read_b128 v[208:211], v154 offset:6144
	ds_read_b128 v[212:215], v154 offset:7168
	global_load_lds_dwordx4 v[216:217], off
	v_lshl_add_u64 v[216:217], s[36:37], 0, v[138:139]
	s_add_i32 m0, s41, 0xe000
	s_nop 0
	global_load_lds_dwordx4 v[216:217], off
	s_waitcnt vmcnt(8)
	s_waitcnt lgkmcnt(0)
	s_barrier
	s_setprio 1
	v_mfma_f32_16x16x32_bf16 v[124:127], v[146:149], v[184:187], v[124:127]
	v_mfma_f32_16x16x32_bf16 v[120:123], v[160:163], v[184:187], v[120:123]
	v_mfma_f32_16x16x32_bf16 v[112:115], v[146:149], v[192:195], v[112:115]
	v_mfma_f32_16x16x32_bf16 v[104:107], v[160:163], v[192:195], v[104:107]
	v_mfma_f32_16x16x32_bf16 v[96:99], v[146:149], v[200:203], v[96:99]
	v_mfma_f32_16x16x32_bf16 v[88:91], v[160:163], v[200:203], v[88:91]
	v_mfma_f32_16x16x32_bf16 v[80:83], v[146:149], v[208:211], v[80:83]
	v_mfma_f32_16x16x32_bf16 v[72:75], v[160:163], v[208:211], v[72:75]
	v_mfma_f32_16x16x32_bf16 v[124:127], v[156:159], v[188:191], v[124:127]
	v_mfma_f32_16x16x32_bf16 v[120:123], v[164:167], v[188:191], v[120:123]
	v_mfma_f32_16x16x32_bf16 v[112:115], v[156:159], v[196:199], v[112:115]
	v_mfma_f32_16x16x32_bf16 v[104:107], v[164:167], v[196:199], v[104:107]
	v_mfma_f32_16x16x32_bf16 v[96:99], v[156:159], v[204:207], v[96:99]
	v_mfma_f32_16x16x32_bf16 v[88:91], v[164:167], v[204:207], v[88:91]
	v_mfma_f32_16x16x32_bf16 v[80:83], v[156:159], v[212:215], v[80:83]
	v_mfma_f32_16x16x32_bf16 v[72:75], v[164:167], v[212:215], v[72:75]
	s_setprio 0
	s_setprio 1
	v_mfma_f32_16x16x32_bf16 v[116:119], v[168:171], v[184:187], v[116:119]
	v_mfma_f32_16x16x32_bf16 v[108:111], v[176:179], v[184:187], v[108:111]
	v_mfma_f32_16x16x32_bf16 v[100:103], v[168:171], v[192:195], v[100:103]
	v_mfma_f32_16x16x32_bf16 v[92:95], v[176:179], v[192:195], v[92:95]
	v_mfma_f32_16x16x32_bf16 v[84:87], v[168:171], v[200:203], v[84:87]
	v_mfma_f32_16x16x32_bf16 v[76:79], v[176:179], v[200:203], v[76:79]
	v_mfma_f32_16x16x32_bf16 v[68:71], v[168:171], v[208:211], v[68:71]
	v_mfma_f32_16x16x32_bf16 v[64:67], v[176:179], v[208:211], v[64:67]
	v_mfma_f32_16x16x32_bf16 v[116:119], v[172:175], v[188:191], v[116:119]
	v_mfma_f32_16x16x32_bf16 v[108:111], v[180:183], v[188:191], v[108:111]
	v_mfma_f32_16x16x32_bf16 v[100:103], v[172:175], v[196:199], v[100:103]
	v_mfma_f32_16x16x32_bf16 v[92:95], v[180:183], v[196:199], v[92:95]
	v_mfma_f32_16x16x32_bf16 v[84:87], v[172:175], v[204:207], v[84:87]
	v_mfma_f32_16x16x32_bf16 v[76:79], v[180:183], v[204:207], v[76:79]
	v_mfma_f32_16x16x32_bf16 v[68:71], v[172:175], v[212:215], v[68:71]
	v_mfma_f32_16x16x32_bf16 v[64:67], v[180:183], v[212:215], v[64:67]
	s_setprio 0
	s_barrier
	s_add_i32 s62, s52, s3
	v_lshl_add_u64 v[216:217], s[44:45], 0, v[132:133]
	s_mov_b32 m0, s62
	ds_read_b128 v[184:187], v154 offset:16384
	ds_read_b128 v[188:191], v154 offset:17408
	ds_read_b128 v[192:195], v154 offset:18432
	ds_read_b128 v[196:199], v154 offset:19456
	ds_read_b128 v[200:203], v154 offset:20480
	ds_read_b128 v[204:207], v154 offset:21504
	ds_read_b128 v[208:211], v154 offset:22528
	ds_read_b128 v[212:215], v154 offset:23552
	global_load_lds_dwordx4 v[216:217], off
	s_add_i32 m0, s62, 0x2000
	s_add_u32 s62, s44, 0x40000
	v_lshl_add_u64 v[218:219], s[44:45], 0, v[128:129]
	s_addc_u32 s63, s45, 0
	s_add_i32 s64, s53, s3
	global_load_lds_dwordx4 v[218:219], off
	v_lshl_add_u64 v[220:221], s[62:63], 0, v[132:133]
	s_mov_b32 m0, s64
	v_lshl_add_u64 v[222:223], s[46:47], 0, v[130:131]
	global_load_lds_dwordx4 v[220:221], off
	v_lshl_add_u64 v[220:221], s[62:63], 0, v[128:129]
	s_add_i32 m0, s64, 0x2000
	s_nop 0
	global_load_lds_dwordx4 v[220:221], off
	v_lshl_add_u64 v[220:221], s[46:47], 0, v[134:135]
	s_mov_b32 m0, s41
	s_nop 0
	global_load_lds_dwordx4 v[220:221], off
	s_mov_b32 m0, s42
	s_nop 0
	global_load_lds_dwordx4 v[222:223], off
	s_waitcnt vmcnt(8)
	s_waitcnt lgkmcnt(0)
	s_barrier
; #define PG8_STAGE(bufoff, gbase, voff) do { _Pragma("unroll") for (int _i = 0; _i < 2; ++_i) \
;         __builtin_amdgcn_global_load_lds((const unsigned*)((const char*)(gbase) + (voff)[_i]), (PG8_LAS unsigned*)(lds + (bufoff) + ldsw + _i * 8192), 16, 0, 0); } while (0)
; #define PG8_WAIT_V(n) asm volatile("s_waitcnt vmcnt(" #n ")" ::: "memory")
; #define PG8_WAIT_L(n) asm volatile("s_waitcnt lgkmcnt(" #n ")" ::: "memory")
; #define PG8_BAR __builtin_amdgcn_s_barrier()
; #define PG8_SCHED __builtin_amdgcn_sched_barrier(0)
; template <class Epi, class Sched, bool ALIGN_EPI = false, bool SP2 = false, bool FP8 = false, bool PEEL = false>
; __device__ __forceinline__ void gemm_phase(PG8_LAS unsigned char* lds, const Gemm g, const Sched& S, const Epi& E, const int wid) {
;     ...
;             PG8_WAIT_V(8); PG8_WAIT_L(0); PG8_BAR; PG8_MMA(1, 0, At, B0); PG8_MMA(1, 1, At, B1); PG8_BAR; PG8_SCHED;
;             PG8_LDB(B0, 1, 0); PG8_LDB(B1, 1, 1); PG8_SCHED; PG8_LDA(At, 1, 0); PG8_STAGE(PG8_SA(0, 1), a2 + hstep, voffA);
;             PG8_WAIT_V(8); PG8_WAIT_L(0); PG8_BAR; PG8_MMA(0, 0, At, B0); PG8_MMA(0, 1, At, B1); PG8_BAR; PG8_SCHED;
	s_setprio 1
	v_mfma_f32_16x16x32_bf16 v[60:63], v[146:149], v[184:187], v[60:63]
	v_mfma_f32_16x16x32_bf16 v[56:59], v[160:163], v[184:187], v[56:59]
	v_mfma_f32_16x16x32_bf16 v[48:51], v[146:149], v[192:195], v[48:51]
	v_mfma_f32_16x16x32_bf16 v[40:43], v[160:163], v[192:195], v[40:43]
	v_mfma_f32_16x16x32_bf16 v[32:35], v[146:149], v[200:203], v[32:35]
	v_mfma_f32_16x16x32_bf16 v[24:27], v[160:163], v[200:203], v[24:27]
	v_mfma_f32_16x16x32_bf16 v[16:19], v[146:149], v[208:211], v[16:19]
	v_mfma_f32_16x16x32_bf16 v[8:11], v[160:163], v[208:211], v[8:11]
	v_mfma_f32_16x16x32_bf16 v[60:63], v[156:159], v[188:191], v[60:63]
	v_mfma_f32_16x16x32_bf16 v[56:59], v[164:167], v[188:191], v[56:59]
	v_mfma_f32_16x16x32_bf16 v[48:51], v[156:159], v[196:199], v[48:51]
	v_mfma_f32_16x16x32_bf16 v[40:43], v[164:167], v[196:199], v[40:43]
	v_mfma_f32_16x16x32_bf16 v[32:35], v[156:159], v[204:207], v[32:35]
	v_mfma_f32_16x16x32_bf16 v[24:27], v[164:167], v[204:207], v[24:27]
	v_mfma_f32_16x16x32_bf16 v[16:19], v[156:159], v[212:215], v[16:19]
	v_mfma_f32_16x16x32_bf16 v[8:11], v[164:167], v[212:215], v[8:11]
	s_setprio 0
	s_setprio 1
	v_mfma_f32_16x16x32_bf16 v[52:55], v[168:171], v[184:187], v[52:55]
	v_mfma_f32_16x16x32_bf16 v[44:47], v[176:179], v[184:187], v[44:47]
	v_mfma_f32_16x16x32_bf16 v[36:39], v[168:171], v[192:195], v[36:39]
	v_mfma_f32_16x16x32_bf16 v[28:31], v[176:179], v[192:195], v[28:31]
	v_mfma_f32_16x16x32_bf16 v[20:23], v[168:171], v[200:203], v[20:23]
	v_mfma_f32_16x16x32_bf16 v[12:15], v[176:179], v[200:203], v[12:15]
	v_mfma_f32_16x16x32_bf16 v[4:7], v[168:171], v[208:211], v[4:7]
	v_mfma_f32_16x16x32_bf16 v[0:3], v[176:179], v[208:211], v[0:3]
	v_mfma_f32_16x16x32_bf16 v[52:55], v[172:175], v[188:191], v[52:55]
	v_mfma_f32_16x16x32_bf16 v[44:47], v[180:183], v[188:191], v[44:47]
	v_mfma_f32_16x16x32_bf16 v[36:39], v[172:175], v[196:199], v[36:39]
	v_mfma_f32_16x16x32_bf16 v[28:31], v[180:183], v[196:199], v[28:31]
	v_mfma_f32_16x16x32_bf16 v[20:23], v[172:175], v[204:207], v[20:23]
	v_mfma_f32_16x16x32_bf16 v[12:15], v[180:183], v[204:207], v[12:15]
	v_mfma_f32_16x16x32_bf16 v[4:7], v[172:175], v[212:215], v[4:7]
	v_mfma_f32_16x16x32_bf16 v[0:3], v[180:183], v[212:215], v[0:3]
	s_setprio 0
	s_barrier
	s_add_i32 s62, 0, 0x18000
	v_add_u32_e32 v144, s62, v150
	s_add_i32 s63, 0, 0x1c000
	ds_read_b128 v[146:149], v144
	ds_read_b128 v[156:159], v144 offset:1024
	ds_read_b128 v[160:163], v144 offset:2048
	ds_read_b128 v[164:167], v144 offset:3072
	v_add_u32_e32 v144, s63, v150
	ds_read_b128 v[168:171], v144
	ds_read_b128 v[172:175], v144 offset:1024
	ds_read_b128 v[176:179], v144 offset:2048
	ds_read_b128 v[180:183], v144 offset:3072
	s_add_u32 s46, s46, 0x40000
	s_addc_u32 s47, s47, 0
	s_mov_b32 m0, s43
	v_lshl_add_u64 v[224:225], s[46:47], 0, v[134:135]
	ds_read_b128 v[184:187], v154 offset:32768
	ds_read_b128 v[188:191], v154 offset:33792
	ds_read_b128 v[192:195], v154 offset:34816
	ds_read_b128 v[196:199], v154 offset:35840
	ds_read_b128 v[200:203], v154 offset:36864
	ds_read_b128 v[204:207], v154 offset:37888
	ds_read_b128 v[208:211], v154 offset:38912
	ds_read_b128 v[212:215], v154 offset:39936
	global_load_lds_dwordx4 v[224:225], off
	v_lshl_add_u64 v[224:225], s[46:47], 0, v[130:131]
	s_mov_b32 m0, s48
	s_nop 0
	global_load_lds_dwordx4 v[224:225], off
	s_waitcnt vmcnt(8)
	s_waitcnt lgkmcnt(0)
	s_barrier
	s_setprio 1
	v_mfma_f32_16x16x32_bf16 v[124:127], v[146:149], v[184:187], v[124:127]
	v_mfma_f32_16x16x32_bf16 v[120:123], v[160:163], v[184:187], v[120:123]
	v_mfma_f32_16x16x32_bf16 v[112:115], v[146:149], v[192:195], v[112:115]
	v_mfma_f32_16x16x32_bf16 v[104:107], v[160:163], v[192:195], v[104:107]
	v_mfma_f32_16x16x32_bf16 v[96:99], v[146:149], v[200:203], v[96:99]
	v_mfma_f32_16x16x32_bf16 v[88:91], v[160:163], v[200:203], v[88:91]
	v_mfma_f32_16x16x32_bf16 v[80:83], v[146:149], v[208:211], v[80:83]
	v_mfma_f32_16x16x32_bf16 v[72:75], v[160:163], v[208:211], v[72:75]
	v_mfma_f32_16x16x32_bf16 v[124:127], v[156:159], v[188:191], v[124:127]
	v_mfma_f32_16x16x32_bf16 v[120:123], v[164:167], v[188:191], v[120:123]
	v_mfma_f32_16x16x32_bf16 v[112:115], v[156:159], v[196:199], v[112:115]
	v_mfma_f32_16x16x32_bf16 v[104:107], v[164:167], v[196:199], v[104:107]
	v_mfma_f32_16x16x32_bf16 v[96:99], v[156:159], v[204:207], v[96:99]
	v_mfma_f32_16x16x32_bf16 v[88:91], v[164:167], v[204:207], v[88:91]
	v_mfma_f32_16x16x32_bf16 v[80:83], v[156:159], v[212:215], v[80:83]
	v_mfma_f32_16x16x32_bf16 v[72:75], v[164:167], v[212:215], v[72:75]
	s_setprio 0
	s_setprio 1
	v_mfma_f32_16x16x32_bf16 v[116:119], v[168:171], v[184:187], v[116:119]
	v_mfma_f32_16x16x32_bf16 v[108:111], v[176:179], v[184:187], v[108:111]
	v_mfma_f32_16x16x32_bf16 v[100:103], v[168:171], v[192:195], v[100:103]
	v_mfma_f32_16x16x32_bf16 v[92:95], v[176:179], v[192:195], v[92:95]
	v_mfma_f32_16x16x32_bf16 v[84:87], v[168:171], v[200:203], v[84:87]
	v_mfma_f32_16x16x32_bf16 v[76:79], v[176:179], v[200:203], v[76:79]
	v_mfma_f32_16x16x32_bf16 v[68:71], v[168:171], v[208:211], v[68:71]
	v_mfma_f32_16x16x32_bf16 v[64:67], v[176:179], v[208:211], v[64:67]
	v_mfma_f32_16x16x32_bf16 v[116:119], v[172:175], v[188:191], v[116:119]
	v_mfma_f32_16x16x32_bf16 v[108:111], v[180:183], v[188:191], v[108:111]
	v_mfma_f32_16x16x32_bf16 v[100:103], v[172:175], v[196:199], v[100:103]
	v_mfma_f32_16x16x32_bf16 v[92:95], v[180:183], v[196:199], v[92:95]
	v_mfma_f32_16x16x32_bf16 v[84:87], v[172:175], v[204:207], v[84:87]
	v_mfma_f32_16x16x32_bf16 v[76:79], v[180:183], v[204:207], v[76:79]
	v_mfma_f32_16x16x32_bf16 v[68:71], v[172:175], v[212:215], v[68:71]
	v_mfma_f32_16x16x32_bf16 v[64:67], v[180:183], v[212:215], v[64:67]
	s_setprio 0
	s_barrier
; #define PG8_STAGE(bufoff, gbase, voff) do { _Pragma("unroll") for (int _i = 0; _i < 2; ++_i) \
;         __builtin_amdgcn_global_load_lds((const unsigned*)((const char*)(gbase) + (voff)[_i]), (PG8_LAS unsigned*)(lds + (bufoff) + ldsw + _i * 8192), 16, 0, 0); } while (0)
; #define PG8_WAIT_V(n) asm volatile("s_waitcnt vmcnt(" #n ")" ::: "memory")
; #define PG8_WAIT_L(n) asm volatile("s_waitcnt lgkmcnt(" #n ")" ::: "memory")
; #define PG8_BAR __builtin_amdgcn_s_barrier()
; #define PG8_SCHED __builtin_amdgcn_sched_barrier(0)
; template <class Epi, class Sched, bool ALIGN_EPI = false, bool SP2 = false, bool FP8 = false, bool PEEL = false>
; __device__ __forceinline__ void gemm_phase(PG8_LAS unsigned char* lds, const Gemm g, const Sched& S, const Epi& E, const int wid) {
;     ...
;             PG8_LDA(At, 1, 1); PG8_STAGE(PG8_SB(1, 0), b3, voffB); PG8_STAGE(PG8_SB(1, 1), b3 + hstep, voffB); PG8_STAGE(PG8_SA(1, 0), a3, voffA);
;             PG8_WAIT_V(8); PG8_WAIT_L(0); PG8_BAR; PG8_MMA(1, 0, At, B0); PG8_MMA(1, 1, At, B1); PG8_BAR; PG8_SCHED;
;         }
;     ...
;         if constexpr (ALIGN_EPI) { if (wr == 0) PG8_BAR; }
	s_add_i32 s46, s62, s3
	v_lshl_add_u64 v[216:217], v[216:217], 0, s[14:15]
	s_mov_b32 m0, s46
	ds_read_b128 v[184:187], v154 offset:49152
	ds_read_b128 v[188:191], v154 offset:50176
	ds_read_b128 v[192:195], v154 offset:51200
	ds_read_b128 v[196:199], v154 offset:52224
	ds_read_b128 v[200:203], v154 offset:53248
	ds_read_b128 v[204:207], v154 offset:54272
	ds_read_b128 v[208:211], v154 offset:55296
	ds_read_b128 v[212:215], v154 offset:56320
	global_load_lds_dwordx4 v[216:217], off
	s_add_i32 m0, s46, 0x2000
	s_add_u32 s44, s44, 0x40080
	v_lshl_add_u64 v[216:217], v[218:219], 0, s[14:15]
	s_addc_u32 s45, s45, 0
	s_add_i32 s46, s63, s3
	global_load_lds_dwordx4 v[216:217], off
	v_lshl_add_u64 v[216:217], s[44:45], 0, v[132:133]
	s_mov_b32 m0, s46
	s_nop 0
	global_load_lds_dwordx4 v[216:217], off
	v_lshl_add_u64 v[216:217], s[44:45], 0, v[128:129]
	s_add_i32 m0, s46, 0x2000
	s_nop 0
	global_load_lds_dwordx4 v[216:217], off
	v_lshl_add_u64 v[216:217], v[220:221], 0, s[14:15]
	s_mov_b32 m0, s50
	s_nop 0
	global_load_lds_dwordx4 v[216:217], off
	v_lshl_add_u64 v[216:217], v[222:223], 0, s[14:15]
	s_mov_b32 m0, s51
	s_nop 0
	global_load_lds_dwordx4 v[216:217], off
	s_waitcnt vmcnt(8)
	s_waitcnt lgkmcnt(0)
	s_barrier
	s_setprio 1
	v_mfma_f32_16x16x32_bf16 v[60:63], v[146:149], v[184:187], v[60:63]
	v_mfma_f32_16x16x32_bf16 v[56:59], v[160:163], v[184:187], v[56:59]
	v_mfma_f32_16x16x32_bf16 v[48:51], v[146:149], v[192:195], v[48:51]
	v_mfma_f32_16x16x32_bf16 v[40:43], v[160:163], v[192:195], v[40:43]
	v_mfma_f32_16x16x32_bf16 v[32:35], v[146:149], v[200:203], v[32:35]
	v_mfma_f32_16x16x32_bf16 v[24:27], v[160:163], v[200:203], v[24:27]
	v_mfma_f32_16x16x32_bf16 v[16:19], v[146:149], v[208:211], v[16:19]
	v_mfma_f32_16x16x32_bf16 v[8:11], v[160:163], v[208:211], v[8:11]
	v_mfma_f32_16x16x32_bf16 v[60:63], v[156:159], v[188:191], v[60:63]
	v_mfma_f32_16x16x32_bf16 v[56:59], v[164:167], v[188:191], v[56:59]
	v_mfma_f32_16x16x32_bf16 v[48:51], v[156:159], v[196:199], v[48:51]
	v_mfma_f32_16x16x32_bf16 v[40:43], v[164:167], v[196:199], v[40:43]
	v_mfma_f32_16x16x32_bf16 v[32:35], v[156:159], v[204:207], v[32:35]
	v_mfma_f32_16x16x32_bf16 v[24:27], v[164:167], v[204:207], v[24:27]
	v_mfma_f32_16x16x32_bf16 v[16:19], v[156:159], v[212:215], v[16:19]
	v_mfma_f32_16x16x32_bf16 v[8:11], v[164:167], v[212:215], v[8:11]
	s_setprio 0
	s_setprio 1
	v_mfma_f32_16x16x32_bf16 v[52:55], v[168:171], v[184:187], v[52:55]
	v_mfma_f32_16x16x32_bf16 v[44:47], v[176:179], v[184:187], v[44:47]
	v_mfma_f32_16x16x32_bf16 v[36:39], v[168:171], v[192:195], v[36:39]
	v_mfma_f32_16x16x32_bf16 v[28:31], v[176:179], v[192:195], v[28:31]
	v_mfma_f32_16x16x32_bf16 v[20:23], v[168:171], v[200:203], v[20:23]
	v_mfma_f32_16x16x32_bf16 v[12:15], v[176:179], v[200:203], v[12:15]
	v_mfma_f32_16x16x32_bf16 v[4:7], v[168:171], v[208:211], v[4:7]
	v_mfma_f32_16x16x32_bf16 v[0:3], v[176:179], v[208:211], v[0:3]
	v_mfma_f32_16x16x32_bf16 v[52:55], v[172:175], v[188:191], v[52:55]
	v_mfma_f32_16x16x32_bf16 v[44:47], v[180:183], v[188:191], v[44:47]
	v_mfma_f32_16x16x32_bf16 v[36:39], v[172:175], v[196:199], v[36:39]
	v_mfma_f32_16x16x32_bf16 v[28:31], v[180:183], v[196:199], v[28:31]
	v_mfma_f32_16x16x32_bf16 v[20:23], v[172:175], v[204:207], v[20:23]
	v_mfma_f32_16x16x32_bf16 v[12:15], v[180:183], v[204:207], v[12:15]
	v_mfma_f32_16x16x32_bf16 v[4:7], v[172:175], v[212:215], v[4:7]
	v_mfma_f32_16x16x32_bf16 v[0:3], v[180:183], v[212:215], v[0:3]
	s_setprio 0
	s_barrier
	s_add_i32 s61, s61, 2
	s_add_u32 s36, s36, 0x100
	s_addc_u32 s37, s37, 0
	s_add_u32 s59, s59, 0x100
	s_addc_u32 s60, s60, 0
	s_cmp_gt_u32 s61, 13
	s_cbranch_scc0 .LBB0_1120
	s_and_b64 vcc, exec, s[12:13]
	s_cbranch_vccz .LBB0_1123
	s_barrier

; #define PG8_STAGE(bufoff, gbase, voff) do { _Pragma("unroll") for (int _i = 0; _i < 2; ++_i) \
;         __builtin_amdgcn_global_load_lds((const unsigned*)((const char*)(gbase) + (voff)[_i]), (PG8_LAS unsigned*)(lds + (bufoff) + ldsw + _i * 8192), 16, 0, 0); } while (0)
; #define PG8_WAIT_V(n) asm volatile("s_waitcnt vmcnt(" #n ")" ::: "memory")
; #define PG8_WAIT_L(n) asm volatile("s_waitcnt lgkmcnt(" #n ")" ::: "memory")
; #define PG8_BAR __builtin_amdgcn_s_barrier()
; #define PG8_SCHED __builtin_amdgcn_sched_barrier(0)
; template <class Epi, class Sched, bool ALIGN_EPI = false, bool SP2 = false, bool FP8 = false, bool PEEL = false>
; __device__ __forceinline__ void gemm_phase(PG8_LAS unsigned char* lds, const Gemm g, const Sched& S, const Epi& E, const int wid) {
;     ...
;         for (int t = 0; t < nt; t += 2) {
;             const bool last = (t == nt - 2);
;             const char* a1 = cA + (size_t)(t + 1) * kstep;
;             const char* a2 = last ? nA : cA + (size_t)(t + 2) * kstep; const char* b2 = last ? nB : cB + (size_t)(t + 2) * kstep;
;             const char* a3 = a2 + kstep; const char* b3 = b2 + kstep;
;             if (last && has_next) S.a_ready(nxt);
;             PG8_LDB(B0, 0, 0); PG8_LDB(B1, 0, 1); PG8_SCHED; PG8_LDA(At, 0, 0); PG8_STAGE(PG8_SA(1, 1), a1 + hstep, voffA);
;             PG8_WAIT_V(8); PG8_WAIT_L(0); PG8_BAR; PG8_MMA(0, 0, At, B0); PG8_MMA(0, 1, At, B1); PG8_BAR; PG8_SCHED;
;             PG8_LDA(At, 0, 1); PG8_STAGE(PG8_SB(0, 0), b2, voffB); PG8_STAGE(PG8_SB(0, 1), b2 + hstep, voffB); PG8_STAGE(PG8_SA(0, 0), a2, voffA);
;             PG8_WAIT_V(8); PG8_WAIT_L(0); PG8_BAR; PG8_MMA(1, 0, At, B0); PG8_MMA(1, 1, At, B1); PG8_BAR; PG8_SCHED;
.LBB0_1535:
	ds_read_b128 v[128:131], v209
	ds_read_b128 v[132:135], v209 offset:1024
	ds_read_b128 v[136:139], v209 offset:2048
	ds_read_b128 v[140:143], v209 offset:3072
	ds_read_b128 v[144:147], v210
	ds_read_b128 v[148:151], v210 offset:1024
	ds_read_b128 v[152:155], v210 offset:2048
	ds_read_b128 v[156:159], v210 offset:3072
	s_add_u32 s30, s26, 0xfffc0080
	s_addc_u32 s31, s27, -1
	s_cmp_eq_u32 s67, 12
	s_cselect_b32 s37, s15, s31
	s_cselect_b32 s36, s63, s30
	s_cselect_b32 s31, s13, s66
	s_cselect_b32 s30, s64, s65
	v_lshl_add_u64 v[204:205], s[26:27], 0, v[196:197]
	s_add_i32 m0, s41, 0xc000
	ds_read_b128 v[160:163], v211
	ds_read_b128 v[164:167], v211 offset:1024
	ds_read_b128 v[168:171], v211 offset:2048
	ds_read_b128 v[172:175], v211 offset:3072
	ds_read_b128 v[176:179], v211 offset:4096
	ds_read_b128 v[180:183], v211 offset:5120
	ds_read_b128 v[184:187], v211 offset:6144
	ds_read_b128 v[212:215], v211 offset:7168
	global_load_lds_dwordx4 v[204:205], off
	v_lshl_add_u64 v[204:205], s[26:27], 0, v[198:199]
	s_add_i32 m0, s41, 0xe000
	s_nop 0
	global_load_lds_dwordx4 v[204:205], off
	s_waitcnt vmcnt(8)
	s_waitcnt lgkmcnt(0)
	s_barrier
	s_setprio 1
	v_mfma_f32_16x16x32_bf16 v[124:127], v[128:131], v[160:163], v[124:127]
	v_mfma_f32_16x16x32_bf16 v[120:123], v[136:139], v[160:163], v[120:123]
	v_mfma_f32_16x16x32_bf16 v[108:111], v[128:131], v[168:171], v[108:111]
	v_mfma_f32_16x16x32_bf16 v[104:107], v[136:139], v[168:171], v[104:107]
	v_mfma_f32_16x16x32_bf16 v[92:95], v[128:131], v[176:179], v[92:95]
	v_mfma_f32_16x16x32_bf16 v[88:91], v[136:139], v[176:179], v[88:91]
	v_mfma_f32_16x16x32_bf16 v[76:79], v[128:131], v[184:187], v[76:79]
	v_mfma_f32_16x16x32_bf16 v[72:75], v[136:139], v[184:187], v[72:75]
	v_mfma_f32_16x16x32_bf16 v[124:127], v[132:135], v[164:167], v[124:127]
	v_mfma_f32_16x16x32_bf16 v[120:123], v[140:143], v[164:167], v[120:123]
	v_mfma_f32_16x16x32_bf16 v[108:111], v[132:135], v[172:175], v[108:111]
	v_mfma_f32_16x16x32_bf16 v[104:107], v[140:143], v[172:175], v[104:107]
	v_mfma_f32_16x16x32_bf16 v[92:95], v[132:135], v[180:183], v[92:95]
	v_mfma_f32_16x16x32_bf16 v[88:91], v[140:143], v[180:183], v[88:91]
	v_mfma_f32_16x16x32_bf16 v[76:79], v[132:135], v[212:215], v[76:79]
	v_mfma_f32_16x16x32_bf16 v[72:75], v[140:143], v[212:215], v[72:75]
	s_setprio 0
	s_setprio 1
	v_mfma_f32_16x16x32_bf16 v[116:119], v[144:147], v[160:163], v[116:119]
	v_mfma_f32_16x16x32_bf16 v[112:115], v[152:155], v[160:163], v[112:115]
	v_mfma_f32_16x16x32_bf16 v[100:103], v[144:147], v[168:171], v[100:103]
	v_mfma_f32_16x16x32_bf16 v[96:99], v[152:155], v[168:171], v[96:99]
	v_mfma_f32_16x16x32_bf16 v[84:87], v[144:147], v[176:179], v[84:87]
	v_mfma_f32_16x16x32_bf16 v[80:83], v[152:155], v[176:179], v[80:83]
	v_mfma_f32_16x16x32_bf16 v[68:71], v[144:147], v[184:187], v[68:71]
	v_mfma_f32_16x16x32_bf16 v[64:67], v[152:155], v[184:187], v[64:67]
	v_mfma_f32_16x16x32_bf16 v[116:119], v[148:151], v[164:167], v[116:119]
	v_mfma_f32_16x16x32_bf16 v[112:115], v[156:159], v[164:167], v[112:115]
	v_mfma_f32_16x16x32_bf16 v[100:103], v[148:151], v[172:175], v[100:103]
	v_mfma_f32_16x16x32_bf16 v[96:99], v[156:159], v[172:175], v[96:99]
	v_mfma_f32_16x16x32_bf16 v[84:87], v[148:151], v[180:183], v[84:87]
	v_mfma_f32_16x16x32_bf16 v[80:83], v[156:159], v[180:183], v[80:83]
	v_mfma_f32_16x16x32_bf16 v[68:71], v[148:151], v[212:215], v[68:71]
	v_mfma_f32_16x16x32_bf16 v[64:67], v[156:159], v[212:215], v[64:67]
	s_setprio 0
	s_barrier
	s_add_i32 s75, s54, s39
	v_lshl_add_u64 v[204:205], s[30:31], 0, v[192:193]
	s_mov_b32 m0, s75
	ds_read_b128 v[160:163], v211 offset:16384
	ds_read_b128 v[164:167], v211 offset:17408
	ds_read_b128 v[168:171], v211 offset:18432
	ds_read_b128 v[172:175], v211 offset:19456
	ds_read_b128 v[176:179], v211 offset:20480
	ds_read_b128 v[180:183], v211 offset:21504
	ds_read_b128 v[184:187], v211 offset:22528
	ds_read_b128 v[212:215], v211 offset:23552
	global_load_lds_dwordx4 v[204:205], off
	s_add_i32 m0, s75, 0x2000
	s_add_u32 s80, s30, 0x40000
	v_lshl_add_u64 v[216:217], s[30:31], 0, v[188:189]
	s_addc_u32 s81, s31, 0
	s_add_i32 s75, s55, s39
	global_load_lds_dwordx4 v[216:217], off
	v_lshl_add_u64 v[218:219], s[80:81], 0, v[192:193]
	s_mov_b32 m0, s75
	v_lshl_add_u64 v[220:221], s[36:37], 0, v[190:191]
	global_load_lds_dwordx4 v[218:219], off
	v_lshl_add_u64 v[218:219], s[80:81], 0, v[188:189]
	s_add_i32 m0, s75, 0x2000
	s_nop 0
	global_load_lds_dwordx4 v[218:219], off
	v_lshl_add_u64 v[218:219], s[36:37], 0, v[194:195]
	s_mov_b32 m0, s41
	s_nop 0
	global_load_lds_dwordx4 v[218:219], off
	s_mov_b32 m0, s42
	s_nop 0
	global_load_lds_dwordx4 v[220:221], off
	s_waitcnt vmcnt(8)
	s_waitcnt lgkmcnt(0)
	s_barrier
; #define PG8_STAGE(bufoff, gbase, voff) do { _Pragma("unroll") for (int _i = 0; _i < 2; ++_i) \
;         __builtin_amdgcn_global_load_lds((const unsigned*)((const char*)(gbase) + (voff)[_i]), (PG8_LAS unsigned*)(lds + (bufoff) + ldsw + _i * 8192), 16, 0, 0); } while (0)
; #define PG8_WAIT_V(n) asm volatile("s_waitcnt vmcnt(" #n ")" ::: "memory")
; #define PG8_WAIT_L(n) asm volatile("s_waitcnt lgkmcnt(" #n ")" ::: "memory")
; #define PG8_BAR __builtin_amdgcn_s_barrier()
; #define PG8_SCHED __builtin_amdgcn_sched_barrier(0)
; template <class Epi, class Sched, bool ALIGN_EPI = false, bool SP2 = false, bool FP8 = false, bool PEEL = false>
; __device__ __forceinline__ void gemm_phase(PG8_LAS unsigned char* lds, const Gemm g, const Sched& S, const Epi& E, const int wid) {
;     ...
;             PG8_LDB(B0, 0, 0); PG8_LDB(B1, 0, 1); PG8_SCHED; PG8_LDA(At, 0, 0); PG8_STAGE(PG8_SA(1, 1), a1 + hstep, voffA);
;             PG8_WAIT_V(8); PG8_WAIT_L(0); PG8_BAR; PG8_MMA(0, 0, At, B0); PG8_MMA(0, 1, At, B1); PG8_BAR; PG8_SCHED;
;             PG8_LDA(At, 0, 1); PG8_STAGE(PG8_SB(0, 0), b2, voffB); PG8_STAGE(PG8_SB(0, 1), b2 + hstep, voffB); PG8_STAGE(PG8_SA(0, 0), a2, voffA);
;             PG8_WAIT_V(8); PG8_WAIT_L(0); PG8_BAR; PG8_MMA(1, 0, At, B0); PG8_MMA(1, 1, At, B1); PG8_BAR; PG8_SCHED;
;             PG8_LDB(B0, 1, 0); PG8_LDB(B1, 1, 1); PG8_SCHED; PG8_LDA(At, 1, 0); PG8_STAGE(PG8_SA(0, 1), a2 + hstep, voffA);
;             PG8_WAIT_V(8); PG8_WAIT_L(0); PG8_BAR; PG8_MMA(0, 0, At, B0); PG8_MMA(0, 1, At, B1); PG8_BAR; PG8_SCHED;
;             PG8_LDA(At, 1, 1); PG8_STAGE(PG8_SB(1, 0), b3, voffB); PG8_STAGE(PG8_SB(1, 1), b3 + hstep, voffB); PG8_STAGE(PG8_SA(1, 0), a3, voffA);
;             PG8_WAIT_V(8); PG8_WAIT_L(0); PG8_BAR; PG8_MMA(1, 0, At, B0); PG8_MMA(1, 1, At, B1); PG8_BAR; PG8_SCHED;
	s_setprio 1
	v_mfma_f32_16x16x32_bf16 v[60:63], v[128:131], v[160:163], v[60:63]
	v_mfma_f32_16x16x32_bf16 v[56:59], v[136:139], v[160:163], v[56:59]
	v_mfma_f32_16x16x32_bf16 v[44:47], v[128:131], v[168:171], v[44:47]
	v_mfma_f32_16x16x32_bf16 v[40:43], v[136:139], v[168:171], v[40:43]
	v_mfma_f32_16x16x32_bf16 v[28:31], v[128:131], v[176:179], v[28:31]
	v_mfma_f32_16x16x32_bf16 v[24:27], v[136:139], v[176:179], v[24:27]
	v_mfma_f32_16x16x32_bf16 v[12:15], v[128:131], v[184:187], v[12:15]
	v_mfma_f32_16x16x32_bf16 v[8:11], v[136:139], v[184:187], v[8:11]
	v_mfma_f32_16x16x32_bf16 v[60:63], v[132:135], v[164:167], v[60:63]
	v_mfma_f32_16x16x32_bf16 v[56:59], v[140:143], v[164:167], v[56:59]
	v_mfma_f32_16x16x32_bf16 v[44:47], v[132:135], v[172:175], v[44:47]
	v_mfma_f32_16x16x32_bf16 v[40:43], v[140:143], v[172:175], v[40:43]
	v_mfma_f32_16x16x32_bf16 v[28:31], v[132:135], v[180:183], v[28:31]
	v_mfma_f32_16x16x32_bf16 v[24:27], v[140:143], v[180:183], v[24:27]
	v_mfma_f32_16x16x32_bf16 v[12:15], v[132:135], v[212:215], v[12:15]
	v_mfma_f32_16x16x32_bf16 v[8:11], v[140:143], v[212:215], v[8:11]
	s_setprio 0
	s_setprio 1
	v_mfma_f32_16x16x32_bf16 v[52:55], v[144:147], v[160:163], v[52:55]
	v_mfma_f32_16x16x32_bf16 v[48:51], v[152:155], v[160:163], v[48:51]
	v_mfma_f32_16x16x32_bf16 v[36:39], v[144:147], v[168:171], v[36:39]
	v_mfma_f32_16x16x32_bf16 v[32:35], v[152:155], v[168:171], v[32:35]
	v_mfma_f32_16x16x32_bf16 v[20:23], v[144:147], v[176:179], v[20:23]
	v_mfma_f32_16x16x32_bf16 v[16:19], v[152:155], v[176:179], v[16:19]
	v_mfma_f32_16x16x32_bf16 v[4:7], v[144:147], v[184:187], v[4:7]
	v_mfma_f32_16x16x32_bf16 v[0:3], v[152:155], v[184:187], v[0:3]
	v_mfma_f32_16x16x32_bf16 v[52:55], v[148:151], v[164:167], v[52:55]
	v_mfma_f32_16x16x32_bf16 v[48:51], v[156:159], v[164:167], v[48:51]
	v_mfma_f32_16x16x32_bf16 v[36:39], v[148:151], v[172:175], v[36:39]
	v_mfma_f32_16x16x32_bf16 v[32:35], v[156:159], v[172:175], v[32:35]
	v_mfma_f32_16x16x32_bf16 v[20:23], v[148:151], v[180:183], v[20:23]
	v_mfma_f32_16x16x32_bf16 v[16:19], v[156:159], v[180:183], v[16:19]
	v_mfma_f32_16x16x32_bf16 v[4:7], v[148:151], v[212:215], v[4:7]
	v_mfma_f32_16x16x32_bf16 v[0:3], v[156:159], v[212:215], v[0:3]
	s_setprio 0
	s_barrier
	s_add_i32 s75, 0, 0x18000
	s_add_i32 s80, 0, 0x1c000
	v_add_u32_e32 v140, s75, v207
	v_add_u32_e32 v156, s80, v207
	ds_read_b128 v[128:131], v140
	ds_read_b128 v[132:135], v140 offset:1024
	ds_read_b128 v[136:139], v140 offset:2048
	ds_read_b128 v[140:143], v140 offset:3072
	ds_read_b128 v[144:147], v156
	ds_read_b128 v[148:151], v156 offset:1024
	ds_read_b128 v[152:155], v156 offset:2048
	ds_read_b128 v[156:159], v156 offset:3072
	s_add_u32 s36, s36, 0x40000
	s_addc_u32 s37, s37, 0
	s_mov_b32 m0, s43
	v_lshl_add_u64 v[222:223], s[36:37], 0, v[194:195]
	ds_read_b128 v[160:163], v211 offset:32768
	ds_read_b128 v[164:167], v211 offset:33792
	ds_read_b128 v[168:171], v211 offset:34816
	ds_read_b128 v[172:175], v211 offset:35840
	ds_read_b128 v[176:179], v211 offset:36864
	ds_read_b128 v[180:183], v211 offset:37888
	ds_read_b128 v[184:187], v211 offset:38912
	ds_read_b128 v[212:215], v211 offset:39936
	global_load_lds_dwordx4 v[222:223], off
	v_lshl_add_u64 v[222:223], s[36:37], 0, v[190:191]
	s_mov_b32 m0, s44
	s_nop 0
	global_load_lds_dwordx4 v[222:223], off
	s_waitcnt vmcnt(8)
	s_waitcnt lgkmcnt(0)
	s_barrier
	s_setprio 1
	v_mfma_f32_16x16x32_bf16 v[124:127], v[128:131], v[160:163], v[124:127]
	v_mfma_f32_16x16x32_bf16 v[120:123], v[136:139], v[160:163], v[120:123]
	v_mfma_f32_16x16x32_bf16 v[108:111], v[128:131], v[168:171], v[108:111]
	v_mfma_f32_16x16x32_bf16 v[104:107], v[136:139], v[168:171], v[104:107]
	v_mfma_f32_16x16x32_bf16 v[92:95], v[128:131], v[176:179], v[92:95]
	v_mfma_f32_16x16x32_bf16 v[88:91], v[136:139], v[176:179], v[88:91]
	v_mfma_f32_16x16x32_bf16 v[76:79], v[128:131], v[184:187], v[76:79]
	v_mfma_f32_16x16x32_bf16 v[72:75], v[136:139], v[184:187], v[72:75]
	v_mfma_f32_16x16x32_bf16 v[124:127], v[132:135], v[164:167], v[124:127]
	v_mfma_f32_16x16x32_bf16 v[120:123], v[140:143], v[164:167], v[120:123]
	v_mfma_f32_16x16x32_bf16 v[108:111], v[132:135], v[172:175], v[108:111]
	v_mfma_f32_16x16x32_bf16 v[104:107], v[140:143], v[172:175], v[104:107]
	v_mfma_f32_16x16x32_bf16 v[92:95], v[132:135], v[180:183], v[92:95]
	v_mfma_f32_16x16x32_bf16 v[88:91], v[140:143], v[180:183], v[88:91]
	v_mfma_f32_16x16x32_bf16 v[76:79], v[132:135], v[212:215], v[76:79]
	v_mfma_f32_16x16x32_bf16 v[72:75], v[140:143], v[212:215], v[72:75]
	s_setprio 0
	s_setprio 1
	v_mfma_f32_16x16x32_bf16 v[116:119], v[144:147], v[160:163], v[116:119]
	v_mfma_f32_16x16x32_bf16 v[112:115], v[152:155], v[160:163], v[112:115]
	v_mfma_f32_16x16x32_bf16 v[100:103], v[144:147], v[168:171], v[100:103]
	v_mfma_f32_16x16x32_bf16 v[96:99], v[152:155], v[168:171], v[96:99]
	v_mfma_f32_16x16x32_bf16 v[84:87], v[144:147], v[176:179], v[84:87]
	v_mfma_f32_16x16x32_bf16 v[80:83], v[152:155], v[176:179], v[80:83]
	v_mfma_f32_16x16x32_bf16 v[68:71], v[144:147], v[184:187], v[68:71]
	v_mfma_f32_16x16x32_bf16 v[64:67], v[152:155], v[184:187], v[64:67]
	v_mfma_f32_16x16x32_bf16 v[116:119], v[148:151], v[164:167], v[116:119]
	v_mfma_f32_16x16x32_bf16 v[112:115], v[156:159], v[164:167], v[112:115]
	v_mfma_f32_16x16x32_bf16 v[100:103], v[148:151], v[172:175], v[100:103]
	v_mfma_f32_16x16x32_bf16 v[96:99], v[156:159], v[172:175], v[96:99]
	v_mfma_f32_16x16x32_bf16 v[84:87], v[148:151], v[180:183], v[84:87]
	v_mfma_f32_16x16x32_bf16 v[80:83], v[156:159], v[180:183], v[80:83]
	v_mfma_f32_16x16x32_bf16 v[68:71], v[148:151], v[212:215], v[68:71]
	v_mfma_f32_16x16x32_bf16 v[64:67], v[156:159], v[212:215], v[64:67]
	s_setprio 0
	s_barrier
; #define PG8_STAGE(bufoff, gbase, voff) do { _Pragma("unroll") for (int _i = 0; _i < 2; ++_i) \
;         __builtin_amdgcn_global_load_lds((const unsigned*)((const char*)(gbase) + (voff)[_i]), (PG8_LAS unsigned*)(lds + (bufoff) + ldsw + _i * 8192), 16, 0, 0); } while (0)
; #define PG8_WAIT_V(n) asm volatile("s_waitcnt vmcnt(" #n ")" ::: "memory")
; #define PG8_WAIT_L(n) asm volatile("s_waitcnt lgkmcnt(" #n ")" ::: "memory")
; #define PG8_BAR __builtin_amdgcn_s_barrier()
; #define PG8_SCHED __builtin_amdgcn_sched_barrier(0)
; template <class Epi, class Sched, bool ALIGN_EPI = false, bool SP2 = false, bool FP8 = false, bool PEEL = false>
; __device__ __forceinline__ void gemm_phase(PG8_LAS unsigned char* lds, const Gemm g, const Sched& S, const Epi& E, const int wid) {
;     ...
;             PG8_LDA(At, 1, 1); PG8_STAGE(PG8_SB(1, 0), b3, voffB); PG8_STAGE(PG8_SB(1, 1), b3 + hstep, voffB); PG8_STAGE(PG8_SA(1, 0), a3, voffA);
;             PG8_WAIT_V(8); PG8_WAIT_L(0); PG8_BAR; PG8_MMA(1, 0, At, B0); PG8_MMA(1, 1, At, B1); PG8_BAR; PG8_SCHED;
;     ...
;         if constexpr (ALIGN_EPI) { if (wr == 0) PG8_BAR; }
	s_add_i32 s36, s75, s39
	v_lshl_add_u64 v[204:205], v[204:205], 0, s[10:11]
	s_mov_b32 m0, s36
	ds_read_b128 v[160:163], v211 offset:49152
	ds_read_b128 v[164:167], v211 offset:50176
	ds_read_b128 v[168:171], v211 offset:51200
	ds_read_b128 v[172:175], v211 offset:52224
	ds_read_b128 v[176:179], v211 offset:53248
	ds_read_b128 v[180:183], v211 offset:54272
	ds_read_b128 v[184:187], v211 offset:55296
	ds_read_b128 v[212:215], v211 offset:56320
	global_load_lds_dwordx4 v[204:205], off
	s_add_i32 m0, s36, 0x2000
	s_add_u32 s30, s30, 0x40080
	v_lshl_add_u64 v[204:205], v[216:217], 0, s[10:11]
	s_addc_u32 s31, s31, 0
	s_add_i32 s36, s80, s39
	global_load_lds_dwordx4 v[204:205], off
	v_lshl_add_u64 v[204:205], s[30:31], 0, v[192:193]
	s_mov_b32 m0, s36
	s_nop 0
	global_load_lds_dwordx4 v[204:205], off
	v_lshl_add_u64 v[204:205], s[30:31], 0, v[188:189]
	s_add_i32 m0, s36, 0x2000
	s_nop 0
	global_load_lds_dwordx4 v[204:205], off
	v_lshl_add_u64 v[204:205], v[218:219], 0, s[10:11]
	s_mov_b32 m0, s50
	s_nop 0
	global_load_lds_dwordx4 v[204:205], off
	v_lshl_add_u64 v[204:205], v[220:221], 0, s[10:11]
	s_mov_b32 m0, s51
	s_nop 0
	global_load_lds_dwordx4 v[204:205], off
	s_waitcnt vmcnt(8)
	s_waitcnt lgkmcnt(0)
	s_barrier
	s_setprio 1
	v_mfma_f32_16x16x32_bf16 v[60:63], v[128:131], v[160:163], v[60:63]
	v_mfma_f32_16x16x32_bf16 v[56:59], v[136:139], v[160:163], v[56:59]
	v_mfma_f32_16x16x32_bf16 v[44:47], v[128:131], v[168:171], v[44:47]
	v_mfma_f32_16x16x32_bf16 v[40:43], v[136:139], v[168:171], v[40:43]
	v_mfma_f32_16x16x32_bf16 v[28:31], v[128:131], v[176:179], v[28:31]
	v_mfma_f32_16x16x32_bf16 v[24:27], v[136:139], v[176:179], v[24:27]
	v_mfma_f32_16x16x32_bf16 v[12:15], v[128:131], v[184:187], v[12:15]
	v_mfma_f32_16x16x32_bf16 v[8:11], v[136:139], v[184:187], v[8:11]
	v_mfma_f32_16x16x32_bf16 v[60:63], v[132:135], v[164:167], v[60:63]
	v_mfma_f32_16x16x32_bf16 v[56:59], v[140:143], v[164:167], v[56:59]
	v_mfma_f32_16x16x32_bf16 v[44:47], v[132:135], v[172:175], v[44:47]
	v_mfma_f32_16x16x32_bf16 v[40:43], v[140:143], v[172:175], v[40:43]
	v_mfma_f32_16x16x32_bf16 v[28:31], v[132:135], v[180:183], v[28:31]
	v_mfma_f32_16x16x32_bf16 v[24:27], v[140:143], v[180:183], v[24:27]
	v_mfma_f32_16x16x32_bf16 v[12:15], v[132:135], v[212:215], v[12:15]
	v_mfma_f32_16x16x32_bf16 v[8:11], v[140:143], v[212:215], v[8:11]
	s_setprio 0
	s_setprio 1
	v_mfma_f32_16x16x32_bf16 v[52:55], v[144:147], v[160:163], v[52:55]
	v_mfma_f32_16x16x32_bf16 v[48:51], v[152:155], v[160:163], v[48:51]
	v_mfma_f32_16x16x32_bf16 v[36:39], v[144:147], v[168:171], v[36:39]
	v_mfma_f32_16x16x32_bf16 v[32:35], v[152:155], v[168:171], v[32:35]
	v_mfma_f32_16x16x32_bf16 v[20:23], v[144:147], v[176:179], v[20:23]
	v_mfma_f32_16x16x32_bf16 v[16:19], v[152:155], v[176:179], v[16:19]
	v_mfma_f32_16x16x32_bf16 v[4:7], v[144:147], v[184:187], v[4:7]
	v_mfma_f32_16x16x32_bf16 v[0:3], v[152:155], v[184:187], v[0:3]
	v_mfma_f32_16x16x32_bf16 v[52:55], v[148:151], v[164:167], v[52:55]
	v_mfma_f32_16x16x32_bf16 v[48:51], v[156:159], v[164:167], v[48:51]
	v_mfma_f32_16x16x32_bf16 v[36:39], v[148:151], v[172:175], v[36:39]
	v_mfma_f32_16x16x32_bf16 v[32:35], v[156:159], v[172:175], v[32:35]
	v_mfma_f32_16x16x32_bf16 v[20:23], v[148:151], v[180:183], v[20:23]
	v_mfma_f32_16x16x32_bf16 v[16:19], v[156:159], v[180:183], v[16:19]
	v_mfma_f32_16x16x32_bf16 v[4:7], v[148:151], v[212:215], v[4:7]
	v_mfma_f32_16x16x32_bf16 v[0:3], v[156:159], v[212:215], v[0:3]
	s_setprio 0
	s_barrier
	s_add_i32 s67, s67, 2
	s_add_u32 s26, s26, 0x100
	s_addc_u32 s27, s27, 0
	s_add_u32 s65, s65, 0x100
	s_addc_u32 s66, s66, 0
	s_cmp_gt_u32 s67, 13
	s_cbranch_scc0 .LBB0_1535
	s_and_b64 vcc, exec, s[8:9]
	s_cbranch_vccz .LBB0_1538
	s_barrier

; __device__ __forceinline__ unsigned cvt_pk4_fp8(float a, float b, float c, float d) { int w = 0; w = __builtin_amdgcn_cvt_pk_fp8_f32(a, b, w, false); w = __builtin_amdgcn_cvt_pk_fp8_f32(c, d, w, true); return (unsigned)w; }
; __device__ __forceinline__ float bf_lo(unsigned w) { return __uint_as_float(w << 16); }
; __device__ __forceinline__ float bf_hi(unsigned w) { return __uint_as_float(w & 0xffff0000u); }
; __device__ __forceinline__ void route_rows(Frame& F, const bf16* xin, const float* g, const float* shift, const float* scale, const float* w_router, const float* b_router,
;                                            unsigned char* XS, float* wl, int* posi, gu32* cnt) {
;     ...
; #pragma unroll
;             for (int r = 0; r < 4; ++r) { const float rs = __builtin_bit_cast(float, __builtin_amdgcn_readlane(__builtin_bit_cast(int, rstd), 16 * r));
; #pragma unroll
;                 for (int j = 0; j < 4; ++j) { const f32x4 xv = (f32x4){bf_lo(xb[r][j].x), bf_hi(xb[r][j].x), bf_lo(xb[r][j].y), bf_hi(xb[r][j].y)}; const f32x4 y = xv * rs * gs[j] + sh[j];
;                     stage[(gq * 4 + r) * 256 + lane + 64 * j] = pg8::cvt_pk4_fp8(y.x, y.y, y.z, y.w); } }
.LBB0_1648:
	s_or_b64 exec, exec, s[4:5]
	v_readlane_b32 s4, v56, 0
	s_nop 0
	v_pk_mul_f32 v[36:37], s[4:5], v[36:37] op_sel_hi:[0,1]
	v_pk_fma_f32 v[36:37], v[40:41], v[36:37], v[0:1]
	s_nop 0
	v_cvt_pk_fp8_f32 v57, v36, v37
	v_pk_mul_f32 v[36:37], s[4:5], v[50:51] op_sel_hi:[0,1]
	v_pk_fma_f32 v[36:37], v[42:43], v[36:37], v[2:3]
	v_pk_mul_f32 v[50:51], s[4:5], v[74:75] op_sel_hi:[0,1]
	v_cvt_pk_fp8_f32 v57, v36, v37 op_sel:[0,0,1]
	v_pk_mul_f32 v[36:37], s[4:5], v[66:67] op_sel_hi:[0,1]
	v_pk_fma_f32 v[36:37], v[32:33], v[36:37], v[4:5]
	v_cvt_pk_fp8_f32 v66, v36, v37
	v_pk_mul_f32 v[36:37], s[4:5], v[82:83] op_sel_hi:[0,1]
	v_pk_fma_f32 v[36:37], v[24:25], v[36:37], v[8:9]
	v_cvt_pk_fp8_f32 v67, v36, v37
	v_pk_mul_f32 v[36:37], s[4:5], v[90:91] op_sel_hi:[0,1]
	v_pk_fma_f32 v[36:37], v[26:27], v[36:37], v[10:11]
	v_pk_fma_f32 v[50:51], v[34:35], v[50:51], v[6:7]
	v_cvt_pk_fp8_f32 v67, v36, v37 op_sel:[0,0,1]
	v_pk_mul_f32 v[36:37], s[4:5], v[98:99] op_sel_hi:[0,1]
	v_cvt_pk_fp8_f32 v66, v50, v51 op_sel:[0,0,1]
	v_pk_fma_f32 v[36:37], v[16:17], v[36:37], v[12:13]
	v_cvt_pk_fp8_f32 v50, v36, v37
	v_pk_mov_b32 v[36:37], v[108:109], v[106:107] op_sel:[1,0]
	v_lshl_add_u32 v51, s45, 12, v118
	v_pk_mul_f32 v[36:37], s[4:5], v[36:37] op_sel_hi:[0,1]
	s_xor_b64 s[4:5], s[10:11], -1
	v_readlane_b32 s10, v56, 16
	v_pk_fma_f32 v[36:37], v[18:19], v[36:37], v[14:15]
	s_mov_b32 s45, 1
	v_pk_mul_f32 v[30:31], s[10:11], v[30:31] op_sel_hi:[0,1]
	v_cvt_pk_fp8_f32 v50, v36, v37 op_sel:[0,0,1]
	v_pk_mul_f32 v[36:37], s[10:11], v[46:47] op_sel_hi:[0,1]
	v_pk_fma_f32 v[30:31], v[40:41], v[30:31], v[0:1]
	v_cvt_pk_fp8_f32 v46, v30, v31
	v_pk_mul_f32 v[30:31], s[10:11], v[64:65] op_sel_hi:[0,1]
	v_pk_fma_f32 v[30:31], v[32:33], v[30:31], v[4:5]
	v_cvt_pk_fp8_f32 v47, v30, v31
	v_pk_mul_f32 v[30:31], s[10:11], v[72:73] op_sel_hi:[0,1]
	v_pk_fma_f32 v[30:31], v[34:35], v[30:31], v[6:7]
	v_pk_fma_f32 v[36:37], v[42:43], v[36:37], v[2:3]
	v_cvt_pk_fp8_f32 v47, v30, v31 op_sel:[0,0,1]
	v_pk_mul_f32 v[30:31], s[10:11], v[80:81] op_sel_hi:[0,1]
	v_cvt_pk_fp8_f32 v46, v36, v37 op_sel:[0,0,1]
	v_pk_fma_f32 v[30:31], v[24:25], v[30:31], v[8:9]
	v_cvt_pk_fp8_f32 v36, v30, v31
	v_pk_mul_f32 v[30:31], s[10:11], v[88:89] op_sel_hi:[0,1]
	v_pk_fma_f32 v[30:31], v[26:27], v[30:31], v[10:11]
	v_cvt_pk_fp8_f32 v36, v30, v31 op_sel:[0,0,1]
	v_pk_mul_f32 v[30:31], s[10:11], v[96:97] op_sel_hi:[0,1]
	v_pk_fma_f32 v[30:31], v[16:17], v[30:31], v[12:13]
	ds_write2st64_b32 v51, v57, v66 offset0:128 offset1:129
	ds_write2st64_b32 v51, v67, v50 offset0:130 offset1:131
	v_cvt_pk_fp8_f32 v37, v30, v31
	v_pk_mov_b32 v[30:31], v[104:105], v[62:63] op_sel:[1,0]
	ds_write2st64_b32 v51, v46, v47 offset0:132 offset1:133
	v_pk_mul_f32 v[30:31], s[10:11], v[30:31] op_sel_hi:[0,1]
	v_readlane_b32 s10, v56, 32
	v_pk_fma_f32 v[30:31], v[18:19], v[30:31], v[14:15]
	v_pk_mul_f32 v[28:29], s[10:11], v[28:29] op_sel_hi:[0,1]
	v_pk_fma_f32 v[28:29], v[40:41], v[28:29], v[0:1]
	v_cvt_pk_fp8_f32 v37, v30, v31 op_sel:[0,0,1]
	v_cvt_pk_fp8_f32 v46, v28, v29
	v_pk_mul_f32 v[28:29], s[10:11], v[44:45] op_sel_hi:[0,1]
	v_pk_fma_f32 v[28:29], v[42:43], v[28:29], v[2:3]
	ds_write2st64_b32 v51, v36, v37 offset0:134 offset1:135
	v_cvt_pk_fp8_f32 v46, v28, v29 op_sel:[0,0,1]
	v_pk_mul_f32 v[28:29], s[10:11], v[60:61] op_sel_hi:[0,1]
	v_pk_fma_f32 v[28:29], v[32:33], v[28:29], v[4:5]
	v_cvt_pk_fp8_f32 v36, v28, v29
	v_pk_mul_f32 v[28:29], s[10:11], v[78:79] op_sel_hi:[0,1]
	v_pk_fma_f32 v[28:29], v[24:25], v[28:29], v[8:9]
	v_cvt_pk_fp8_f32 v37, v28, v29
	v_pk_mul_f32 v[30:31], s[10:11], v[70:71] op_sel_hi:[0,1]
	v_pk_fma_f32 v[30:31], v[34:35], v[30:31], v[6:7]
	v_pk_mul_f32 v[28:29], s[10:11], v[86:87] op_sel_hi:[0,1]
	v_cvt_pk_fp8_f32 v36, v30, v31 op_sel:[0,0,1]
	v_pk_fma_f32 v[28:29], v[26:27], v[28:29], v[10:11]
	v_pk_mov_b32 v[30:31], v[102:103], v[58:59] op_sel:[1,0]
	v_cvt_pk_fp8_f32 v37, v28, v29 op_sel:[0,0,1]
	v_pk_mul_f32 v[28:29], s[10:11], v[94:95] op_sel_hi:[0,1]
	v_pk_mul_f32 v[30:31], s[10:11], v[30:31] op_sel_hi:[0,1]
	v_readlane_b32 s10, v56, 48
	v_pk_fma_f32 v[28:29], v[16:17], v[28:29], v[12:13]
	v_pk_mul_f32 v[22:23], s[10:11], v[22:23] op_sel_hi:[0,1]
	v_pk_fma_f32 v[22:23], v[40:41], v[22:23], v[0:1]
	v_cvt_pk_fp8_f32 v45, v22, v23
	v_cvt_pk_fp8_f32 v44, v28, v29
	v_pk_mul_f32 v[22:23], s[10:11], v[38:39] op_sel_hi:[0,1]
	v_pk_fma_f32 v[22:23], v[42:43], v[22:23], v[2:3]
	v_pk_fma_f32 v[30:31], v[18:19], v[30:31], v[14:15]
	v_cvt_pk_fp8_f32 v45, v22, v23 op_sel:[0,0,1]
	v_pk_mul_f32 v[22:23], s[10:11], v[52:53] op_sel_hi:[0,1]
	v_cvt_pk_fp8_f32 v44, v30, v31 op_sel:[0,0,1]
	v_pk_fma_f32 v[22:23], v[32:33], v[22:23], v[4:5]
	v_cvt_pk_fp8_f32 v30, v22, v23
	v_pk_mul_f32 v[22:23], s[10:11], v[76:77] op_sel_hi:[0,1]
	v_pk_fma_f32 v[22:23], v[24:25], v[22:23], v[8:9]
	v_cvt_pk_fp8_f32 v31, v22, v23
	v_pk_mul_f32 v[22:23], s[10:11], v[84:85] op_sel_hi:[0,1]
	v_pk_mul_f32 v[28:29], s[10:11], v[68:69] op_sel_hi:[0,1]
	v_pk_fma_f32 v[22:23], v[26:27], v[22:23], v[10:11]
	v_pk_fma_f32 v[28:29], v[34:35], v[28:29], v[6:7]
	v_cvt_pk_fp8_f32 v31, v22, v23 op_sel:[0,0,1]
	v_pk_mul_f32 v[22:23], s[10:11], v[92:93] op_sel_hi:[0,1]
	v_cvt_pk_fp8_f32 v30, v28, v29 op_sel:[0,0,1]
	v_pk_fma_f32 v[22:23], v[16:17], v[22:23], v[12:13]
	v_cvt_pk_fp8_f32 v28, v22, v23
	v_pk_mov_b32 v[22:23], v[100:101], v[54:55] op_sel:[1,0]
	s_and_b64 vcc, exec, s[4:5]
	v_pk_mul_f32 v[22:23], s[10:11], v[22:23] op_sel_hi:[0,1]
	v_pk_fma_f32 v[22:23], v[18:19], v[22:23], v[14:15]
	s_mov_b64 s[10:11], 0
	v_cvt_pk_fp8_f32 v28, v22, v23 op_sel:[0,0,1]
	ds_write2st64_b32 v51, v46, v36 offset0:136 offset1:137
	ds_write2st64_b32 v51, v37, v44 offset0:138 offset1:139
	ds_write2st64_b32 v51, v45, v30 offset0:140 offset1:141
	ds_write2st64_b32 v51, v31, v28 offset0:142 offset1:143
	s_cbranch_vccnz .LBB0_1663

; #define PG8_STAGE(bufoff, gbase, voff) do { _Pragma("unroll") for (int _i = 0; _i < 2; ++_i) \
;         __builtin_amdgcn_global_load_lds((const unsigned*)((const char*)(gbase) + (voff)[_i]), (PG8_LAS unsigned*)(lds + (bufoff) + ldsw + _i * 8192), 16, 0, 0); } while (0)
; #define PG8_WAIT_V(n) asm volatile("s_waitcnt vmcnt(" #n ")" ::: "memory")
; #define PG8_WAIT_L(n) asm volatile("s_waitcnt lgkmcnt(" #n ")" ::: "memory")
; #define PG8_BAR __builtin_amdgcn_s_barrier()
; #define PG8_SCHED __builtin_amdgcn_sched_barrier(0)
; template <class Epi, class Sched, bool ALIGN_EPI = false, bool SP2 = false, bool FP8 = false, bool PEEL = false>
; __device__ __forceinline__ void gemm_phase(PG8_LAS unsigned char* lds, const Gemm g, const Sched& S, const Epi& E, const int wid) {
;     ...
;             if (last && has_next) S.a_ready(nxt);
;             PG8_LDB(B0, 0, 0); PG8_LDB(B1, 0, 1); PG8_SCHED; PG8_LDA(At, 0, 0); PG8_STAGE(PG8_SA(1, 1), a1 + hstep, voffA);
;             PG8_WAIT_V(8); PG8_WAIT_L(0); PG8_BAR; PG8_MMAZ(0, 0, At, B0); PG8_MMAZ(0, 1, At, B1); PG8_BAR; PG8_SCHED;
;             PG8_LDA(At, 0, 1); PG8_STAGE(PG8_SB(0, 0), b2, voffB); PG8_STAGE(PG8_SB(0, 1), b2 + hstep, voffB); PG8_STAGE(PG8_SA(0, 0), a2, voffA);
;             PG8_WAIT_V(8); PG8_WAIT_L(0); PG8_BAR; PG8_MMAZ(1, 0, At, B0); PG8_MMAZ(1, 1, At, B1); PG8_BAR; PG8_SCHED;
.LBB0_1760:
	s_ashr_i32 s25, s24, 31
	s_lshl_b64 s[30:31], s[24:25], 18
	v_add_u32_e32 v186, s62, v183
	v_add_u32_e32 v187, s63, v183
	s_add_u32 s30, s34, s30
	ds_read_b128 v[16:19], v186
	ds_read_b128 v[20:23], v186 offset:1024
	ds_read_b128 v[24:27], v186 offset:2048
	ds_read_b128 v[28:31], v186 offset:3072
	ds_read_b128 v[0:3], v187
	ds_read_b128 v[4:7], v187 offset:1024
	ds_read_b128 v[8:11], v187 offset:2048
	ds_read_b128 v[12:15], v187 offset:3072
	s_addc_u32 s31, s35, s31
	s_ashr_i32 s27, s26, 31
	s_lshl_b64 s[36:37], s[26:27], 18
	s_add_u32 s36, s47, s36
	s_addc_u32 s37, s48, s37
	s_and_b64 s[42:43], s[4:5], exec
	s_cselect_b32 s25, s31, s41
	s_cselect_b32 s27, s30, s40
	s_cselect_b32 s75, s37, s39
	s_cselect_b32 s76, s36, s38
	s_add_u32 s42, s40, 0x20080
	s_addc_u32 s43, s41, 0
	s_add_i32 s77, s54, 0xc000
	v_lshl_add_u64 v[212:213], s[42:43], 0, v[160:161]
	s_mov_b32 m0, s77
	s_add_i32 s78, s54, 0xe000
	ds_read_b128 v[174:177], v185
	ds_read_b128 v[178:181], v185 offset:1024
	ds_read_b128 v[188:191], v185 offset:2048
	ds_read_b128 v[192:195], v185 offset:3072
	ds_read_b128 v[196:199], v185 offset:4096
	ds_read_b128 v[200:203], v185 offset:5120
	ds_read_b128 v[204:207], v185 offset:6144
	ds_read_b128 v[208:211], v185 offset:7168
	global_load_lds_dwordx4 v[212:213], off
	v_lshl_add_u64 v[212:213], s[42:43], 0, v[164:165]
	s_mov_b32 m0, s78
	s_nop 0
	global_load_lds_dwordx4 v[212:213], off
	s_waitcnt vmcnt(8)
	s_waitcnt lgkmcnt(0)
	s_barrier
	s_setprio 1
	v_mfma_f32_16x16x128_f8f6f4 v[156:159], v[16:23], v[174:181], 0
	v_mfma_f32_16x16x128_f8f6f4 v[152:155], v[24:31], v[174:181], 0
	v_mfma_f32_16x16x128_f8f6f4 v[148:151], v[16:23], v[188:195], 0
	v_mfma_f32_16x16x128_f8f6f4 v[144:147], v[24:31], v[188:195], 0
	v_mfma_f32_16x16x128_f8f6f4 v[140:143], v[16:23], v[196:203], 0
	v_mfma_f32_16x16x128_f8f6f4 v[136:139], v[24:31], v[196:203], 0
	v_mfma_f32_16x16x128_f8f6f4 v[132:135], v[16:23], v[204:211], 0
	v_mfma_f32_16x16x128_f8f6f4 v[128:131], v[24:31], v[204:211], 0
	s_setprio 0
	s_setprio 1
	v_mfma_f32_16x16x128_f8f6f4 v[124:127], v[0:7], v[174:181], 0
	v_mfma_f32_16x16x128_f8f6f4 v[120:123], v[8:15], v[174:181], 0
	v_mfma_f32_16x16x128_f8f6f4 v[116:119], v[0:7], v[188:195], 0
	v_mfma_f32_16x16x128_f8f6f4 v[112:115], v[8:15], v[188:195], 0
	v_mfma_f32_16x16x128_f8f6f4 v[108:111], v[0:7], v[196:203], 0
	v_mfma_f32_16x16x128_f8f6f4 v[104:107], v[8:15], v[196:203], 0
	v_mfma_f32_16x16x128_f8f6f4 v[100:103], v[0:7], v[204:211], 0
	v_mfma_f32_16x16x128_f8f6f4 v[96:99], v[8:15], v[204:211], 0
	s_setprio 0
	s_barrier
	v_lshl_add_u64 v[174:175], s[38:39], 0, v[162:163]
	s_add_i32 s79, s62, s49
	v_lshl_add_u64 v[176:177], v[174:175], 0, s[12:13]
	s_mov_b32 m0, s79
	s_add_i32 s80, s79, 0x2000
	ds_read_b128 v[188:191], v185 offset:16384
	ds_read_b128 v[192:195], v185 offset:17408
	ds_read_b128 v[196:199], v185 offset:18432
	ds_read_b128 v[200:203], v185 offset:19456
	ds_read_b128 v[204:207], v185 offset:20480
	ds_read_b128 v[208:211], v185 offset:21504
	ds_read_b128 v[212:215], v185 offset:22528
	ds_read_b128 v[216:219], v185 offset:23552
	global_load_lds_dwordx4 v[176:177], off
	v_lshl_add_u64 v[176:177], s[38:39], 0, v[166:167]
	s_add_u32 s42, s38, 0x20100
	v_lshl_add_u64 v[178:179], v[176:177], 0, s[12:13]
	s_mov_b32 m0, s80
	s_addc_u32 s43, s39, 0
	s_add_i32 s81, s63, s49
	global_load_lds_dwordx4 v[178:179], off
	v_lshl_add_u64 v[178:179], s[42:43], 0, v[162:163]
	s_mov_b32 m0, s81
	s_add_i32 s82, s81, 0x2000
	global_load_lds_dwordx4 v[178:179], off
	v_lshl_add_u64 v[178:179], s[42:43], 0, v[166:167]
	s_mov_b32 m0, s82
	s_nop 0
	global_load_lds_dwordx4 v[178:179], off
	v_lshl_add_u64 v[178:179], s[40:41], 0, v[160:161]
	v_lshl_add_u64 v[180:181], v[178:179], 0, s[12:13]
	s_mov_b32 m0, s54
	s_nop 0
	global_load_lds_dwordx4 v[180:181], off
	v_lshl_add_u64 v[180:181], s[40:41], 0, v[164:165]
	v_lshl_add_u64 v[220:221], v[180:181], 0, s[12:13]
	s_mov_b32 m0, s55
	s_nop 0
	global_load_lds_dwordx4 v[220:221], off
	s_waitcnt vmcnt(8)
	s_waitcnt lgkmcnt(0)
	s_barrier
	s_setprio 1
	v_mfma_f32_16x16x128_f8f6f4 v[92:95], v[16:23], v[188:195], 0
	v_mfma_f32_16x16x128_f8f6f4 v[88:91], v[24:31], v[188:195], 0
	v_mfma_f32_16x16x128_f8f6f4 v[84:87], v[16:23], v[196:203], 0
	v_mfma_f32_16x16x128_f8f6f4 v[80:83], v[24:31], v[196:203], 0
	v_mfma_f32_16x16x128_f8f6f4 v[76:79], v[16:23], v[204:211], 0
	v_mfma_f32_16x16x128_f8f6f4 v[72:75], v[24:31], v[204:211], 0
	v_mfma_f32_16x16x128_f8f6f4 v[68:71], v[16:23], v[212:219], 0
	v_mfma_f32_16x16x128_f8f6f4 v[64:67], v[24:31], v[212:219], 0
	s_setprio 0
	s_setprio 1
	v_mfma_f32_16x16x128_f8f6f4 v[60:63], v[0:7], v[188:195], 0
	v_mfma_f32_16x16x128_f8f6f4 v[56:59], v[8:15], v[188:195], 0
	v_mfma_f32_16x16x128_f8f6f4 v[52:55], v[0:7], v[196:203], 0
	v_mfma_f32_16x16x128_f8f6f4 v[48:51], v[8:15], v[196:203], 0
	v_mfma_f32_16x16x128_f8f6f4 v[44:47], v[0:7], v[204:211], 0
	v_mfma_f32_16x16x128_f8f6f4 v[40:43], v[8:15], v[204:211], 0
	v_mfma_f32_16x16x128_f8f6f4 v[36:39], v[0:7], v[212:219], 0
	v_mfma_f32_16x16x128_f8f6f4 v[32:35], v[8:15], v[212:219], 0
	s_setprio 0
	s_barrier
; #define PG8_STAGE(bufoff, gbase, voff) do { _Pragma("unroll") for (int _i = 0; _i < 2; ++_i) \
;         __builtin_amdgcn_global_load_lds((const unsigned*)((const char*)(gbase) + (voff)[_i]), (PG8_LAS unsigned*)(lds + (bufoff) + ldsw + _i * 8192), 16, 0, 0); } while (0)
; #define PG8_WAIT_V(n) asm volatile("s_waitcnt vmcnt(" #n ")" ::: "memory")
; #define PG8_WAIT_L(n) asm volatile("s_waitcnt lgkmcnt(" #n ")" ::: "memory")
; #define PG8_BAR __builtin_amdgcn_s_barrier()
; #define PG8_SCHED __builtin_amdgcn_sched_barrier(0)
; template <class Epi, class Sched, bool ALIGN_EPI = false, bool SP2 = false, bool FP8 = false, bool PEEL = false>
; __device__ __forceinline__ void gemm_phase(PG8_LAS unsigned char* lds, const Gemm g, const Sched& S, const Epi& E, const int wid) {
;     ...
;             PG8_LDB(B0, 1, 0); PG8_LDB(B1, 1, 1); PG8_SCHED; PG8_LDA(At, 1, 0); PG8_STAGE(PG8_SA(0, 1), a2 + hstep, voffA);
;             PG8_WAIT_V(8); PG8_WAIT_L(0); PG8_BAR; PG8_MMA(0, 0, At, B0); PG8_MMA(0, 1, At, B1); PG8_BAR; PG8_SCHED;
;             PG8_LDA(At, 1, 1); PG8_STAGE(PG8_SB(1, 0), b3, voffB); PG8_STAGE(PG8_SB(1, 1), b3 + hstep, voffB); PG8_STAGE(PG8_SA(1, 0), a3, voffA);
;             PG8_WAIT_V(8); PG8_WAIT_L(0); PG8_BAR; PG8_MMA(1, 0, At, B0); PG8_MMA(1, 1, At, B1); PG8_BAR; PG8_SCHED;
	s_add_i32 s83, 0, 0x18000
	s_add_i32 s85, 0, 0x1c000
	v_add_u32_e32 v188, s83, v183
	v_add_u32_e32 v189, s85, v183
	ds_read_b128 v[16:19], v188
	ds_read_b128 v[20:23], v188 offset:1024
	ds_read_b128 v[24:27], v188 offset:2048
	ds_read_b128 v[28:31], v188 offset:3072
	ds_read_b128 v[0:3], v189
	ds_read_b128 v[4:7], v189 offset:1024
	ds_read_b128 v[8:11], v189 offset:2048
	ds_read_b128 v[12:15], v189 offset:3072
	s_add_u32 s42, s40, 0x20100
	s_addc_u32 s43, s41, 0
	s_mov_b32 m0, s56
	v_lshl_add_u64 v[222:223], s[42:43], 0, v[160:161]
	ds_read_b128 v[190:193], v185 offset:32768
	ds_read_b128 v[194:197], v185 offset:33792
	ds_read_b128 v[198:201], v185 offset:34816
	ds_read_b128 v[202:205], v185 offset:35840
	ds_read_b128 v[206:209], v185 offset:36864
	ds_read_b128 v[210:213], v185 offset:37888
	ds_read_b128 v[214:217], v185 offset:38912
	ds_read_b128 v[218:221], v185 offset:39936
	global_load_lds_dwordx4 v[222:223], off
	v_lshl_add_u64 v[222:223], s[42:43], 0, v[164:165]
	s_mov_b32 m0, s57
	s_nop 0
	global_load_lds_dwordx4 v[222:223], off
	s_waitcnt vmcnt(8)
	s_waitcnt lgkmcnt(0)
	s_barrier
	s_setprio 1
	v_mfma_f32_16x16x128_f8f6f4 v[156:159], v[16:23], v[190:197], v[156:159]
	v_mfma_f32_16x16x128_f8f6f4 v[152:155], v[24:31], v[190:197], v[152:155]
	v_mfma_f32_16x16x128_f8f6f4 v[148:151], v[16:23], v[198:205], v[148:151]
	v_mfma_f32_16x16x128_f8f6f4 v[144:147], v[24:31], v[198:205], v[144:147]
	v_mfma_f32_16x16x128_f8f6f4 v[140:143], v[16:23], v[206:213], v[140:143]
	v_mfma_f32_16x16x128_f8f6f4 v[136:139], v[24:31], v[206:213], v[136:139]
	v_mfma_f32_16x16x128_f8f6f4 v[132:135], v[16:23], v[214:221], v[132:135]
	v_mfma_f32_16x16x128_f8f6f4 v[128:131], v[24:31], v[214:221], v[128:131]
	s_setprio 0
	s_setprio 1
	v_mfma_f32_16x16x128_f8f6f4 v[124:127], v[0:7], v[190:197], v[124:127]
	v_mfma_f32_16x16x128_f8f6f4 v[120:123], v[8:15], v[190:197], v[120:123]
	v_mfma_f32_16x16x128_f8f6f4 v[116:119], v[0:7], v[198:205], v[116:119]
	v_mfma_f32_16x16x128_f8f6f4 v[112:115], v[8:15], v[198:205], v[112:115]
	v_mfma_f32_16x16x128_f8f6f4 v[108:111], v[0:7], v[206:213], v[108:111]
	v_mfma_f32_16x16x128_f8f6f4 v[104:107], v[8:15], v[206:213], v[104:107]
	v_mfma_f32_16x16x128_f8f6f4 v[100:103], v[0:7], v[214:221], v[100:103]
	v_mfma_f32_16x16x128_f8f6f4 v[96:99], v[8:15], v[214:221], v[96:99]
	s_setprio 0
	s_barrier
	s_add_i32 s83, s83, s49
	s_add_i32 s84, s83, 0x2000
	v_lshl_add_u64 v[174:175], v[174:175], 0, s[14:15]
	s_mov_b32 m0, s83
	s_add_u32 s42, s38, 0x20180
	ds_read_b128 v[190:193], v185 offset:49152
	ds_read_b128 v[194:197], v185 offset:50176
	ds_read_b128 v[198:201], v185 offset:51200
	ds_read_b128 v[202:205], v185 offset:52224
	ds_read_b128 v[206:209], v185 offset:53248
	ds_read_b128 v[210:213], v185 offset:54272
	ds_read_b128 v[214:217], v185 offset:55296
	ds_read_b128 v[218:221], v185 offset:56320
	global_load_lds_dwordx4 v[174:175], off
	v_lshl_add_u64 v[174:175], v[176:177], 0, s[14:15]
	s_mov_b32 m0, s84
	s_addc_u32 s43, s39, 0
	s_add_i32 s85, s85, s49
	global_load_lds_dwordx4 v[174:175], off
	v_lshl_add_u64 v[174:175], s[42:43], 0, v[162:163]
	s_mov_b32 m0, s85
	s_add_i32 s86, s85, 0x2000
	global_load_lds_dwordx4 v[174:175], off
	v_lshl_add_u64 v[174:175], s[42:43], 0, v[166:167]
	s_mov_b32 m0, s86
	s_nop 0
	global_load_lds_dwordx4 v[174:175], off
	v_lshl_add_u64 v[174:175], v[178:179], 0, s[14:15]
	s_mov_b32 m0, s60
	s_nop 0
	global_load_lds_dwordx4 v[174:175], off
	v_lshl_add_u64 v[174:175], v[180:181], 0, s[14:15]
	s_mov_b32 m0, s61
	s_nop 0
	global_load_lds_dwordx4 v[174:175], off
	s_waitcnt vmcnt(8)
	s_waitcnt lgkmcnt(0)
	s_barrier
	s_setprio 1
	v_mfma_f32_16x16x128_f8f6f4 v[92:95], v[16:23], v[190:197], v[92:95]
	v_mfma_f32_16x16x128_f8f6f4 v[88:91], v[24:31], v[190:197], v[88:91]
	v_mfma_f32_16x16x128_f8f6f4 v[84:87], v[16:23], v[198:205], v[84:87]
	v_mfma_f32_16x16x128_f8f6f4 v[80:83], v[24:31], v[198:205], v[80:83]
	v_mfma_f32_16x16x128_f8f6f4 v[76:79], v[16:23], v[206:213], v[76:79]
	v_mfma_f32_16x16x128_f8f6f4 v[72:75], v[24:31], v[206:213], v[72:75]
	v_mfma_f32_16x16x128_f8f6f4 v[68:71], v[16:23], v[214:221], v[68:71]
	v_mfma_f32_16x16x128_f8f6f4 v[64:67], v[24:31], v[214:221], v[64:67]
	s_setprio 0
	s_setprio 1
	v_mfma_f32_16x16x128_f8f6f4 v[60:63], v[0:7], v[190:197], v[60:63]
	v_mfma_f32_16x16x128_f8f6f4 v[56:59], v[8:15], v[190:197], v[56:59]
	v_mfma_f32_16x16x128_f8f6f4 v[52:55], v[0:7], v[198:205], v[52:55]
	v_mfma_f32_16x16x128_f8f6f4 v[48:51], v[8:15], v[198:205], v[48:51]
	v_mfma_f32_16x16x128_f8f6f4 v[44:47], v[0:7], v[206:213], v[44:47]
	v_mfma_f32_16x16x128_f8f6f4 v[40:43], v[8:15], v[206:213], v[40:43]
	v_mfma_f32_16x16x128_f8f6f4 v[36:39], v[0:7], v[214:221], v[36:39]
	v_mfma_f32_16x16x128_f8f6f4 v[32:35], v[8:15], v[214:221], v[32:35]
	s_setprio 0
	s_barrier
	s_add_u32 s40, s40, 0x20180
	s_addc_u32 s41, s41, 0
	s_add_u32 s87, s38, 0x200
	s_addc_u32 s88, s39, 0
	s_mov_b32 s89, 0
; #define PG8_STAGE(bufoff, gbase, voff) do { _Pragma("unroll") for (int _i = 0; _i < 2; ++_i) \
;         __builtin_amdgcn_global_load_lds((const unsigned*)((const char*)(gbase) + (voff)[_i]), (PG8_LAS unsigned*)(lds + (bufoff) + ldsw + _i * 8192), 16, 0, 0); } while (0)
; #define PG8_WAIT_V(n) asm volatile("s_waitcnt vmcnt(" #n ")" ::: "memory")
; #define PG8_WAIT_L(n) asm volatile("s_waitcnt lgkmcnt(" #n ")" ::: "memory")
; #define PG8_BAR __builtin_amdgcn_s_barrier()
; #define PG8_SCHED __builtin_amdgcn_sched_barrier(0)
; template <class Epi, class Sched, bool ALIGN_EPI = false, bool SP2 = false, bool FP8 = false, bool PEEL = false>
; __device__ __forceinline__ void gemm_phase(PG8_LAS unsigned char* lds, const Gemm g, const Sched& S, const Epi& E, const int wid) {
;     ...
;             PG8_LDB(B0, 0, 0); PG8_LDB(B1, 0, 1); PG8_SCHED; PG8_LDA(At, 0, 0); PG8_STAGE(PG8_SA(1, 1), a1 + hstep, voffA);
;             PG8_WAIT_V(8); PG8_WAIT_L(0); PG8_BAR; PG8_MMA(0, 0, At, B0); PG8_MMA(0, 1, At, B1); PG8_BAR; PG8_SCHED;
;             PG8_LDA(At, 0, 1); PG8_STAGE(PG8_SB(0, 0), b2, voffB); PG8_STAGE(PG8_SB(0, 1), b2 + hstep, voffB); PG8_STAGE(PG8_SA(0, 0), a2, voffA);
;             PG8_WAIT_V(8); PG8_WAIT_L(0); PG8_BAR; PG8_MMA(1, 0, At, B0); PG8_MMA(1, 1, At, B1); PG8_BAR; PG8_SCHED;
;             PG8_LDB(B0, 1, 0); PG8_LDB(B1, 1, 1); PG8_SCHED; PG8_LDA(At, 1, 0); PG8_STAGE(PG8_SA(0, 1), a2 + hstep, voffA);
.LBB0_1761:
	ds_read_b128 v[0:3], v186
	ds_read_b128 v[4:7], v186 offset:1024
	ds_read_b128 v[16:19], v186 offset:2048
	ds_read_b128 v[20:23], v186 offset:3072
	ds_read_b128 v[24:27], v187
	ds_read_b128 v[28:31], v187 offset:1024
	ds_read_b128 v[174:177], v187 offset:2048
	ds_read_b128 v[178:181], v187 offset:3072
	s_add_u32 s38, s40, 0xfffe0080
	s_addc_u32 s39, s41, -1
	s_cmp_eq_u32 s89, 4
	s_cselect_b32 s43, s25, s39
	s_cselect_b32 s42, s27, s38
	s_cselect_b32 s39, s75, s88
	s_cselect_b32 s38, s76, s87
	s_mov_b32 m0, s77
	v_lshl_add_u64 v[214:215], s[40:41], 0, v[168:169]
	ds_read_b128 v[8:11], v185
	ds_read_b128 v[12:15], v185 offset:1024
	ds_read_b128 v[190:193], v185 offset:2048
	ds_read_b128 v[194:197], v185 offset:3072
	ds_read_b128 v[198:201], v185 offset:4096
	ds_read_b128 v[202:205], v185 offset:5120
	ds_read_b128 v[206:209], v185 offset:6144
	ds_read_b128 v[210:213], v185 offset:7168
	global_load_lds_dwordx4 v[214:215], off
	v_lshl_add_u64 v[214:215], s[40:41], 0, v[170:171]
	s_mov_b32 m0, s78
	s_nop 0
	global_load_lds_dwordx4 v[214:215], off
	s_waitcnt vmcnt(8)
	s_waitcnt lgkmcnt(0)
	s_barrier
	s_setprio 1
	v_mfma_f32_16x16x128_f8f6f4 v[156:159], v[0:7], v[8:15], v[156:159]
	v_mfma_f32_16x16x128_f8f6f4 v[152:155], v[16:23], v[8:15], v[152:155]
	v_mfma_f32_16x16x128_f8f6f4 v[148:151], v[0:7], v[190:197], v[148:151]
	v_mfma_f32_16x16x128_f8f6f4 v[144:147], v[16:23], v[190:197], v[144:147]
	v_mfma_f32_16x16x128_f8f6f4 v[140:143], v[0:7], v[198:205], v[140:143]
	v_mfma_f32_16x16x128_f8f6f4 v[136:139], v[16:23], v[198:205], v[136:139]
	v_mfma_f32_16x16x128_f8f6f4 v[132:135], v[0:7], v[206:213], v[132:135]
	v_mfma_f32_16x16x128_f8f6f4 v[128:131], v[16:23], v[206:213], v[128:131]
	s_setprio 0
	s_setprio 1
	v_mfma_f32_16x16x128_f8f6f4 v[124:127], v[24:31], v[8:15], v[124:127]
	v_mfma_f32_16x16x128_f8f6f4 v[120:123], v[174:181], v[8:15], v[120:123]
	v_mfma_f32_16x16x128_f8f6f4 v[116:119], v[24:31], v[190:197], v[116:119]
	v_mfma_f32_16x16x128_f8f6f4 v[112:115], v[174:181], v[190:197], v[112:115]
	v_mfma_f32_16x16x128_f8f6f4 v[108:111], v[24:31], v[198:205], v[108:111]
	v_mfma_f32_16x16x128_f8f6f4 v[104:107], v[174:181], v[198:205], v[104:107]
	v_mfma_f32_16x16x128_f8f6f4 v[100:103], v[24:31], v[206:213], v[100:103]
	v_mfma_f32_16x16x128_f8f6f4 v[96:99], v[174:181], v[206:213], v[96:99]
	s_setprio 0
	s_barrier
	s_mov_b32 m0, s79
	v_lshl_add_u64 v[8:9], s[38:39], 0, v[162:163]
	s_add_u32 s90, s38, 0x20000
	ds_read_b128 v[190:193], v185 offset:16384
	ds_read_b128 v[194:197], v185 offset:17408
	ds_read_b128 v[198:201], v185 offset:18432
	ds_read_b128 v[202:205], v185 offset:19456
	ds_read_b128 v[206:209], v185 offset:20480
	ds_read_b128 v[210:213], v185 offset:21504
	ds_read_b128 v[214:217], v185 offset:22528
	ds_read_b128 v[218:221], v185 offset:23552
	global_load_lds_dwordx4 v[8:9], off
	v_lshl_add_u64 v[10:11], s[38:39], 0, v[166:167]
	s_mov_b32 m0, s80
	s_addc_u32 s91, s39, 0
	global_load_lds_dwordx4 v[10:11], off
	v_lshl_add_u64 v[12:13], s[90:91], 0, v[162:163]
	s_mov_b32 m0, s81
	v_lshl_add_u64 v[14:15], s[42:43], 0, v[164:165]
	global_load_lds_dwordx4 v[12:13], off
	v_lshl_add_u64 v[12:13], s[90:91], 0, v[166:167]
	s_mov_b32 m0, s82
	s_nop 0
	global_load_lds_dwordx4 v[12:13], off
	v_lshl_add_u64 v[12:13], s[42:43], 0, v[160:161]
	s_mov_b32 m0, s54
	s_nop 0
	global_load_lds_dwordx4 v[12:13], off
	s_mov_b32 m0, s55
	s_nop 0
	global_load_lds_dwordx4 v[14:15], off
	s_waitcnt vmcnt(8)
	s_waitcnt lgkmcnt(0)
	s_barrier
	s_setprio 1
	v_mfma_f32_16x16x128_f8f6f4 v[92:95], v[0:7], v[190:197], v[92:95]
	v_mfma_f32_16x16x128_f8f6f4 v[88:91], v[16:23], v[190:197], v[88:91]
	v_mfma_f32_16x16x128_f8f6f4 v[84:87], v[0:7], v[198:205], v[84:87]
	v_mfma_f32_16x16x128_f8f6f4 v[80:83], v[16:23], v[198:205], v[80:83]
	v_mfma_f32_16x16x128_f8f6f4 v[76:79], v[0:7], v[206:213], v[76:79]
	v_mfma_f32_16x16x128_f8f6f4 v[72:75], v[16:23], v[206:213], v[72:75]
	v_mfma_f32_16x16x128_f8f6f4 v[68:71], v[0:7], v[214:221], v[68:71]
	v_mfma_f32_16x16x128_f8f6f4 v[64:67], v[16:23], v[214:221], v[64:67]
	s_setprio 0
	s_setprio 1
	v_mfma_f32_16x16x128_f8f6f4 v[60:63], v[24:31], v[190:197], v[60:63]
	v_mfma_f32_16x16x128_f8f6f4 v[56:59], v[174:181], v[190:197], v[56:59]
	v_mfma_f32_16x16x128_f8f6f4 v[52:55], v[24:31], v[198:205], v[52:55]
	v_mfma_f32_16x16x128_f8f6f4 v[48:51], v[174:181], v[198:205], v[48:51]
	v_mfma_f32_16x16x128_f8f6f4 v[44:47], v[24:31], v[206:213], v[44:47]
	v_mfma_f32_16x16x128_f8f6f4 v[40:43], v[174:181], v[206:213], v[40:43]
	v_mfma_f32_16x16x128_f8f6f4 v[36:39], v[24:31], v[214:221], v[36:39]
	v_mfma_f32_16x16x128_f8f6f4 v[32:35], v[174:181], v[214:221], v[32:35]
	s_setprio 0
	s_barrier
	ds_read_b128 v[16:19], v188
	ds_read_b128 v[20:23], v188 offset:1024
	ds_read_b128 v[24:27], v188 offset:2048
	ds_read_b128 v[28:31], v188 offset:3072
	ds_read_b128 v[0:3], v189
	ds_read_b128 v[4:7], v189 offset:1024
	ds_read_b128 v[174:177], v189 offset:2048
	ds_read_b128 v[178:181], v189 offset:3072
	s_add_u32 s42, s42, 0x20000
	s_addc_u32 s43, s43, 0
	s_mov_b32 m0, s56
	v_lshl_add_u64 v[222:223], s[42:43], 0, v[160:161]
	ds_read_b128 v[190:193], v185 offset:32768
	ds_read_b128 v[194:197], v185 offset:33792
	ds_read_b128 v[198:201], v185 offset:34816
	ds_read_b128 v[202:205], v185 offset:35840
	ds_read_b128 v[206:209], v185 offset:36864
	ds_read_b128 v[210:213], v185 offset:37888
	ds_read_b128 v[214:217], v185 offset:38912
	ds_read_b128 v[218:221], v185 offset:39936
	global_load_lds_dwordx4 v[222:223], off
	v_lshl_add_u64 v[222:223], s[42:43], 0, v[164:165]
	s_mov_b32 m0, s57
	s_nop 0
	global_load_lds_dwordx4 v[222:223], off
	s_waitcnt vmcnt(8)
	s_waitcnt lgkmcnt(0)
	s_barrier
; __device__ __forceinline__ unsigned cvt_pk4_fp8(float a, float b, float c, float d) { int w = 0; w = __builtin_amdgcn_cvt_pk_fp8_f32(a, b, w, false); w = __builtin_amdgcn_cvt_pk_fp8_f32(c, d, w, true); return (unsigned)w; }
; #define PG8_STAGE(bufoff, gbase, voff) do { _Pragma("unroll") for (int _i = 0; _i < 2; ++_i) \
;         __builtin_amdgcn_global_load_lds((const unsigned*)((const char*)(gbase) + (voff)[_i]), (PG8_LAS unsigned*)(lds + (bufoff) + ldsw + _i * 8192), 16, 0, 0); } while (0)
;     __device__ __forceinline__ void operator()(const f32x4 (&acc)[2][2][4][2], const Unit& u, int wr, int wc, int fr, int fq) const {
;     ...
;             for (int m = 0; m < 4; ++m) { const size_t off = (size_t)(row0 + ai * HALF + m * 16) * ldc + col0;
;                 const f32x4 g0 = acc[ai][0][m][0], g1 = acc[ai][0][m][1], u0 = acc[ai][1][m][0], u1 = acc[ai][1][m][1];
;                 float v[8];
;                 { const f32x2p a = silu_mul2k((f32x2p){g0[0], g0[1]}, (f32x2p){u0[0], u0[1]}, kt, ci), b = silu_mul2k((f32x2p){g0[2], g0[3]}, (f32x2p){u0[2], u0[3]}, kt, ci), c = silu_mul2k((f32x2p){g1[0], g1[1]}, (f32x2p){u1[0], u1[1]}, kt, ci), d = silu_mul2k((f32x2p){g1[2], g1[3]}, (f32x2p){u1[2], u1[3]}, kt, ci);
;                   v[0] = a.x; v[1] = a.y; v[2] = b.x; v[3] = b.y; v[4] = c.x; v[5] = c.y; v[6] = d.x; v[7] = d.y; }
;                 if constexpr (FP8OUT) { typedef unsigned u32x2 __attribute__((ext_vector_type(2))); u32x2 w; w.x = cvt_pk4_fp8(v[0], v[1], v[2], v[3]); w.y = cvt_pk4_fp8(v[4], v[5], v[6], v[7]); __builtin_nontemporal_store(w, (u32x2*)((unsigned char*)O + off)); }
; template <class Epi, class Sched, bool ALIGN_EPI = false, bool SP2 = false, bool FP8 = false, bool PEEL = false>
; __device__ __forceinline__ void gemm_phase(PG8_LAS unsigned char* lds, const Gemm g, const Sched& S, const Epi& E, const int wid) {
;     ...
;             PG8_LDB(B0, 1, 0); PG8_LDB(B1, 1, 1); PG8_SCHED; PG8_LDA(At, 1, 0); PG8_STAGE(PG8_SA(0, 1), a2 + hstep, voffA);
;             PG8_WAIT_V(8); PG8_WAIT_L(0); PG8_BAR; PG8_MMA(0, 0, At, B0); PG8_MMA(0, 1, At, B1); PG8_BAR; PG8_SCHED;
;             PG8_LDA(At, 1, 1); PG8_STAGE(PG8_SB(1, 0), b3, voffB); PG8_STAGE(PG8_SB(1, 1), b3 + hstep, voffB); PG8_STAGE(PG8_SA(1, 0), a3, voffA);
;             PG8_WAIT_V(8); PG8_WAIT_L(0); PG8_BAR; PG8_MMA(1, 0, At, B0); PG8_MMA(1, 1, At, B1); PG8_BAR; PG8_SCHED;
	s_setprio 1
	v_mfma_f32_16x16x128_f8f6f4 v[156:159], v[16:23], v[190:197], v[156:159]
	v_mfma_f32_16x16x128_f8f6f4 v[152:155], v[24:31], v[190:197], v[152:155]
	v_mfma_f32_16x16x128_f8f6f4 v[148:151], v[16:23], v[198:205], v[148:151]
	v_mfma_f32_16x16x128_f8f6f4 v[144:147], v[24:31], v[198:205], v[144:147]
	v_mfma_f32_16x16x128_f8f6f4 v[140:143], v[16:23], v[206:213], v[140:143]
	v_mfma_f32_16x16x128_f8f6f4 v[136:139], v[24:31], v[206:213], v[136:139]
	v_mfma_f32_16x16x128_f8f6f4 v[132:135], v[16:23], v[214:221], v[132:135]
	v_mfma_f32_16x16x128_f8f6f4 v[128:131], v[24:31], v[214:221], v[128:131]
	s_setprio 0
	s_setprio 1
	v_mfma_f32_16x16x128_f8f6f4 v[124:127], v[0:7], v[190:197], v[124:127]
	v_mfma_f32_16x16x128_f8f6f4 v[120:123], v[174:181], v[190:197], v[120:123]
	v_mfma_f32_16x16x128_f8f6f4 v[116:119], v[0:7], v[198:205], v[116:119]
	v_mfma_f32_16x16x128_f8f6f4 v[112:115], v[174:181], v[198:205], v[112:115]
	v_mfma_f32_16x16x128_f8f6f4 v[108:111], v[0:7], v[206:213], v[108:111]
	v_mfma_f32_16x16x128_f8f6f4 v[104:107], v[174:181], v[206:213], v[104:107]
	v_mfma_f32_16x16x128_f8f6f4 v[100:103], v[0:7], v[214:221], v[100:103]
	v_mfma_f32_16x16x128_f8f6f4 v[96:99], v[174:181], v[214:221], v[96:99]
	s_setprio 0
	s_barrier
	s_mov_b32 m0, s83
	v_lshl_add_u64 v[8:9], v[8:9], 0, s[10:11]
	s_add_u32 s38, s38, 0x20080
	ds_read_b128 v[190:193], v185 offset:49152
	ds_read_b128 v[194:197], v185 offset:50176
	ds_read_b128 v[198:201], v185 offset:51200
	ds_read_b128 v[202:205], v185 offset:52224
	ds_read_b128 v[206:209], v185 offset:53248
	ds_read_b128 v[210:213], v185 offset:54272
	ds_read_b128 v[214:217], v185 offset:55296
	ds_read_b128 v[218:221], v185 offset:56320
	global_load_lds_dwordx4 v[8:9], off
	v_lshl_add_u64 v[8:9], v[10:11], 0, s[10:11]
	s_mov_b32 m0, s84
	s_addc_u32 s39, s39, 0
	global_load_lds_dwordx4 v[8:9], off
	v_lshl_add_u64 v[8:9], s[38:39], 0, v[162:163]
	s_mov_b32 m0, s85
	s_nop 0
	global_load_lds_dwordx4 v[8:9], off
	v_lshl_add_u64 v[8:9], s[38:39], 0, v[166:167]
	s_mov_b32 m0, s86
	s_nop 0
	global_load_lds_dwordx4 v[8:9], off
	v_lshl_add_u64 v[8:9], v[12:13], 0, s[10:11]
	s_mov_b32 m0, s60
	s_nop 0
	global_load_lds_dwordx4 v[8:9], off
	v_lshl_add_u64 v[8:9], v[14:15], 0, s[10:11]
	s_mov_b32 m0, s61
	s_nop 0
	global_load_lds_dwordx4 v[8:9], off
	s_waitcnt vmcnt(8)
	s_waitcnt lgkmcnt(0)
	s_barrier
	s_setprio 1
	v_mfma_f32_16x16x128_f8f6f4 v[92:95], v[16:23], v[190:197], v[92:95]
	v_mfma_f32_16x16x128_f8f6f4 v[88:91], v[24:31], v[190:197], v[88:91]
	v_mfma_f32_16x16x128_f8f6f4 v[84:87], v[16:23], v[198:205], v[84:87]
	v_mfma_f32_16x16x128_f8f6f4 v[80:83], v[24:31], v[198:205], v[80:83]
	v_mfma_f32_16x16x128_f8f6f4 v[76:79], v[16:23], v[206:213], v[76:79]
	v_mfma_f32_16x16x128_f8f6f4 v[72:75], v[24:31], v[206:213], v[72:75]
	v_mfma_f32_16x16x128_f8f6f4 v[68:71], v[16:23], v[214:221], v[68:71]
	v_mfma_f32_16x16x128_f8f6f4 v[64:67], v[24:31], v[214:221], v[64:67]
	s_setprio 0
	s_setprio 1
	v_mfma_f32_16x16x128_f8f6f4 v[60:63], v[0:7], v[190:197], v[60:63]
	v_mfma_f32_16x16x128_f8f6f4 v[56:59], v[174:181], v[190:197], v[56:59]
	v_mfma_f32_16x16x128_f8f6f4 v[52:55], v[0:7], v[198:205], v[52:55]
	v_mfma_f32_16x16x128_f8f6f4 v[48:51], v[174:181], v[198:205], v[48:51]
	v_mfma_f32_16x16x128_f8f6f4 v[44:47], v[0:7], v[206:213], v[44:47]
	v_mfma_f32_16x16x128_f8f6f4 v[40:43], v[174:181], v[206:213], v[40:43]
	v_mfma_f32_16x16x128_f8f6f4 v[36:39], v[0:7], v[214:221], v[36:39]
	v_mfma_f32_16x16x128_f8f6f4 v[32:35], v[174:181], v[214:221], v[32:35]
	s_setprio 0
	s_barrier
	s_add_i32 s89, s89, 2
	s_add_u32 s40, s40, 0x100
	s_addc_u32 s41, s41, 0
	s_add_u32 s87, s87, 0x100
	s_addc_u32 s88, s88, 0
	s_cmp_gt_u32 s89, 5
	s_cbranch_scc0 .LBB0_1761
	v_readlane_b32 s76, v254, 57
	s_and_b64 vcc, exec, s[8:9]
	v_readlane_b32 s77, v254, 58
	v_readlane_b32 s78, v254, 59
	v_readlane_b32 s79, v254, 60
	v_readlane_b32 s80, v254, 61
	v_readlane_b32 s81, v254, 62
	v_readlane_b32 s82, v254, 63
	v_readlane_b32 s83, v255, 0
	s_cbranch_vccz .LBB0_1764
	s_barrier
.LBB0_1764:
	v_pk_mul_f32 v[0:1], v[156:157], s[16:17] op_sel_hi:[1,0]
	v_pk_mul_f32 v[8:9], v[156:157], v[124:125]
	v_exp_f32_e32 v2, v0
	v_exp_f32_e32 v3, v1
	v_pk_mul_f32 v[10:11], v[152:153], s[16:17] op_sel_hi:[1,0]
	v_pk_mul_f32 v[12:13], v[154:155], s[16:17] op_sel_hi:[1,0]
	v_exp_f32_e32 v10, v10
	v_pk_fma_f32 v[2:3], v[2:3], s[22:23], s[22:23] op_sel_hi:[1,0,0]
	v_exp_f32_e32 v11, v11
	v_rcp_f32_e32 v2, v2
	v_rcp_f32_e32 v3, v3
	v_exp_f32_e32 v12, v12
	v_pk_fma_f32 v[10:11], v[10:11], s[22:23], s[22:23] op_sel_hi:[1,0,0]
	v_exp_f32_e32 v13, v13
	v_pk_mul_f32 v[2:3], v[8:9], v[2:3]
	v_pk_mul_f32 v[8:9], v[158:159], s[16:17] op_sel_hi:[1,0]
	v_rcp_f32_e32 v10, v10
	v_exp_f32_e32 v8, v8
	v_exp_f32_e32 v9, v9
	v_rcp_f32_e32 v11, v11
	v_pk_mul_f32 v[6:7], v[158:159], v[126:127]
	v_add_u32_e32 v4, s74, v182
	v_pk_fma_f32 v[8:9], v[8:9], s[22:23], s[22:23] op_sel_hi:[1,0,0]
	v_lshl_add_u32 v0, s67, 7, v184
	v_rcp_f32_e32 v8, v8
	v_rcp_f32_e32 v9, v9
	v_ashrrev_i32_e32 v1, 31, v0
	s_nop 15
	s_nop 15
	v_pk_mul_f32 v[14:15], v[146:147], s[16:17] op_sel_hi:[1,0]
	v_pk_mul_f32 v[6:7], v[6:7], v[8:9]
	v_pk_mul_f32 v[8:9], v[152:153], v[120:121]
	v_exp_f32_e32 v14, v14
	v_pk_mul_f32 v[8:9], v[8:9], v[10:11]
	v_pk_fma_f32 v[10:11], v[12:13], s[22:23], s[22:23] op_sel_hi:[1,0,0]
	v_cvt_pk_fp8_f32 v12, v2, v3
	v_rcp_f32_e32 v10, v10
	v_rcp_f32_e32 v11, v11
	v_cvt_pk_fp8_f32 v12, v6, v7 op_sel:[0,0,1]
	v_pk_mul_f32 v[6:7], v[148:149], s[16:17] op_sel_hi:[1,0]
	v_cvt_pk_fp8_f32 v13, v8, v9
	v_exp_f32_e32 v6, v6
	v_exp_f32_e32 v7, v7
	v_pk_mul_f32 v[2:3], v[154:155], v[122:123]
	v_exp_f32_e32 v15, v15
; __device__ __forceinline__ unsigned cvt_pk4_fp8(float a, float b, float c, float d) { int w = 0; w = __builtin_amdgcn_cvt_pk_fp8_f32(a, b, w, false); w = __builtin_amdgcn_cvt_pk_fp8_f32(c, d, w, true); return (unsigned)w; }
; __device__ __forceinline__ f32x2p silu_mul2k(f32x2p ag, f32x2p au, float kt, float ci) { const f32x2p t = ag * kt; f32x2p e; e.x = __builtin_amdgcn_exp2f(t.x); e.y = __builtin_amdgcn_exp2f(t.y);
;     const f32x2p d = e * ci + ci; f32x2p r; r.x = __builtin_amdgcn_rcpf(d.x); r.y = __builtin_amdgcn_rcpf(d.y); return (ag * au) * r; }
;     __device__ __forceinline__ void operator()(const f32x4 (&acc)[2][2][4][2], const Unit& u, int wr, int wc, int fr, int fq) const {
;     ...
;             for (int m = 0; m < 4; ++m) { const size_t off = (size_t)(row0 + ai * HALF + m * 16) * ldc + col0;
;                 const f32x4 g0 = acc[ai][0][m][0], g1 = acc[ai][0][m][1], u0 = acc[ai][1][m][0], u1 = acc[ai][1][m][1];
;                 float v[8];
;                 { const f32x2p a = silu_mul2k((f32x2p){g0[0], g0[1]}, (f32x2p){u0[0], u0[1]}, kt, ci), b = silu_mul2k((f32x2p){g0[2], g0[3]}, (f32x2p){u0[2], u0[3]}, kt, ci), c = silu_mul2k((f32x2p){g1[0], g1[1]}, (f32x2p){u1[0], u1[1]}, kt, ci), d = silu_mul2k((f32x2p){g1[2], g1[3]}, (f32x2p){u1[2], u1[3]}, kt, ci);
;                   v[0] = a.x; v[1] = a.y; v[2] = b.x; v[3] = b.y; v[4] = c.x; v[5] = c.y; v[6] = d.x; v[7] = d.y; }
;                 if constexpr (FP8OUT) { typedef unsigned u32x2 __attribute__((ext_vector_type(2))); u32x2 w; w.x = cvt_pk4_fp8(v[0], v[1], v[2], v[3]); w.y = cvt_pk4_fp8(v[4], v[5], v[6], v[7]); __builtin_nontemporal_store(w, (u32x2*)((unsigned char*)O + off)); }
	v_pk_mul_f32 v[2:3], v[2:3], v[10:11]
	v_pk_fma_f32 v[6:7], v[6:7], s[22:23], s[22:23] op_sel_hi:[1,0,0]
	v_cvt_pk_fp8_f32 v13, v2, v3 op_sel:[0,0,1]
	v_rcp_f32_e32 v6, v6
	v_rcp_f32_e32 v7, v7
	v_mov_b64_e32 v[2:3], s[20:21]
	v_mad_i64_i32 v[8:9], s[38:39], v4, s64, v[2:3]
	v_pk_mul_f32 v[10:11], v[148:149], v[116:117]
	v_lshl_add_u64 v[8:9], v[8:9], 0, v[0:1]
	v_pk_mul_f32 v[6:7], v[10:11], v[6:7]
	v_pk_mul_f32 v[10:11], v[150:151], s[16:17] op_sel_hi:[1,0]
	global_store_dwordx2 v[8:9], v[12:13], off
	v_exp_f32_e32 v10, v10
	v_exp_f32_e32 v11, v11
	v_pk_mul_f32 v[12:13], v[144:145], s[16:17] op_sel_hi:[1,0]
	v_pk_mul_f32 v[8:9], v[150:151], v[118:119]
	v_exp_f32_e32 v12, v12
	v_exp_f32_e32 v13, v13
	v_pk_fma_f32 v[10:11], v[10:11], s[22:23], s[22:23] op_sel_hi:[1,0,0]
	v_add_u32_e32 v5, 16, v4
	v_rcp_f32_e32 v10, v10
	v_rcp_f32_e32 v11, v11
	v_pk_fma_f32 v[12:13], v[12:13], s[22:23], s[22:23] op_sel_hi:[1,0,0]
	s_andn2_b64 vcc, exec, s[4:5]
	v_rcp_f32_e32 v12, v12
	v_rcp_f32_e32 v13, v13
	v_pk_mul_f32 v[8:9], v[8:9], v[10:11]
	v_pk_mul_f32 v[10:11], v[144:145], v[112:113]
	s_mov_b64 s[4:5], -1
	v_pk_mul_f32 v[10:11], v[10:11], v[12:13]
	v_pk_fma_f32 v[12:13], v[14:15], s[22:23], s[22:23] op_sel_hi:[1,0,0]
	v_rcp_f32_e32 v12, v12
	v_rcp_f32_e32 v13, v13
	v_cvt_pk_fp8_f32 v15, v10, v11
	v_cvt_pk_fp8_f32 v14, v6, v7
	v_pk_mul_f32 v[6:7], v[146:147], v[114:115]
	v_pk_mul_f32 v[10:11], v[140:141], v[108:109]
	v_pk_mul_f32 v[6:7], v[6:7], v[12:13]
	v_pk_mul_f32 v[12:13], v[136:137], s[16:17] op_sel_hi:[1,0]
	v_cvt_pk_fp8_f32 v15, v6, v7 op_sel:[0,0,1]
	v_pk_mul_f32 v[6:7], v[140:141], s[16:17] op_sel_hi:[1,0]
	v_cvt_pk_fp8_f32 v14, v8, v9 op_sel:[0,0,1]
	v_exp_f32_e32 v6, v6
	v_exp_f32_e32 v7, v7
	v_exp_f32_e32 v12, v12
	v_exp_f32_e32 v13, v13
	v_mad_i64_i32 v[8:9], s[38:39], v5, s64, v[2:3]
	v_pk_fma_f32 v[6:7], v[6:7], s[22:23], s[22:23] op_sel_hi:[1,0,0]
	v_lshl_add_u64 v[8:9], v[8:9], 0, v[0:1]
	v_rcp_f32_e32 v6, v6
	v_rcp_f32_e32 v7, v7
	global_store_dwordx2 v[8:9], v[14:15], off
	v_pk_fma_f32 v[12:13], v[12:13], s[22:23], s[22:23] op_sel_hi:[1,0,0]
	v_pk_mul_f32 v[14:15], v[138:139], s[16:17] op_sel_hi:[1,0]
	v_pk_mul_f32 v[6:7], v[10:11], v[6:7]
	v_pk_mul_f32 v[10:11], v[142:143], s[16:17] op_sel_hi:[1,0]
	v_rcp_f32_e32 v12, v12
	v_exp_f32_e32 v10, v10
	v_exp_f32_e32 v11, v11
	v_rcp_f32_e32 v13, v13
	v_exp_f32_e32 v14, v14
	v_exp_f32_e32 v15, v15
	v_pk_fma_f32 v[10:11], v[10:11], s[22:23], s[22:23] op_sel_hi:[1,0,0]
	v_pk_mul_f32 v[8:9], v[142:143], v[110:111]
	v_rcp_f32_e32 v10, v10
	v_rcp_f32_e32 v11, v11
	v_add_u32_e32 v5, 32, v4
	v_pk_mul_f32 v[8:9], v[8:9], v[10:11]
	v_pk_mul_f32 v[10:11], v[136:137], v[104:105]
	s_nop 0
	v_pk_mul_f32 v[10:11], v[10:11], v[12:13]
	v_pk_fma_f32 v[12:13], v[14:15], s[22:23], s[22:23] op_sel_hi:[1,0,0]
	v_rcp_f32_e32 v12, v12
	v_rcp_f32_e32 v13, v13
	v_cvt_pk_fp8_f32 v15, v10, v11
	v_cvt_pk_fp8_f32 v14, v6, v7
	v_pk_mul_f32 v[6:7], v[138:139], v[106:107]
	v_pk_mul_f32 v[10:11], v[132:133], v[100:101]
	v_pk_mul_f32 v[6:7], v[6:7], v[12:13]
	v_pk_mul_f32 v[12:13], v[128:129], s[16:17] op_sel_hi:[1,0]
	v_cvt_pk_fp8_f32 v15, v6, v7 op_sel:[0,0,1]
	v_pk_mul_f32 v[6:7], v[132:133], s[16:17] op_sel_hi:[1,0]
	v_cvt_pk_fp8_f32 v14, v8, v9 op_sel:[0,0,1]
	v_exp_f32_e32 v6, v6
	v_exp_f32_e32 v7, v7
	v_exp_f32_e32 v12, v12
	v_exp_f32_e32 v13, v13
	v_mad_i64_i32 v[8:9], s[38:39], v5, s64, v[2:3]
	v_pk_fma_f32 v[6:7], v[6:7], s[22:23], s[22:23] op_sel_hi:[1,0,0]
	v_lshl_add_u64 v[8:9], v[8:9], 0, v[0:1]
	v_rcp_f32_e32 v6, v6
	v_rcp_f32_e32 v7, v7
	global_store_dwordx2 v[8:9], v[14:15], off
	v_pk_fma_f32 v[12:13], v[12:13], s[22:23], s[22:23] op_sel_hi:[1,0,0]
	v_pk_mul_f32 v[14:15], v[130:131], s[16:17] op_sel_hi:[1,0]
	v_pk_mul_f32 v[6:7], v[10:11], v[6:7]
	v_pk_mul_f32 v[10:11], v[134:135], s[16:17] op_sel_hi:[1,0]
	v_rcp_f32_e32 v12, v12
	v_exp_f32_e32 v10, v10
	v_exp_f32_e32 v11, v11
	v_rcp_f32_e32 v13, v13
	v_exp_f32_e32 v14, v14
	v_exp_f32_e32 v15, v15
	v_pk_fma_f32 v[10:11], v[10:11], s[22:23], s[22:23] op_sel_hi:[1,0,0]
	v_pk_mul_f32 v[8:9], v[134:135], v[102:103]
	v_rcp_f32_e32 v10, v10
	v_rcp_f32_e32 v11, v11
	v_add_u32_e32 v5, 48, v4
	v_pk_mul_f32 v[8:9], v[8:9], v[10:11]
	v_pk_mul_f32 v[10:11], v[128:129], v[96:97]
	s_nop 0
	v_pk_mul_f32 v[10:11], v[10:11], v[12:13]
	v_pk_fma_f32 v[12:13], v[14:15], s[22:23], s[22:23] op_sel_hi:[1,0,0]
	v_rcp_f32_e32 v12, v12
	v_rcp_f32_e32 v13, v13
	v_cvt_pk_fp8_f32 v15, v10, v11
	v_cvt_pk_fp8_f32 v14, v6, v7
	v_pk_mul_f32 v[6:7], v[130:131], v[98:99]
	v_pk_mul_f32 v[10:11], v[92:93], v[60:61]
	v_pk_mul_f32 v[6:7], v[6:7], v[12:13]
	v_pk_mul_f32 v[12:13], v[88:89], s[16:17] op_sel_hi:[1,0]
	v_cvt_pk_fp8_f32 v15, v6, v7 op_sel:[0,0,1]
	v_pk_mul_f32 v[6:7], v[92:93], s[16:17] op_sel_hi:[1,0]
	v_cvt_pk_fp8_f32 v14, v8, v9 op_sel:[0,0,1]
	v_exp_f32_e32 v6, v6
	v_exp_f32_e32 v7, v7
	v_exp_f32_e32 v12, v12
	v_exp_f32_e32 v13, v13
	v_mad_i64_i32 v[8:9], s[38:39], v5, s64, v[2:3]
	v_pk_fma_f32 v[6:7], v[6:7], s[22:23], s[22:23] op_sel_hi:[1,0,0]
	v_lshl_add_u64 v[8:9], v[8:9], 0, v[0:1]
	v_rcp_f32_e32 v6, v6
	v_rcp_f32_e32 v7, v7
	global_store_dwordx2 v[8:9], v[14:15], off
	v_pk_fma_f32 v[12:13], v[12:13], s[22:23], s[22:23] op_sel_hi:[1,0,0]
	v_pk_mul_f32 v[14:15], v[90:91], s[16:17] op_sel_hi:[1,0]
	v_pk_mul_f32 v[6:7], v[10:11], v[6:7]
	v_pk_mul_f32 v[10:11], v[94:95], s[16:17] op_sel_hi:[1,0]
	v_rcp_f32_e32 v12, v12
	v_exp_f32_e32 v10, v10
	v_exp_f32_e32 v11, v11
	v_rcp_f32_e32 v13, v13
	v_exp_f32_e32 v14, v14
	v_exp_f32_e32 v15, v15
; __device__ __forceinline__ unsigned cvt_pk4_fp8(float a, float b, float c, float d) { int w = 0; w = __builtin_amdgcn_cvt_pk_fp8_f32(a, b, w, false); w = __builtin_amdgcn_cvt_pk_fp8_f32(c, d, w, true); return (unsigned)w; }
; __device__ __forceinline__ f32x2p silu_mul2k(f32x2p ag, f32x2p au, float kt, float ci) { const f32x2p t = ag * kt; f32x2p e; e.x = __builtin_amdgcn_exp2f(t.x); e.y = __builtin_amdgcn_exp2f(t.y);
;     const f32x2p d = e * ci + ci; f32x2p r; r.x = __builtin_amdgcn_rcpf(d.x); r.y = __builtin_amdgcn_rcpf(d.y); return (ag * au) * r; }
;     __device__ __forceinline__ void operator()(const f32x4 (&acc)[2][2][4][2], const Unit& u, int wr, int wc, int fr, int fq) const {
;     ...
;             for (int m = 0; m < 4; ++m) { const size_t off = (size_t)(row0 + ai * HALF + m * 16) * ldc + col0;
;                 const f32x4 g0 = acc[ai][0][m][0], g1 = acc[ai][0][m][1], u0 = acc[ai][1][m][0], u1 = acc[ai][1][m][1];
;                 float v[8];
;                 { const f32x2p a = silu_mul2k((f32x2p){g0[0], g0[1]}, (f32x2p){u0[0], u0[1]}, kt, ci), b = silu_mul2k((f32x2p){g0[2], g0[3]}, (f32x2p){u0[2], u0[3]}, kt, ci), c = silu_mul2k((f32x2p){g1[0], g1[1]}, (f32x2p){u1[0], u1[1]}, kt, ci), d = silu_mul2k((f32x2p){g1[2], g1[3]}, (f32x2p){u1[2], u1[3]}, kt, ci);
;                   v[0] = a.x; v[1] = a.y; v[2] = b.x; v[3] = b.y; v[4] = c.x; v[5] = c.y; v[6] = d.x; v[7] = d.y; }
;                 if constexpr (FP8OUT) { typedef unsigned u32x2 __attribute__((ext_vector_type(2))); u32x2 w; w.x = cvt_pk4_fp8(v[0], v[1], v[2], v[3]); w.y = cvt_pk4_fp8(v[4], v[5], v[6], v[7]); __builtin_nontemporal_store(w, (u32x2*)((unsigned char*)O + off)); }
	v_pk_fma_f32 v[10:11], v[10:11], s[22:23], s[22:23] op_sel_hi:[1,0,0]
	v_pk_mul_f32 v[8:9], v[94:95], v[62:63]
	v_rcp_f32_e32 v10, v10
	v_rcp_f32_e32 v11, v11
	v_add_u32_e32 v5, 0x80, v4
	v_pk_mul_f32 v[8:9], v[8:9], v[10:11]
	v_pk_mul_f32 v[10:11], v[88:89], v[56:57]
	s_nop 0
	v_pk_mul_f32 v[10:11], v[10:11], v[12:13]
	v_pk_fma_f32 v[12:13], v[14:15], s[22:23], s[22:23] op_sel_hi:[1,0,0]
	v_rcp_f32_e32 v12, v12
	v_rcp_f32_e32 v13, v13
	v_cvt_pk_fp8_f32 v15, v10, v11
	v_cvt_pk_fp8_f32 v14, v6, v7
	v_pk_mul_f32 v[6:7], v[90:91], v[58:59]
	v_pk_mul_f32 v[10:11], v[84:85], v[52:53]
	v_pk_mul_f32 v[6:7], v[6:7], v[12:13]
	v_pk_mul_f32 v[12:13], v[80:81], s[16:17] op_sel_hi:[1,0]
	v_cvt_pk_fp8_f32 v15, v6, v7 op_sel:[0,0,1]
	v_pk_mul_f32 v[6:7], v[84:85], s[16:17] op_sel_hi:[1,0]
	v_cvt_pk_fp8_f32 v14, v8, v9 op_sel:[0,0,1]
	v_exp_f32_e32 v6, v6
	v_exp_f32_e32 v7, v7
	v_exp_f32_e32 v12, v12
	v_exp_f32_e32 v13, v13
	v_mad_i64_i32 v[8:9], s[38:39], v5, s64, v[2:3]
	v_pk_fma_f32 v[6:7], v[6:7], s[22:23], s[22:23] op_sel_hi:[1,0,0]
	v_lshl_add_u64 v[8:9], v[8:9], 0, v[0:1]
	v_rcp_f32_e32 v6, v6
	v_rcp_f32_e32 v7, v7
	global_store_dwordx2 v[8:9], v[14:15], off
	v_pk_fma_f32 v[12:13], v[12:13], s[22:23], s[22:23] op_sel_hi:[1,0,0]
	v_pk_mul_f32 v[14:15], v[82:83], s[16:17] op_sel_hi:[1,0]
	v_pk_mul_f32 v[6:7], v[10:11], v[6:7]
	v_pk_mul_f32 v[10:11], v[86:87], s[16:17] op_sel_hi:[1,0]
	v_rcp_f32_e32 v12, v12
	v_exp_f32_e32 v10, v10
	v_exp_f32_e32 v11, v11
	v_rcp_f32_e32 v13, v13
	v_exp_f32_e32 v14, v14
	v_exp_f32_e32 v15, v15
	v_pk_fma_f32 v[10:11], v[10:11], s[22:23], s[22:23] op_sel_hi:[1,0,0]
	v_pk_mul_f32 v[8:9], v[86:87], v[54:55]
	v_rcp_f32_e32 v10, v10
	v_rcp_f32_e32 v11, v11
	v_add_u32_e32 v5, 0x90, v4
	v_pk_mul_f32 v[8:9], v[8:9], v[10:11]
	v_pk_mul_f32 v[10:11], v[80:81], v[48:49]
	s_nop 0
	v_pk_mul_f32 v[10:11], v[10:11], v[12:13]
	v_pk_fma_f32 v[12:13], v[14:15], s[22:23], s[22:23] op_sel_hi:[1,0,0]
	v_rcp_f32_e32 v12, v12
	v_rcp_f32_e32 v13, v13
	v_cvt_pk_fp8_f32 v15, v10, v11
	v_cvt_pk_fp8_f32 v14, v6, v7
	v_pk_mul_f32 v[6:7], v[82:83], v[50:51]
	v_pk_mul_f32 v[10:11], v[76:77], v[44:45]
	v_pk_mul_f32 v[6:7], v[6:7], v[12:13]
	v_pk_mul_f32 v[12:13], v[72:73], s[16:17] op_sel_hi:[1,0]
	v_cvt_pk_fp8_f32 v15, v6, v7 op_sel:[0,0,1]
	v_pk_mul_f32 v[6:7], v[76:77], s[16:17] op_sel_hi:[1,0]
	v_cvt_pk_fp8_f32 v14, v8, v9 op_sel:[0,0,1]
	v_exp_f32_e32 v6, v6
	v_exp_f32_e32 v7, v7
	v_exp_f32_e32 v12, v12
	v_exp_f32_e32 v13, v13
	v_mad_i64_i32 v[8:9], s[38:39], v5, s64, v[2:3]
	v_pk_fma_f32 v[6:7], v[6:7], s[22:23], s[22:23] op_sel_hi:[1,0,0]
	v_lshl_add_u64 v[8:9], v[8:9], 0, v[0:1]
	v_rcp_f32_e32 v6, v6
	v_rcp_f32_e32 v7, v7
	global_store_dwordx2 v[8:9], v[14:15], off
	v_pk_fma_f32 v[12:13], v[12:13], s[22:23], s[22:23] op_sel_hi:[1,0,0]
	v_pk_mul_f32 v[14:15], v[74:75], s[16:17] op_sel_hi:[1,0]
	v_pk_mul_f32 v[6:7], v[10:11], v[6:7]
	v_pk_mul_f32 v[10:11], v[78:79], s[16:17] op_sel_hi:[1,0]
	v_rcp_f32_e32 v12, v12
	v_exp_f32_e32 v10, v10
	v_exp_f32_e32 v11, v11
	v_rcp_f32_e32 v13, v13
	v_exp_f32_e32 v14, v14
	v_exp_f32_e32 v15, v15
	v_pk_fma_f32 v[10:11], v[10:11], s[22:23], s[22:23] op_sel_hi:[1,0,0]
	v_pk_mul_f32 v[8:9], v[78:79], v[46:47]
	v_rcp_f32_e32 v10, v10
	v_rcp_f32_e32 v11, v11
	v_add_u32_e32 v5, 0xa0, v4
	v_pk_mul_f32 v[8:9], v[8:9], v[10:11]
	v_pk_mul_f32 v[10:11], v[72:73], v[40:41]
	s_nop 0
	v_pk_mul_f32 v[10:11], v[10:11], v[12:13]
	v_pk_fma_f32 v[12:13], v[14:15], s[22:23], s[22:23] op_sel_hi:[1,0,0]
	v_rcp_f32_e32 v12, v12
	v_rcp_f32_e32 v13, v13
	v_cvt_pk_fp8_f32 v15, v10, v11
	v_cvt_pk_fp8_f32 v14, v6, v7
	v_pk_mul_f32 v[6:7], v[74:75], v[42:43]
	v_pk_mul_f32 v[10:11], v[64:65], s[16:17] op_sel_hi:[1,0]
	v_pk_mul_f32 v[6:7], v[6:7], v[12:13]
	v_cvt_pk_fp8_f32 v14, v8, v9 op_sel:[0,0,1]
	v_cvt_pk_fp8_f32 v15, v6, v7 op_sel:[0,0,1]
	v_pk_mul_f32 v[6:7], v[68:69], s[16:17] op_sel_hi:[1,0]
	v_mad_i64_i32 v[8:9], s[38:39], v5, s64, v[2:3]
	v_exp_f32_e32 v6, v6
	v_exp_f32_e32 v7, v7
	v_lshl_add_u64 v[8:9], v[8:9], 0, v[0:1]
	global_store_dwordx2 v[8:9], v[14:15], off
	v_pk_mul_f32 v[8:9], v[68:69], v[36:37]
	v_pk_fma_f32 v[6:7], v[6:7], s[22:23], s[22:23] op_sel_hi:[1,0,0]
	v_exp_f32_e32 v10, v10
	v_rcp_f32_e32 v6, v6
	v_rcp_f32_e32 v7, v7
	v_exp_f32_e32 v11, v11
	v_pk_mul_f32 v[12:13], v[66:67], s[16:17] op_sel_hi:[1,0]
	v_add_u32_e32 v14, 0xb0, v4
	v_pk_mul_f32 v[6:7], v[8:9], v[6:7]
	v_pk_mul_f32 v[8:9], v[70:71], s[16:17] op_sel_hi:[1,0]
	v_pk_fma_f32 v[10:11], v[10:11], s[22:23], s[22:23] op_sel_hi:[1,0,0]
	v_exp_f32_e32 v8, v8
	v_exp_f32_e32 v9, v9
	v_rcp_f32_e32 v10, v10
	v_rcp_f32_e32 v11, v11
	v_exp_f32_e32 v12, v12
	v_pk_fma_f32 v[8:9], v[8:9], s[22:23], s[22:23] op_sel_hi:[1,0,0]
	v_exp_f32_e32 v13, v13
	v_rcp_f32_e32 v8, v8
	v_rcp_f32_e32 v9, v9
	v_pk_mul_f32 v[4:5], v[70:71], v[38:39]
	v_mad_i64_i32 v[2:3], s[38:39], v14, s64, v[2:3]
	v_pk_mul_f32 v[4:5], v[4:5], v[8:9]
	v_pk_mul_f32 v[8:9], v[64:65], v[32:33]
	v_lshl_add_u64 v[0:1], v[2:3], 0, v[0:1]
	v_pk_mul_f32 v[8:9], v[8:9], v[10:11]
	v_pk_fma_f32 v[10:11], v[12:13], s[22:23], s[22:23] op_sel_hi:[1,0,0]
	v_rcp_f32_e32 v10, v10
	v_rcp_f32_e32 v11, v11
	v_cvt_pk_fp8_f32 v12, v6, v7
	v_cvt_pk_fp8_f32 v13, v8, v9
	v_pk_mul_f32 v[6:7], v[66:67], v[34:35]
	v_cvt_pk_fp8_f32 v12, v4, v5 op_sel:[0,0,1]
	v_pk_mul_f32 v[6:7], v[6:7], v[10:11]
	s_nop 0
	v_cvt_pk_fp8_f32 v13, v6, v7 op_sel:[0,0,1]
	global_store_dwordx2 v[0:1], v[12:13], off
	s_cbranch_vccnz .LBB0_1753
	s_andn2_b64 vcc, exec, s[6:7]
	s_cbranch_vccnz .LBB0_1752
	s_barrier
	s_branch .LBB0_1752

; #define PG8_STAGE(bufoff, gbase, voff) do { _Pragma("unroll") for (int _i = 0; _i < 2; ++_i) \
;         __builtin_amdgcn_global_load_lds((const unsigned*)((const char*)(gbase) + (voff)[_i]), (PG8_LAS unsigned*)(lds + (bufoff) + ldsw + _i * 8192), 16, 0, 0); } while (0)
; #define PG8_WAIT_V(n) asm volatile("s_waitcnt vmcnt(" #n ")" ::: "memory")
; #define PG8_WAIT_L(n) asm volatile("s_waitcnt lgkmcnt(" #n ")" ::: "memory")
; #define PG8_BAR __builtin_amdgcn_s_barrier()
; #define PG8_SCHED __builtin_amdgcn_sched_barrier(0)
; template <class Epi, class Sched, bool ALIGN_EPI = false, bool SP2 = false, bool FP8 = false, bool PEEL = false>
; __device__ __forceinline__ void gemm_phase(PG8_LAS unsigned char* lds, const Gemm g, const Sched& S, const Epi& E, const int wid) {
;     ...
;             PG8_LDB(B0, 0, 0); PG8_LDB(B1, 0, 1); PG8_SCHED; PG8_LDA(At, 0, 0); PG8_STAGE(PG8_SA(1, 1), a1 + hstep, voffA);
;             PG8_WAIT_V(8); PG8_WAIT_L(0); PG8_BAR; PG8_MMAZ(0, 0, At, B0); PG8_MMAZ(0, 1, At, B1); PG8_BAR; PG8_SCHED;
;             PG8_LDA(At, 0, 1); PG8_STAGE(PG8_SB(0, 0), b2, voffB); PG8_STAGE(PG8_SB(0, 1), b2 + hstep, voffB); PG8_STAGE(PG8_SA(0, 0), a2, voffA);
;             PG8_WAIT_V(8); PG8_WAIT_L(0); PG8_BAR; PG8_MMAZ(1, 0, At, B0); PG8_MMAZ(1, 1, At, B1); PG8_BAR; PG8_SCHED;
;             PG8_LDB(B0, 1, 0); PG8_LDB(B1, 1, 1); PG8_SCHED; PG8_LDA(At, 1, 0); PG8_STAGE(PG8_SA(0, 1), a2 + hstep, voffA);
.LBB0_1852:
	v_add_u32_e32 v187, s65, v185
	v_add_u32_e32 v188, s66, v185
	ds_read_b128 v[16:19], v187
	ds_read_b128 v[20:23], v187 offset:1024
	ds_read_b128 v[24:27], v187 offset:2048
	ds_read_b128 v[28:31], v187 offset:3072
	ds_read_b128 v[0:3], v188
	ds_read_b128 v[4:7], v188 offset:1024
	ds_read_b128 v[8:11], v188 offset:2048
	ds_read_b128 v[12:15], v188 offset:3072
	s_add_u32 s40, s36, 0x70080
	s_addc_u32 s41, s37, 0
	s_add_i32 s80, s59, 0xc000
	v_lshl_add_u64 v[214:215], s[40:41], 0, v[160:161]
	s_mov_b32 m0, s80
	s_add_i32 s81, s59, 0xe000
	ds_read_b128 v[176:179], v186
	ds_read_b128 v[180:183], v186 offset:1024
	ds_read_b128 v[190:193], v186 offset:2048
	ds_read_b128 v[194:197], v186 offset:3072
	ds_read_b128 v[198:201], v186 offset:4096
	ds_read_b128 v[202:205], v186 offset:5120
	ds_read_b128 v[206:209], v186 offset:6144
	ds_read_b128 v[210:213], v186 offset:7168
	global_load_lds_dwordx4 v[214:215], off
	v_lshl_add_u64 v[214:215], s[40:41], 0, v[164:165]
	s_mov_b32 m0, s81
	s_nop 0
	global_load_lds_dwordx4 v[214:215], off
	s_waitcnt vmcnt(8)
	s_waitcnt lgkmcnt(0)
	s_barrier
	s_setprio 1
	v_mfma_f32_16x16x128_f8f6f4 v[156:159], v[16:23], v[176:183], 0
	v_mfma_f32_16x16x128_f8f6f4 v[152:155], v[24:31], v[176:183], 0
	v_mfma_f32_16x16x128_f8f6f4 v[148:151], v[16:23], v[190:197], 0
	v_mfma_f32_16x16x128_f8f6f4 v[144:147], v[24:31], v[190:197], 0
	v_mfma_f32_16x16x128_f8f6f4 v[140:143], v[16:23], v[198:205], 0
	v_mfma_f32_16x16x128_f8f6f4 v[136:139], v[24:31], v[198:205], 0
	v_mfma_f32_16x16x128_f8f6f4 v[132:135], v[16:23], v[206:213], 0
	v_mfma_f32_16x16x128_f8f6f4 v[128:131], v[24:31], v[206:213], 0
	s_setprio 0
	s_setprio 1
	v_mfma_f32_16x16x128_f8f6f4 v[124:127], v[0:7], v[176:183], 0
	v_mfma_f32_16x16x128_f8f6f4 v[120:123], v[8:15], v[176:183], 0
	v_mfma_f32_16x16x128_f8f6f4 v[116:119], v[0:7], v[190:197], 0
	v_mfma_f32_16x16x128_f8f6f4 v[112:115], v[8:15], v[190:197], 0
	v_mfma_f32_16x16x128_f8f6f4 v[108:111], v[0:7], v[198:205], 0
	v_mfma_f32_16x16x128_f8f6f4 v[104:107], v[8:15], v[198:205], 0
	v_mfma_f32_16x16x128_f8f6f4 v[100:103], v[0:7], v[206:213], 0
	v_mfma_f32_16x16x128_f8f6f4 v[96:99], v[8:15], v[206:213], 0
	s_setprio 0
	s_barrier
	v_lshl_add_u64 v[176:177], s[38:39], 0, v[162:163]
	s_add_i32 s82, s65, s54
	v_lshl_add_u64 v[178:179], v[176:177], 0, s[24:25]
	s_mov_b32 m0, s82
	s_add_i32 s83, s82, 0x2000
	ds_read_b128 v[190:193], v186 offset:16384
	ds_read_b128 v[194:197], v186 offset:17408
	ds_read_b128 v[198:201], v186 offset:18432
	ds_read_b128 v[202:205], v186 offset:19456
	ds_read_b128 v[206:209], v186 offset:20480
	ds_read_b128 v[210:213], v186 offset:21504
	ds_read_b128 v[214:217], v186 offset:22528
	ds_read_b128 v[218:221], v186 offset:23552
	global_load_lds_dwordx4 v[178:179], off
	v_lshl_add_u64 v[178:179], s[38:39], 0, v[166:167]
	s_add_u32 s40, s38, 0x70100
	v_lshl_add_u64 v[180:181], v[178:179], 0, s[24:25]
	s_mov_b32 m0, s83
	s_addc_u32 s41, s39, 0
	s_add_i32 s84, s66, s54
	global_load_lds_dwordx4 v[180:181], off
	v_lshl_add_u64 v[180:181], s[40:41], 0, v[162:163]
	s_mov_b32 m0, s84
	s_add_i32 s85, s84, 0x2000
	global_load_lds_dwordx4 v[180:181], off
	v_lshl_add_u64 v[180:181], s[40:41], 0, v[166:167]
	s_mov_b32 m0, s85
	s_nop 0
	global_load_lds_dwordx4 v[180:181], off
	v_lshl_add_u64 v[180:181], s[36:37], 0, v[160:161]
	v_lshl_add_u64 v[182:183], v[180:181], 0, s[24:25]
	s_mov_b32 m0, s59
	s_nop 0
	global_load_lds_dwordx4 v[182:183], off
	v_lshl_add_u64 v[182:183], s[36:37], 0, v[164:165]
	v_lshl_add_u64 v[222:223], v[182:183], 0, s[24:25]
	s_mov_b32 m0, s60
	s_nop 0
	global_load_lds_dwordx4 v[222:223], off
	s_waitcnt vmcnt(8)
	s_waitcnt lgkmcnt(0)
	s_barrier
	s_setprio 1
	v_mfma_f32_16x16x128_f8f6f4 v[92:95], v[16:23], v[190:197], 0
	v_mfma_f32_16x16x128_f8f6f4 v[88:91], v[24:31], v[190:197], 0
	v_mfma_f32_16x16x128_f8f6f4 v[84:87], v[16:23], v[198:205], 0
	v_mfma_f32_16x16x128_f8f6f4 v[80:83], v[24:31], v[198:205], 0
	v_mfma_f32_16x16x128_f8f6f4 v[76:79], v[16:23], v[206:213], 0
	v_mfma_f32_16x16x128_f8f6f4 v[72:75], v[24:31], v[206:213], 0
	v_mfma_f32_16x16x128_f8f6f4 v[68:71], v[16:23], v[214:221], 0
	v_mfma_f32_16x16x128_f8f6f4 v[64:67], v[24:31], v[214:221], 0
	s_setprio 0
	s_setprio 1
	v_mfma_f32_16x16x128_f8f6f4 v[60:63], v[0:7], v[190:197], 0
	v_mfma_f32_16x16x128_f8f6f4 v[56:59], v[8:15], v[190:197], 0
	v_mfma_f32_16x16x128_f8f6f4 v[52:55], v[0:7], v[198:205], 0
	v_mfma_f32_16x16x128_f8f6f4 v[48:51], v[8:15], v[198:205], 0
	v_mfma_f32_16x16x128_f8f6f4 v[44:47], v[0:7], v[206:213], 0
	v_mfma_f32_16x16x128_f8f6f4 v[40:43], v[8:15], v[206:213], 0
	v_mfma_f32_16x16x128_f8f6f4 v[36:39], v[0:7], v[214:221], 0
	v_mfma_f32_16x16x128_f8f6f4 v[32:35], v[8:15], v[214:221], 0
	s_setprio 0
	s_barrier
	s_add_i32 s86, 0, 0x18000
	s_add_i32 s88, 0, 0x1c000
	v_add_u32_e32 v189, s86, v185
	v_add_u32_e32 v190, s88, v185
	ds_read_b128 v[16:19], v189
	ds_read_b128 v[20:23], v189 offset:1024
	ds_read_b128 v[24:27], v189 offset:2048
	ds_read_b128 v[28:31], v189 offset:3072
	ds_read_b128 v[0:3], v190
	ds_read_b128 v[4:7], v190 offset:1024
	ds_read_b128 v[8:11], v190 offset:2048
	ds_read_b128 v[12:15], v190 offset:3072
	s_add_u32 s40, s36, 0x70100
	s_addc_u32 s41, s37, 0
	s_mov_b32 m0, s61
	v_lshl_add_u64 v[224:225], s[40:41], 0, v[160:161]
	ds_read_b128 v[192:195], v186 offset:32768
	ds_read_b128 v[196:199], v186 offset:33792
	ds_read_b128 v[200:203], v186 offset:34816
	ds_read_b128 v[204:207], v186 offset:35840
	ds_read_b128 v[208:211], v186 offset:36864
	ds_read_b128 v[212:215], v186 offset:37888
	ds_read_b128 v[216:219], v186 offset:38912
	ds_read_b128 v[220:223], v186 offset:39936
	global_load_lds_dwordx4 v[224:225], off
	v_lshl_add_u64 v[224:225], s[40:41], 0, v[164:165]
	s_mov_b32 m0, s62
	s_nop 0
	global_load_lds_dwordx4 v[224:225], off
	s_waitcnt vmcnt(8)
	s_waitcnt lgkmcnt(0)
	s_barrier
; #define PG8_STAGE(bufoff, gbase, voff) do { _Pragma("unroll") for (int _i = 0; _i < 2; ++_i) \
;         __builtin_amdgcn_global_load_lds((const unsigned*)((const char*)(gbase) + (voff)[_i]), (PG8_LAS unsigned*)(lds + (bufoff) + ldsw + _i * 8192), 16, 0, 0); } while (0)
; #define PG8_WAIT_V(n) asm volatile("s_waitcnt vmcnt(" #n ")" ::: "memory")
; #define PG8_WAIT_L(n) asm volatile("s_waitcnt lgkmcnt(" #n ")" ::: "memory")
; #define PG8_BAR __builtin_amdgcn_s_barrier()
; #define PG8_SCHED __builtin_amdgcn_sched_barrier(0)
; template <class Epi, class Sched, bool ALIGN_EPI = false, bool SP2 = false, bool FP8 = false, bool PEEL = false>
; __device__ __forceinline__ void gemm_phase(PG8_LAS unsigned char* lds, const Gemm g, const Sched& S, const Epi& E, const int wid) {
;     ...
;             PG8_WAIT_V(8); PG8_WAIT_L(0); PG8_BAR; PG8_MMA(0, 0, At, B0); PG8_MMA(0, 1, At, B1); PG8_BAR; PG8_SCHED;
;             PG8_LDA(At, 1, 1); PG8_STAGE(PG8_SB(1, 0), b3, voffB); PG8_STAGE(PG8_SB(1, 1), b3 + hstep, voffB); PG8_STAGE(PG8_SA(1, 0), a3, voffA);
;             PG8_WAIT_V(8); PG8_WAIT_L(0); PG8_BAR; PG8_MMA(1, 0, At, B0); PG8_MMA(1, 1, At, B1); PG8_BAR; PG8_SCHED;
;     ...
;             PG8_LDB(B0, 0, 0); PG8_LDB(B1, 0, 1); PG8_SCHED; PG8_LDA(At, 0, 0); PG8_STAGE(PG8_SA(1, 1), a1 + hstep, voffA);
;             PG8_WAIT_V(8); PG8_WAIT_L(0); PG8_BAR; PG8_MMA(0, 0, At, B0); PG8_MMA(0, 1, At, B1); PG8_BAR; PG8_SCHED;
	s_setprio 1
	v_mfma_f32_16x16x128_f8f6f4 v[156:159], v[16:23], v[192:199], v[156:159]
	v_mfma_f32_16x16x128_f8f6f4 v[152:155], v[24:31], v[192:199], v[152:155]
	v_mfma_f32_16x16x128_f8f6f4 v[148:151], v[16:23], v[200:207], v[148:151]
	v_mfma_f32_16x16x128_f8f6f4 v[144:147], v[24:31], v[200:207], v[144:147]
	v_mfma_f32_16x16x128_f8f6f4 v[140:143], v[16:23], v[208:215], v[140:143]
	v_mfma_f32_16x16x128_f8f6f4 v[136:139], v[24:31], v[208:215], v[136:139]
	v_mfma_f32_16x16x128_f8f6f4 v[132:135], v[16:23], v[216:223], v[132:135]
	v_mfma_f32_16x16x128_f8f6f4 v[128:131], v[24:31], v[216:223], v[128:131]
	s_setprio 0
	s_setprio 1
	v_mfma_f32_16x16x128_f8f6f4 v[124:127], v[0:7], v[192:199], v[124:127]
	v_mfma_f32_16x16x128_f8f6f4 v[120:123], v[8:15], v[192:199], v[120:123]
	v_mfma_f32_16x16x128_f8f6f4 v[116:119], v[0:7], v[200:207], v[116:119]
	v_mfma_f32_16x16x128_f8f6f4 v[112:115], v[8:15], v[200:207], v[112:115]
	v_mfma_f32_16x16x128_f8f6f4 v[108:111], v[0:7], v[208:215], v[108:111]
	v_mfma_f32_16x16x128_f8f6f4 v[104:107], v[8:15], v[208:215], v[104:107]
	v_mfma_f32_16x16x128_f8f6f4 v[100:103], v[0:7], v[216:223], v[100:103]
	v_mfma_f32_16x16x128_f8f6f4 v[96:99], v[8:15], v[216:223], v[96:99]
	s_setprio 0
	s_barrier
	s_add_i32 s86, s86, s54
	s_add_i32 s87, s86, 0x2000
	v_lshl_add_u64 v[176:177], v[176:177], 0, s[26:27]
	s_mov_b32 m0, s86
	s_add_u32 s40, s38, 0x70180
	ds_read_b128 v[192:195], v186 offset:49152
	ds_read_b128 v[196:199], v186 offset:50176
	ds_read_b128 v[200:203], v186 offset:51200
	ds_read_b128 v[204:207], v186 offset:52224
	ds_read_b128 v[208:211], v186 offset:53248
	ds_read_b128 v[212:215], v186 offset:54272
	ds_read_b128 v[216:219], v186 offset:55296
	ds_read_b128 v[220:223], v186 offset:56320
	global_load_lds_dwordx4 v[176:177], off
	v_lshl_add_u64 v[176:177], v[178:179], 0, s[26:27]
	s_mov_b32 m0, s87
	s_addc_u32 s41, s39, 0
	s_add_i32 s88, s88, s54
	global_load_lds_dwordx4 v[176:177], off
	v_lshl_add_u64 v[176:177], s[40:41], 0, v[162:163]
	s_mov_b32 m0, s88
	s_add_i32 s89, s88, 0x2000
	global_load_lds_dwordx4 v[176:177], off
	v_lshl_add_u64 v[176:177], s[40:41], 0, v[166:167]
	s_mov_b32 m0, s89
	s_nop 0
	global_load_lds_dwordx4 v[176:177], off
	v_lshl_add_u64 v[176:177], v[180:181], 0, s[26:27]
	s_mov_b32 m0, s63
	s_nop 0
	global_load_lds_dwordx4 v[176:177], off
	v_lshl_add_u64 v[176:177], v[182:183], 0, s[26:27]
	s_mov_b32 m0, s64
	s_nop 0
	global_load_lds_dwordx4 v[176:177], off
	s_waitcnt vmcnt(8)
	s_waitcnt lgkmcnt(0)
	s_barrier
	s_setprio 1
	v_mfma_f32_16x16x128_f8f6f4 v[92:95], v[16:23], v[192:199], v[92:95]
	v_mfma_f32_16x16x128_f8f6f4 v[88:91], v[24:31], v[192:199], v[88:91]
	v_mfma_f32_16x16x128_f8f6f4 v[84:87], v[16:23], v[200:207], v[84:87]
	v_mfma_f32_16x16x128_f8f6f4 v[80:83], v[24:31], v[200:207], v[80:83]
	v_mfma_f32_16x16x128_f8f6f4 v[76:79], v[16:23], v[208:215], v[76:79]
	v_mfma_f32_16x16x128_f8f6f4 v[72:75], v[24:31], v[208:215], v[72:75]
	v_mfma_f32_16x16x128_f8f6f4 v[68:71], v[16:23], v[216:223], v[68:71]
	v_mfma_f32_16x16x128_f8f6f4 v[64:67], v[24:31], v[216:223], v[64:67]
	s_setprio 0
	s_setprio 1
	v_mfma_f32_16x16x128_f8f6f4 v[60:63], v[0:7], v[192:199], v[60:63]
	v_mfma_f32_16x16x128_f8f6f4 v[56:59], v[8:15], v[192:199], v[56:59]
	v_mfma_f32_16x16x128_f8f6f4 v[52:55], v[0:7], v[200:207], v[52:55]
	v_mfma_f32_16x16x128_f8f6f4 v[48:51], v[8:15], v[200:207], v[48:51]
	v_mfma_f32_16x16x128_f8f6f4 v[44:47], v[0:7], v[208:215], v[44:47]
	v_mfma_f32_16x16x128_f8f6f4 v[40:43], v[8:15], v[208:215], v[40:43]
	v_mfma_f32_16x16x128_f8f6f4 v[36:39], v[0:7], v[216:223], v[36:39]
	v_mfma_f32_16x16x128_f8f6f4 v[32:35], v[8:15], v[216:223], v[32:35]
	s_setprio 0
	s_barrier
	s_add_u32 s90, s38, 0x200
	s_addc_u32 s91, s39, 0
	s_mov_b32 s92, 0
.LBB0_1853:
	ds_read_b128 v[0:3], v187
	ds_read_b128 v[4:7], v187 offset:1024
	ds_read_b128 v[16:19], v187 offset:2048
	ds_read_b128 v[20:23], v187 offset:3072
	ds_read_b128 v[24:27], v188
	ds_read_b128 v[28:31], v188 offset:1024
	ds_read_b128 v[176:179], v188 offset:2048
	ds_read_b128 v[180:183], v188 offset:3072
	s_add_u32 s38, s36, 0x200
	s_addc_u32 s39, s37, 0
	s_cmp_eq_u32 s92, 24
	s_cselect_b32 s41, s9, s39
	s_cselect_b32 s40, s8, s38
	s_cselect_b32 s39, s35, s91
	s_cselect_b32 s38, s34, s90
	s_mov_b32 m0, s80
	v_lshl_add_u64 v[216:217], s[36:37], 0, v[170:171]
	ds_read_b128 v[8:11], v186
	ds_read_b128 v[12:15], v186 offset:1024
	ds_read_b128 v[192:195], v186 offset:2048
	ds_read_b128 v[196:199], v186 offset:3072
	ds_read_b128 v[200:203], v186 offset:4096
	ds_read_b128 v[204:207], v186 offset:5120
	ds_read_b128 v[208:211], v186 offset:6144
	ds_read_b128 v[212:215], v186 offset:7168
	global_load_lds_dwordx4 v[216:217], off
	v_lshl_add_u64 v[216:217], s[36:37], 0, v[172:173]
	s_mov_b32 m0, s81
	s_nop 0
	global_load_lds_dwordx4 v[216:217], off
	s_waitcnt vmcnt(8)
	s_waitcnt lgkmcnt(0)
	s_barrier
	s_setprio 1
	v_mfma_f32_16x16x128_f8f6f4 v[156:159], v[0:7], v[8:15], v[156:159]
	v_mfma_f32_16x16x128_f8f6f4 v[152:155], v[16:23], v[8:15], v[152:155]
	v_mfma_f32_16x16x128_f8f6f4 v[148:151], v[0:7], v[192:199], v[148:151]
	v_mfma_f32_16x16x128_f8f6f4 v[144:147], v[16:23], v[192:199], v[144:147]
	v_mfma_f32_16x16x128_f8f6f4 v[140:143], v[0:7], v[200:207], v[140:143]
	v_mfma_f32_16x16x128_f8f6f4 v[136:139], v[16:23], v[200:207], v[136:139]
	v_mfma_f32_16x16x128_f8f6f4 v[132:135], v[0:7], v[208:215], v[132:135]
	v_mfma_f32_16x16x128_f8f6f4 v[128:131], v[16:23], v[208:215], v[128:131]
	s_setprio 0
	s_setprio 1
	v_mfma_f32_16x16x128_f8f6f4 v[124:127], v[24:31], v[8:15], v[124:127]
	v_mfma_f32_16x16x128_f8f6f4 v[120:123], v[176:183], v[8:15], v[120:123]
	v_mfma_f32_16x16x128_f8f6f4 v[116:119], v[24:31], v[192:199], v[116:119]
	v_mfma_f32_16x16x128_f8f6f4 v[112:115], v[176:183], v[192:199], v[112:115]
	v_mfma_f32_16x16x128_f8f6f4 v[108:111], v[24:31], v[200:207], v[108:111]
	v_mfma_f32_16x16x128_f8f6f4 v[104:107], v[176:183], v[200:207], v[104:107]
	v_mfma_f32_16x16x128_f8f6f4 v[100:103], v[24:31], v[208:215], v[100:103]
	v_mfma_f32_16x16x128_f8f6f4 v[96:99], v[176:183], v[208:215], v[96:99]
	s_setprio 0
	s_barrier
; #define PG8_STAGE(bufoff, gbase, voff) do { _Pragma("unroll") for (int _i = 0; _i < 2; ++_i) \
;         __builtin_amdgcn_global_load_lds((const unsigned*)((const char*)(gbase) + (voff)[_i]), (PG8_LAS unsigned*)(lds + (bufoff) + ldsw + _i * 8192), 16, 0, 0); } while (0)
; #define PG8_WAIT_V(n) asm volatile("s_waitcnt vmcnt(" #n ")" ::: "memory")
; #define PG8_WAIT_L(n) asm volatile("s_waitcnt lgkmcnt(" #n ")" ::: "memory")
; #define PG8_BAR __builtin_amdgcn_s_barrier()
; #define PG8_SCHED __builtin_amdgcn_sched_barrier(0)
; template <class Epi, class Sched, bool ALIGN_EPI = false, bool SP2 = false, bool FP8 = false, bool PEEL = false>
; __device__ __forceinline__ void gemm_phase(PG8_LAS unsigned char* lds, const Gemm g, const Sched& S, const Epi& E, const int wid) {
;     ...
;             PG8_LDA(At, 0, 1); PG8_STAGE(PG8_SB(0, 0), b2, voffB); PG8_STAGE(PG8_SB(0, 1), b2 + hstep, voffB); PG8_STAGE(PG8_SA(0, 0), a2, voffA);
;             PG8_WAIT_V(8); PG8_WAIT_L(0); PG8_BAR; PG8_MMA(1, 0, At, B0); PG8_MMA(1, 1, At, B1); PG8_BAR; PG8_SCHED;
;             PG8_LDB(B0, 1, 0); PG8_LDB(B1, 1, 1); PG8_SCHED; PG8_LDA(At, 1, 0); PG8_STAGE(PG8_SA(0, 1), a2 + hstep, voffA);
	s_mov_b32 m0, s82
	v_lshl_add_u64 v[8:9], s[38:39], 0, v[162:163]
	s_add_u32 s94, s38, 0x70000
	ds_read_b128 v[192:195], v186 offset:16384
	ds_read_b128 v[196:199], v186 offset:17408
	ds_read_b128 v[200:203], v186 offset:18432
	ds_read_b128 v[204:207], v186 offset:19456
	ds_read_b128 v[208:211], v186 offset:20480
	ds_read_b128 v[212:215], v186 offset:21504
	ds_read_b128 v[216:219], v186 offset:22528
	ds_read_b128 v[220:223], v186 offset:23552
	global_load_lds_dwordx4 v[8:9], off
	v_lshl_add_u64 v[10:11], s[38:39], 0, v[166:167]
	s_mov_b32 m0, s83
	s_addc_u32 s95, s39, 0
	global_load_lds_dwordx4 v[10:11], off
	v_lshl_add_u64 v[12:13], s[94:95], 0, v[162:163]
	s_mov_b32 m0, s84
	v_lshl_add_u64 v[14:15], s[40:41], 0, v[164:165]
	global_load_lds_dwordx4 v[12:13], off
	v_lshl_add_u64 v[12:13], s[94:95], 0, v[166:167]
	s_mov_b32 m0, s85
	s_nop 0
	global_load_lds_dwordx4 v[12:13], off
	v_lshl_add_u64 v[12:13], s[40:41], 0, v[160:161]
	s_mov_b32 m0, s59
	s_nop 0
	global_load_lds_dwordx4 v[12:13], off
	s_mov_b32 m0, s60
	s_nop 0
	global_load_lds_dwordx4 v[14:15], off
	s_waitcnt vmcnt(8)
	s_waitcnt lgkmcnt(0)
	s_barrier
	s_setprio 1
	v_mfma_f32_16x16x128_f8f6f4 v[92:95], v[0:7], v[192:199], v[92:95]
	v_mfma_f32_16x16x128_f8f6f4 v[88:91], v[16:23], v[192:199], v[88:91]
	v_mfma_f32_16x16x128_f8f6f4 v[84:87], v[0:7], v[200:207], v[84:87]
	v_mfma_f32_16x16x128_f8f6f4 v[80:83], v[16:23], v[200:207], v[80:83]
	v_mfma_f32_16x16x128_f8f6f4 v[76:79], v[0:7], v[208:215], v[76:79]
	v_mfma_f32_16x16x128_f8f6f4 v[72:75], v[16:23], v[208:215], v[72:75]
	v_mfma_f32_16x16x128_f8f6f4 v[68:71], v[0:7], v[216:223], v[68:71]
	v_mfma_f32_16x16x128_f8f6f4 v[64:67], v[16:23], v[216:223], v[64:67]
	s_setprio 0
	s_setprio 1
	v_mfma_f32_16x16x128_f8f6f4 v[60:63], v[24:31], v[192:199], v[60:63]
	v_mfma_f32_16x16x128_f8f6f4 v[56:59], v[176:183], v[192:199], v[56:59]
	v_mfma_f32_16x16x128_f8f6f4 v[52:55], v[24:31], v[200:207], v[52:55]
	v_mfma_f32_16x16x128_f8f6f4 v[48:51], v[176:183], v[200:207], v[48:51]
	v_mfma_f32_16x16x128_f8f6f4 v[44:47], v[24:31], v[208:215], v[44:47]
	v_mfma_f32_16x16x128_f8f6f4 v[40:43], v[176:183], v[208:215], v[40:43]
	v_mfma_f32_16x16x128_f8f6f4 v[36:39], v[24:31], v[216:223], v[36:39]
	v_mfma_f32_16x16x128_f8f6f4 v[32:35], v[176:183], v[216:223], v[32:35]
	s_setprio 0
	s_barrier
	ds_read_b128 v[16:19], v189
	ds_read_b128 v[20:23], v189 offset:1024
	ds_read_b128 v[24:27], v189 offset:2048
	ds_read_b128 v[28:31], v189 offset:3072
	ds_read_b128 v[0:3], v190
	ds_read_b128 v[4:7], v190 offset:1024
	ds_read_b128 v[176:179], v190 offset:2048
	ds_read_b128 v[180:183], v190 offset:3072
	s_add_u32 s40, s40, 0x70000
	s_addc_u32 s41, s41, 0
	s_mov_b32 m0, s61
	v_lshl_add_u64 v[224:225], s[40:41], 0, v[160:161]
	ds_read_b128 v[192:195], v186 offset:32768
	ds_read_b128 v[196:199], v186 offset:33792
	ds_read_b128 v[200:203], v186 offset:34816
	ds_read_b128 v[204:207], v186 offset:35840
	ds_read_b128 v[208:211], v186 offset:36864
	ds_read_b128 v[212:215], v186 offset:37888
	ds_read_b128 v[216:219], v186 offset:38912
	ds_read_b128 v[220:223], v186 offset:39936
	global_load_lds_dwordx4 v[224:225], off
	v_lshl_add_u64 v[224:225], s[40:41], 0, v[164:165]
	s_mov_b32 m0, s62
	s_nop 0
	global_load_lds_dwordx4 v[224:225], off
	s_waitcnt vmcnt(8)
	s_waitcnt lgkmcnt(0)
	s_barrier
; #define PG8_STAGE(bufoff, gbase, voff) do { _Pragma("unroll") for (int _i = 0; _i < 2; ++_i) \
;         __builtin_amdgcn_global_load_lds((const unsigned*)((const char*)(gbase) + (voff)[_i]), (PG8_LAS unsigned*)(lds + (bufoff) + ldsw + _i * 8192), 16, 0, 0); } while (0)
; #define PG8_WAIT_V(n) asm volatile("s_waitcnt vmcnt(" #n ")" ::: "memory")
; #define PG8_WAIT_L(n) asm volatile("s_waitcnt lgkmcnt(" #n ")" ::: "memory")
; #define PG8_BAR __builtin_amdgcn_s_barrier()
; #define PG8_SCHED __builtin_amdgcn_sched_barrier(0)
; template <class Epi, class Sched, bool ALIGN_EPI = false, bool SP2 = false, bool FP8 = false, bool PEEL = false>
; __device__ __forceinline__ void gemm_phase(PG8_LAS unsigned char* lds, const Gemm g, const Sched& S, const Epi& E, const int wid) {
;     ...
;             PG8_LDB(B0, 1, 0); PG8_LDB(B1, 1, 1); PG8_SCHED; PG8_LDA(At, 1, 0); PG8_STAGE(PG8_SA(0, 1), a2 + hstep, voffA);
;             PG8_WAIT_V(8); PG8_WAIT_L(0); PG8_BAR; PG8_MMA(0, 0, At, B0); PG8_MMA(0, 1, At, B1); PG8_BAR; PG8_SCHED;
;             PG8_LDA(At, 1, 1); PG8_STAGE(PG8_SB(1, 0), b3, voffB); PG8_STAGE(PG8_SB(1, 1), b3 + hstep, voffB); PG8_STAGE(PG8_SA(1, 0), a3, voffA);
;             PG8_WAIT_V(8); PG8_WAIT_L(0); PG8_BAR; PG8_MMA(1, 0, At, B0); PG8_MMA(1, 1, At, B1); PG8_BAR; PG8_SCHED;
;     ...
;         if constexpr (ALIGN_EPI) { if (wr == 0) PG8_BAR; }
	s_setprio 1
	v_mfma_f32_16x16x128_f8f6f4 v[156:159], v[16:23], v[192:199], v[156:159]
	v_mfma_f32_16x16x128_f8f6f4 v[152:155], v[24:31], v[192:199], v[152:155]
	v_mfma_f32_16x16x128_f8f6f4 v[148:151], v[16:23], v[200:207], v[148:151]
	v_mfma_f32_16x16x128_f8f6f4 v[144:147], v[24:31], v[200:207], v[144:147]
	v_mfma_f32_16x16x128_f8f6f4 v[140:143], v[16:23], v[208:215], v[140:143]
	v_mfma_f32_16x16x128_f8f6f4 v[136:139], v[24:31], v[208:215], v[136:139]
	v_mfma_f32_16x16x128_f8f6f4 v[132:135], v[16:23], v[216:223], v[132:135]
	v_mfma_f32_16x16x128_f8f6f4 v[128:131], v[24:31], v[216:223], v[128:131]
	s_setprio 0
	s_setprio 1
	v_mfma_f32_16x16x128_f8f6f4 v[124:127], v[0:7], v[192:199], v[124:127]
	v_mfma_f32_16x16x128_f8f6f4 v[120:123], v[176:183], v[192:199], v[120:123]
	v_mfma_f32_16x16x128_f8f6f4 v[116:119], v[0:7], v[200:207], v[116:119]
	v_mfma_f32_16x16x128_f8f6f4 v[112:115], v[176:183], v[200:207], v[112:115]
	v_mfma_f32_16x16x128_f8f6f4 v[108:111], v[0:7], v[208:215], v[108:111]
	v_mfma_f32_16x16x128_f8f6f4 v[104:107], v[176:183], v[208:215], v[104:107]
	v_mfma_f32_16x16x128_f8f6f4 v[100:103], v[0:7], v[216:223], v[100:103]
	v_mfma_f32_16x16x128_f8f6f4 v[96:99], v[176:183], v[216:223], v[96:99]
	s_setprio 0
	s_barrier
	s_mov_b32 m0, s86
	v_lshl_add_u64 v[8:9], v[8:9], 0, s[22:23]
	s_add_u32 s38, s38, 0x70080
	ds_read_b128 v[192:195], v186 offset:49152
	ds_read_b128 v[196:199], v186 offset:50176
	ds_read_b128 v[200:203], v186 offset:51200
	ds_read_b128 v[204:207], v186 offset:52224
	ds_read_b128 v[208:211], v186 offset:53248
	ds_read_b128 v[212:215], v186 offset:54272
	ds_read_b128 v[216:219], v186 offset:55296
	ds_read_b128 v[220:223], v186 offset:56320
	global_load_lds_dwordx4 v[8:9], off
	v_lshl_add_u64 v[8:9], v[10:11], 0, s[22:23]
	s_mov_b32 m0, s87
	s_addc_u32 s39, s39, 0
	global_load_lds_dwordx4 v[8:9], off
	v_lshl_add_u64 v[8:9], s[38:39], 0, v[162:163]
	s_mov_b32 m0, s88
	s_nop 0
	global_load_lds_dwordx4 v[8:9], off
	v_lshl_add_u64 v[8:9], s[38:39], 0, v[166:167]
	s_mov_b32 m0, s89
	s_nop 0
	global_load_lds_dwordx4 v[8:9], off
	v_lshl_add_u64 v[8:9], v[12:13], 0, s[22:23]
	s_mov_b32 m0, s63
	s_nop 0
	global_load_lds_dwordx4 v[8:9], off
	v_lshl_add_u64 v[8:9], v[14:15], 0, s[22:23]
	s_mov_b32 m0, s64
	s_nop 0
	global_load_lds_dwordx4 v[8:9], off
	s_waitcnt vmcnt(8)
	s_waitcnt lgkmcnt(0)
	s_barrier
	s_setprio 1
	v_mfma_f32_16x16x128_f8f6f4 v[92:95], v[16:23], v[192:199], v[92:95]
	v_mfma_f32_16x16x128_f8f6f4 v[88:91], v[24:31], v[192:199], v[88:91]
	v_mfma_f32_16x16x128_f8f6f4 v[84:87], v[16:23], v[200:207], v[84:87]
	v_mfma_f32_16x16x128_f8f6f4 v[80:83], v[24:31], v[200:207], v[80:83]
	v_mfma_f32_16x16x128_f8f6f4 v[76:79], v[16:23], v[208:215], v[76:79]
	v_mfma_f32_16x16x128_f8f6f4 v[72:75], v[24:31], v[208:215], v[72:75]
	v_mfma_f32_16x16x128_f8f6f4 v[68:71], v[16:23], v[216:223], v[68:71]
	v_mfma_f32_16x16x128_f8f6f4 v[64:67], v[24:31], v[216:223], v[64:67]
	s_setprio 0
	s_setprio 1
	v_mfma_f32_16x16x128_f8f6f4 v[60:63], v[0:7], v[192:199], v[60:63]
	v_mfma_f32_16x16x128_f8f6f4 v[56:59], v[176:183], v[192:199], v[56:59]
	v_mfma_f32_16x16x128_f8f6f4 v[52:55], v[0:7], v[200:207], v[52:55]
	v_mfma_f32_16x16x128_f8f6f4 v[48:51], v[176:183], v[200:207], v[48:51]
	v_mfma_f32_16x16x128_f8f6f4 v[44:47], v[0:7], v[208:215], v[44:47]
	v_mfma_f32_16x16x128_f8f6f4 v[40:43], v[176:183], v[208:215], v[40:43]
	v_mfma_f32_16x16x128_f8f6f4 v[36:39], v[0:7], v[216:223], v[36:39]
	v_mfma_f32_16x16x128_f8f6f4 v[32:35], v[176:183], v[216:223], v[32:35]
	s_setprio 0
	s_barrier
	s_add_i32 s92, s92, 2
	s_add_u32 s36, s36, 0x100
	s_addc_u32 s37, s37, 0
	s_add_u32 s90, s90, 0x100
	s_addc_u32 s91, s91, 0
	s_cmp_gt_u32 s92, 25
	s_cbranch_scc0 .LBB0_1853
	s_and_b64 vcc, exec, s[12:13]
	s_cbranch_vccz .LBB0_1856
	s_barrier

; #define PG8_STAGE(bufoff, gbase, voff) do { _Pragma("unroll") for (int _i = 0; _i < 2; ++_i) \
;         __builtin_amdgcn_global_load_lds((const unsigned*)((const char*)(gbase) + (voff)[_i]), (PG8_LAS unsigned*)(lds + (bufoff) + ldsw + _i * 8192), 16, 0, 0); } while (0)
; #define PG8_WAIT_V(n) asm volatile("s_waitcnt vmcnt(" #n ")" ::: "memory")
; #define PG8_WAIT_L(n) asm volatile("s_waitcnt lgkmcnt(" #n ")" ::: "memory")
; #define PG8_BAR __builtin_amdgcn_s_barrier()
; #define PG8_SCHED __builtin_amdgcn_sched_barrier(0)
; template <class Epi, class Sched, bool ALIGN_EPI = false, bool SP2 = false, bool FP8 = false, bool PEEL = false>
; __device__ __forceinline__ void gemm_phase(PG8_LAS unsigned char* lds, const Gemm g, const Sched& S, const Epi& E, const int wid) {
;     ...
;             PG8_LDB(B0, 0, 0); PG8_LDB(B1, 0, 1); PG8_SCHED; PG8_LDA(At, 0, 0); PG8_STAGE(PG8_SA(1, 1), a1 + hstep, voffA);
;             PG8_WAIT_V(8); PG8_WAIT_L(0); PG8_BAR; PG8_MMA(0, 0, At, B0); PG8_MMA(0, 1, At, B1); PG8_BAR; PG8_SCHED;
;             PG8_LDA(At, 0, 1); PG8_STAGE(PG8_SB(0, 0), b2, voffB); PG8_STAGE(PG8_SB(0, 1), b2 + hstep, voffB); PG8_STAGE(PG8_SA(0, 0), a2, voffA);
;             PG8_WAIT_V(8); PG8_WAIT_L(0); PG8_BAR; PG8_MMA(1, 0, At, B0); PG8_MMA(1, 1, At, B1); PG8_BAR; PG8_SCHED;
.LBB0_1873:
	s_add_u32 s25, s26, s42
	s_addc_u32 s37, s27, s43
	s_add_u32 s46, s25, 0x100
	s_addc_u32 s47, s37, 0
	s_and_b64 s[44:45], s[40:41], exec
	s_cselect_b32 s45, s9, s47
	s_cselect_b32 s44, s8, s46
	s_add_u32 s42, s34, s42
	s_addc_u32 s43, s35, s43
	s_add_u32 s42, s42, 0x100
	s_addc_u32 s43, s43, 0
	s_and_b64 s[40:41], s[40:41], exec
	s_cselect_b32 s47, s31, s43
	s_cselect_b32 s46, s30, s42
	s_add_u32 s50, s25, 0x70080
	ds_read_b128 v[16:19], v183
	ds_read_b128 v[20:23], v183 offset:1024
	ds_read_b128 v[24:27], v183 offset:2048
	ds_read_b128 v[28:31], v183 offset:3072
	ds_read_b128 v[0:3], v184
	ds_read_b128 v[4:7], v184 offset:1024
	ds_read_b128 v[8:11], v184 offset:2048
	ds_read_b128 v[12:15], v184 offset:3072
	s_addc_u32 s51, s37, 0
	s_add_i32 s92, s67, s54
	s_add_i32 m0, s59, 0xc000
	s_add_i32 s93, s59, 0xe000
	s_add_i32 s89, s92, 0x2000
	s_add_u32 s48, s46, 0x70000
	s_addc_u32 s49, s47, 0
	s_add_i32 s91, s74, s54
	s_add_i32 s90, s91, 0x2000
	s_add_i32 s88, 0, 0x18000
	s_add_i32 s87, 0, 0x1c000
	s_add_u32 s42, s44, 0x70000
	s_addc_u32 s43, s45, 0
	s_add_i32 s86, s88, s54
	s_add_i32 s37, s86, 0x2000
	s_add_u32 s40, s46, 0x70080
	s_addc_u32 s41, s47, 0
	s_add_i32 s85, s87, s54
	s_add_i32 s25, s85, 0x2000
	v_lshl_add_u64 v[210:211], s[50:51], 0, v[166:167]
	ds_read_b128 v[174:177], v185
	ds_read_b128 v[178:181], v185 offset:1024
	ds_read_b128 v[186:189], v185 offset:2048
	ds_read_b128 v[190:193], v185 offset:3072
	ds_read_b128 v[194:197], v185 offset:4096
	ds_read_b128 v[198:201], v185 offset:5120
	ds_read_b128 v[202:205], v185 offset:6144
	ds_read_b128 v[206:209], v185 offset:7168
	global_load_lds_dwordx4 v[210:211], off
	v_lshl_add_u64 v[210:211], s[50:51], 0, v[162:163]
	s_mov_b32 m0, s93
	s_nop 0
	global_load_lds_dwordx4 v[210:211], off
	s_waitcnt vmcnt(8)
	s_waitcnt lgkmcnt(0)
	s_barrier
	s_setprio 1
	v_mfma_f32_16x16x128_f8f6f4 v[156:159], v[16:23], v[174:181], v[156:159]
	v_mfma_f32_16x16x128_f8f6f4 v[152:155], v[24:31], v[174:181], v[152:155]
	v_mfma_f32_16x16x128_f8f6f4 v[148:151], v[16:23], v[186:193], v[148:151]
	v_mfma_f32_16x16x128_f8f6f4 v[140:143], v[24:31], v[186:193], v[140:143]
	v_mfma_f32_16x16x128_f8f6f4 v[132:135], v[16:23], v[194:201], v[132:135]
	v_mfma_f32_16x16x128_f8f6f4 v[124:127], v[24:31], v[194:201], v[124:127]
	v_mfma_f32_16x16x128_f8f6f4 v[116:119], v[16:23], v[202:209], v[116:119]
	v_mfma_f32_16x16x128_f8f6f4 v[108:111], v[24:31], v[202:209], v[108:111]
	s_setprio 0
	s_setprio 1
	v_mfma_f32_16x16x128_f8f6f4 v[144:147], v[0:7], v[174:181], v[144:147]
	v_mfma_f32_16x16x128_f8f6f4 v[136:139], v[8:15], v[174:181], v[136:139]
	v_mfma_f32_16x16x128_f8f6f4 v[128:131], v[0:7], v[186:193], v[128:131]
	v_mfma_f32_16x16x128_f8f6f4 v[120:123], v[8:15], v[186:193], v[120:123]
	v_mfma_f32_16x16x128_f8f6f4 v[112:115], v[0:7], v[194:201], v[112:115]
	v_mfma_f32_16x16x128_f8f6f4 v[104:107], v[8:15], v[194:201], v[104:107]
	v_mfma_f32_16x16x128_f8f6f4 v[100:103], v[0:7], v[202:209], v[100:103]
	v_mfma_f32_16x16x128_f8f6f4 v[96:99], v[8:15], v[202:209], v[96:99]
	s_setprio 0
	s_barrier
	s_mov_b32 m0, s92
	v_lshl_add_u64 v[174:175], s[46:47], 0, v[164:165]
	ds_read_b128 v[186:189], v185 offset:16384
	ds_read_b128 v[190:193], v185 offset:17408
	ds_read_b128 v[194:197], v185 offset:18432
	ds_read_b128 v[198:201], v185 offset:19456
	ds_read_b128 v[202:205], v185 offset:20480
	ds_read_b128 v[206:209], v185 offset:21504
	ds_read_b128 v[210:213], v185 offset:22528
	ds_read_b128 v[214:217], v185 offset:23552
	global_load_lds_dwordx4 v[174:175], off
	v_lshl_add_u64 v[176:177], s[46:47], 0, v[160:161]
	s_mov_b32 m0, s89
	v_lshl_add_u64 v[178:179], s[48:49], 0, v[164:165]
	global_load_lds_dwordx4 v[176:177], off
	s_mov_b32 m0, s91
	v_lshl_add_u64 v[180:181], s[44:45], 0, v[162:163]
	global_load_lds_dwordx4 v[178:179], off
	v_lshl_add_u64 v[178:179], s[48:49], 0, v[160:161]
	s_mov_b32 m0, s90
	s_nop 0
	global_load_lds_dwordx4 v[178:179], off
	v_lshl_add_u64 v[178:179], s[44:45], 0, v[166:167]
	s_mov_b32 m0, s59
	s_nop 0
	global_load_lds_dwordx4 v[178:179], off
	s_mov_b32 m0, s60
	s_nop 0
	global_load_lds_dwordx4 v[180:181], off
	s_waitcnt vmcnt(8)
	s_waitcnt lgkmcnt(0)
	s_barrier
	s_setprio 1
	v_mfma_f32_16x16x128_f8f6f4 v[92:95], v[16:23], v[186:193], v[92:95]
	v_mfma_f32_16x16x128_f8f6f4 v[88:91], v[24:31], v[186:193], v[88:91]
	v_mfma_f32_16x16x128_f8f6f4 v[84:87], v[16:23], v[194:201], v[84:87]
	v_mfma_f32_16x16x128_f8f6f4 v[76:79], v[24:31], v[194:201], v[76:79]
	v_mfma_f32_16x16x128_f8f6f4 v[68:71], v[16:23], v[202:209], v[68:71]
	v_mfma_f32_16x16x128_f8f6f4 v[60:63], v[24:31], v[202:209], v[60:63]
	v_mfma_f32_16x16x128_f8f6f4 v[52:55], v[16:23], v[210:217], v[52:55]
	v_mfma_f32_16x16x128_f8f6f4 v[44:47], v[24:31], v[210:217], v[44:47]
	s_setprio 0
	s_setprio 1
	v_mfma_f32_16x16x128_f8f6f4 v[80:83], v[0:7], v[186:193], v[80:83]
	v_mfma_f32_16x16x128_f8f6f4 v[72:75], v[8:15], v[186:193], v[72:75]
	v_mfma_f32_16x16x128_f8f6f4 v[64:67], v[0:7], v[194:201], v[64:67]
	v_mfma_f32_16x16x128_f8f6f4 v[56:59], v[8:15], v[194:201], v[56:59]
	v_mfma_f32_16x16x128_f8f6f4 v[48:51], v[0:7], v[202:209], v[48:51]
	v_mfma_f32_16x16x128_f8f6f4 v[40:43], v[8:15], v[202:209], v[40:43]
	v_mfma_f32_16x16x128_f8f6f4 v[36:39], v[0:7], v[210:217], v[36:39]
	v_mfma_f32_16x16x128_f8f6f4 v[32:35], v[8:15], v[210:217], v[32:35]
	s_setprio 0
	s_barrier
; #define PG8_STAGE(bufoff, gbase, voff) do { _Pragma("unroll") for (int _i = 0; _i < 2; ++_i) \
;         __builtin_amdgcn_global_load_lds((const unsigned*)((const char*)(gbase) + (voff)[_i]), (PG8_LAS unsigned*)(lds + (bufoff) + ldsw + _i * 8192), 16, 0, 0); } while (0)
; #define PG8_WAIT_V(n) asm volatile("s_waitcnt vmcnt(" #n ")" ::: "memory")
; #define PG8_WAIT_L(n) asm volatile("s_waitcnt lgkmcnt(" #n ")" ::: "memory")
; #define PG8_BAR __builtin_amdgcn_s_barrier()
; #define PG8_SCHED __builtin_amdgcn_sched_barrier(0)
; template <class Epi, class Sched, bool ALIGN_EPI = false, bool SP2 = false, bool FP8 = false, bool PEEL = false>
; __device__ __forceinline__ void gemm_phase(PG8_LAS unsigned char* lds, const Gemm g, const Sched& S, const Epi& E, const int wid) {
;     ...
;             PG8_LDB(B0, 1, 0); PG8_LDB(B1, 1, 1); PG8_SCHED; PG8_LDA(At, 1, 0); PG8_STAGE(PG8_SA(0, 1), a2 + hstep, voffA);
;             PG8_WAIT_V(8); PG8_WAIT_L(0); PG8_BAR; PG8_MMA(0, 0, At, B0); PG8_MMA(0, 1, At, B1); PG8_BAR; PG8_SCHED;
;             PG8_LDA(At, 1, 1); PG8_STAGE(PG8_SB(1, 0), b3, voffB); PG8_STAGE(PG8_SB(1, 1), b3 + hstep, voffB); PG8_STAGE(PG8_SA(1, 0), a3, voffA);
;             PG8_WAIT_V(8); PG8_WAIT_L(0); PG8_BAR; PG8_MMA(1, 0, At, B0); PG8_MMA(1, 1, At, B1); PG8_BAR; PG8_SCHED;
	v_add_u32_e32 v12, s88, v182
	v_add_u32_e32 v28, s87, v182
	ds_read_b128 v[0:3], v12
	ds_read_b128 v[4:7], v12 offset:1024
	ds_read_b128 v[8:11], v12 offset:2048
	ds_read_b128 v[12:15], v12 offset:3072
	ds_read_b128 v[16:19], v28
	ds_read_b128 v[20:23], v28 offset:1024
	ds_read_b128 v[24:27], v28 offset:2048
	ds_read_b128 v[28:31], v28 offset:3072
	s_mov_b32 m0, s61
	v_lshl_add_u64 v[218:219], s[42:43], 0, v[166:167]
	ds_read_b128 v[186:189], v185 offset:32768
	ds_read_b128 v[190:193], v185 offset:33792
	ds_read_b128 v[194:197], v185 offset:34816
	ds_read_b128 v[198:201], v185 offset:35840
	ds_read_b128 v[202:205], v185 offset:36864
	ds_read_b128 v[206:209], v185 offset:37888
	ds_read_b128 v[210:213], v185 offset:38912
	ds_read_b128 v[214:217], v185 offset:39936
	global_load_lds_dwordx4 v[218:219], off
	v_lshl_add_u64 v[218:219], s[42:43], 0, v[162:163]
	s_mov_b32 m0, s62
	s_nop 0
	global_load_lds_dwordx4 v[218:219], off
	s_waitcnt vmcnt(8)
	s_waitcnt lgkmcnt(0)
	s_barrier
	s_setprio 1
	v_mfma_f32_16x16x128_f8f6f4 v[156:159], v[0:7], v[186:193], v[156:159]
	v_mfma_f32_16x16x128_f8f6f4 v[152:155], v[8:15], v[186:193], v[152:155]
	v_mfma_f32_16x16x128_f8f6f4 v[148:151], v[0:7], v[194:201], v[148:151]
	v_mfma_f32_16x16x128_f8f6f4 v[140:143], v[8:15], v[194:201], v[140:143]
	v_mfma_f32_16x16x128_f8f6f4 v[132:135], v[0:7], v[202:209], v[132:135]
	v_mfma_f32_16x16x128_f8f6f4 v[124:127], v[8:15], v[202:209], v[124:127]
	v_mfma_f32_16x16x128_f8f6f4 v[116:119], v[0:7], v[210:217], v[116:119]
	v_mfma_f32_16x16x128_f8f6f4 v[108:111], v[8:15], v[210:217], v[108:111]
	s_setprio 0
	s_setprio 1
	v_mfma_f32_16x16x128_f8f6f4 v[144:147], v[16:23], v[186:193], v[144:147]
	v_mfma_f32_16x16x128_f8f6f4 v[136:139], v[24:31], v[186:193], v[136:139]
	v_mfma_f32_16x16x128_f8f6f4 v[128:131], v[16:23], v[194:201], v[128:131]
	v_mfma_f32_16x16x128_f8f6f4 v[120:123], v[24:31], v[194:201], v[120:123]
	v_mfma_f32_16x16x128_f8f6f4 v[112:115], v[16:23], v[202:209], v[112:115]
	v_mfma_f32_16x16x128_f8f6f4 v[104:107], v[24:31], v[202:209], v[104:107]
	v_mfma_f32_16x16x128_f8f6f4 v[100:103], v[16:23], v[210:217], v[100:103]
	v_mfma_f32_16x16x128_f8f6f4 v[96:99], v[24:31], v[210:217], v[96:99]
	s_setprio 0
	s_barrier
	s_mov_b32 m0, s86
	v_lshl_add_u64 v[174:175], v[174:175], 0, s[14:15]
	ds_read_b128 v[186:189], v185 offset:49152
	ds_read_b128 v[190:193], v185 offset:50176
	ds_read_b128 v[194:197], v185 offset:51200
	ds_read_b128 v[198:201], v185 offset:52224
	ds_read_b128 v[202:205], v185 offset:53248
	ds_read_b128 v[206:209], v185 offset:54272
	ds_read_b128 v[210:213], v185 offset:55296
	ds_read_b128 v[214:217], v185 offset:56320
	global_load_lds_dwordx4 v[174:175], off
	v_lshl_add_u64 v[174:175], v[176:177], 0, s[14:15]
	s_mov_b32 m0, s37
	s_nop 0
	global_load_lds_dwordx4 v[174:175], off
	v_lshl_add_u64 v[174:175], s[40:41], 0, v[164:165]
	s_mov_b32 m0, s85
	s_nop 0
	global_load_lds_dwordx4 v[174:175], off
	v_lshl_add_u64 v[174:175], s[40:41], 0, v[160:161]
	s_mov_b32 m0, s25
	s_nop 0
	global_load_lds_dwordx4 v[174:175], off
	v_lshl_add_u64 v[174:175], v[178:179], 0, s[14:15]
	s_mov_b32 m0, s65
	s_nop 0
	global_load_lds_dwordx4 v[174:175], off
	v_lshl_add_u64 v[174:175], v[180:181], 0, s[14:15]
	s_mov_b32 m0, s66
	s_nop 0
	global_load_lds_dwordx4 v[174:175], off
	s_waitcnt vmcnt(8)
	s_waitcnt lgkmcnt(0)
	s_barrier
	s_setprio 1
	v_mfma_f32_16x16x128_f8f6f4 v[92:95], v[0:7], v[186:193], v[92:95]
	v_mfma_f32_16x16x128_f8f6f4 v[88:91], v[8:15], v[186:193], v[88:91]
	v_mfma_f32_16x16x128_f8f6f4 v[84:87], v[0:7], v[194:201], v[84:87]
	v_mfma_f32_16x16x128_f8f6f4 v[76:79], v[8:15], v[194:201], v[76:79]
	v_mfma_f32_16x16x128_f8f6f4 v[68:71], v[0:7], v[202:209], v[68:71]
	v_mfma_f32_16x16x128_f8f6f4 v[60:63], v[8:15], v[202:209], v[60:63]
	v_mfma_f32_16x16x128_f8f6f4 v[52:55], v[0:7], v[210:217], v[52:55]
	v_mfma_f32_16x16x128_f8f6f4 v[44:47], v[8:15], v[210:217], v[44:47]
	s_setprio 0
	s_setprio 1
	v_mfma_f32_16x16x128_f8f6f4 v[80:83], v[16:23], v[186:193], v[80:83]
	v_mfma_f32_16x16x128_f8f6f4 v[72:75], v[24:31], v[186:193], v[72:75]
	v_mfma_f32_16x16x128_f8f6f4 v[64:67], v[16:23], v[194:201], v[64:67]
	v_mfma_f32_16x16x128_f8f6f4 v[56:59], v[24:31], v[194:201], v[56:59]
	v_mfma_f32_16x16x128_f8f6f4 v[48:51], v[16:23], v[202:209], v[48:51]
	v_mfma_f32_16x16x128_f8f6f4 v[40:43], v[24:31], v[202:209], v[40:43]
	v_mfma_f32_16x16x128_f8f6f4 v[36:39], v[16:23], v[210:217], v[36:39]
	v_mfma_f32_16x16x128_f8f6f4 v[32:35], v[24:31], v[210:217], v[32:35]
	s_setprio 0
	s_barrier
	s_andn2_b64 vcc, exec, s[38:39]
	s_mov_b64 s[40:41], -1
	s_mov_b64 s[38:39], 0
	s_mov_b64 s[42:43], 0x100
	s_cbranch_vccz .LBB0_1873
	s_and_b64 vcc, exec, s[12:13]
	s_cbranch_vccz .LBB0_1876
	s_barrier
